# GEMM1 and attention output stores (16-byte) made write-through (sc1) so the XCD leaders' L2 write-back at the following barriers has little to flush
# baseline (speedup 1.0000x reference)
; __device__ __forceinline__ unsigned cvt_pk_bf16(float lo, float hi) { unsigned r; asm volatile("v_cvt_pk_bf16_f32 %0, %1, %2" : "=v"(r) : "v"(lo), "v"(hi)); return r; }
;     __device__ __forceinline__ void operator()(const f32x4 (&acc)[2][2][4][2], const Unit& u, int wr, int wc, int fr, int fq) const {
;     ...
;         } else {
;             unsigned char* base = wb + OFF_U + (unsigned)((pn - 6) * 128 + cl) * 2u;
; #pragma unroll
;             for (int ai = 0; ai < 2; ++ai)
; #pragma unroll
;                 for (int m = 0; m < 4; ++m) { unsigned char* rowp = base + (unsigned)((row0 + ai * HALF + m * 16) * 512) * 2u;
;                     float o[8];
; #pragma unroll
;                     for (int n = 0; n < 2; ++n)
; #pragma unroll
;                         for (int e = 0; e < 4; ++e) { const float a = acc[ai][0][m][n][e], g = acc[ai][1][m][n][e];
;                             o[4 * n + e] = a * __builtin_amdgcn_rcpf(1.0f + __builtin_amdgcn_exp2f(-1.4426950408889634f * g)); }
;                     u32x4 w; w.x = cvt_pk_bf16(o[0], o[1]); w.y = cvt_pk_bf16(o[2], o[3]); w.z = cvt_pk_bf16(o[4], o[5]); w.w = cvt_pk_bf16(o[6], o[7]);
;                     *(u32x4*)rowp = w; }
.LBB0_127:
	s_lshl_b32 s8, s14, 8
	s_mov_b64 s[46:47], s[10:11]
	v_mov_b32_e32 v128, v178
	s_add_i32 s8, s8, s70
	s_cmp_gt_i32 s48, 3
	v_add_u32_e32 v190, s8, v128
	s_mov_b64 s[8:9], -1
	v_lshlrev_b32_e32 v144, 10, v190
	s_cbranch_scc0 .LBB0_133
	s_cmp_gt_u32 s48, 5
	v_add_u32_e32 v158, 0x4000, v144
	v_add_u32_e32 v156, 0x8000, v144
	v_add_u32_e32 v154, 0xc000, v144
	v_add_u32_e32 v134, 0x20000, v144
	v_add_u32_e32 v132, 0x24000, v144
	v_add_u32_e32 v130, 0x28000, v144
	v_add_u32_e32 v128, 0x2c000, v144
	s_cbranch_scc0 .LBB0_130
	v_mul_f32_e32 v129, 0xbfb8aa3b, v116
	v_mul_f32_e32 v131, 0xbfb8aa3b, v117
	v_mul_f32_e32 v133, 0xbfb8aa3b, v118
	v_mul_f32_e32 v135, 0xbfb8aa3b, v119
	v_mul_f32_e32 v162, 0xbfb8aa3b, v115
	v_exp_f32_e32 v129, v129
	v_exp_f32_e32 v131, v131
	v_exp_f32_e32 v133, v133
	v_exp_f32_e32 v135, v135
	v_mul_f32_e32 v155, 0xbfb8aa3b, v112
	v_mul_f32_e32 v157, 0xbfb8aa3b, v113
	v_mul_f32_e32 v159, 0xbfb8aa3b, v114
	v_exp_f32_e32 v162, v162
	v_exp_f32_e32 v155, v155
	v_exp_f32_e32 v157, v157
	v_exp_f32_e32 v159, v159
	v_add_f32_e32 v129, 1.0, v129
	v_add_f32_e32 v131, 1.0, v131
	v_add_f32_e32 v133, 1.0, v133
	v_add_f32_e32 v135, 1.0, v135
	v_add_f32_e32 v162, 1.0, v162
	v_rcp_f32_e32 v129, v129
	v_rcp_f32_e32 v131, v131
	v_rcp_f32_e32 v133, v133
	v_rcp_f32_e32 v135, v135
	v_add_f32_e32 v155, 1.0, v155
	v_add_f32_e32 v157, 1.0, v157
	v_add_f32_e32 v159, 1.0, v159
	v_rcp_f32_e32 v162, v162
	v_lshl_add_u32 v160, s48, 8, v183
	v_mov_b32_e32 v161, v145
	v_rcp_f32_e32 v155, v155
	v_rcp_f32_e32 v157, v157
	v_rcp_f32_e32 v159, v159
	v_lshl_add_u64 v[160:161], s[46:47], 0, v[160:161]
	v_lshl_add_u64 v[160:161], v[160:161], 0, s[22:23]
	v_mul_f32_e32 v129, v124, v129
	v_mul_f32_e32 v131, v125, v131
	v_mul_f32_e32 v133, v126, v133
	v_mul_f32_e32 v135, v127, v135
	v_mul_f32_e32 v165, v123, v162
	v_lshl_add_u64 v[166:167], v[160:161], 0, v[144:145]
	v_cvt_pk_bf16_f32 v162, v129, v131
	v_cvt_pk_bf16_f32 v163, v133, v135
	v_mul_f32_e32 v155, v120, v155
	v_mul_f32_e32 v157, v121, v157
	v_mul_f32_e32 v159, v122, v159
	v_cvt_pk_bf16_f32 v164, v155, v157
	v_mul_f32_e32 v129, 0xbfb8aa3b, v100
	v_cvt_pk_bf16_f32 v165, v159, v165
	flat_store_dwordx4 v[166:167], v[162:165] sc1
	v_mul_f32_e32 v131, 0xbfb8aa3b, v101
	v_mul_f32_e32 v133, 0xbfb8aa3b, v102
	v_mul_f32_e32 v135, 0xbfb8aa3b, v103
	v_mul_f32_e32 v162, 0xbfb8aa3b, v98
	v_mul_f32_e32 v163, 0xbfb8aa3b, v99
	v_exp_f32_e32 v129, v129
	v_exp_f32_e32 v131, v131
	v_exp_f32_e32 v133, v133
	v_exp_f32_e32 v135, v135
	v_mul_f32_e32 v155, 0xbfb8aa3b, v96
	v_mul_f32_e32 v157, 0xbfb8aa3b, v97
	v_exp_f32_e32 v162, v162
	v_exp_f32_e32 v163, v163
	v_exp_f32_e32 v155, v155
	v_exp_f32_e32 v157, v157
	v_add_f32_e32 v129, 1.0, v129
	v_add_f32_e32 v131, 1.0, v131
	v_add_f32_e32 v133, 1.0, v133
	v_add_f32_e32 v135, 1.0, v135
	v_add_f32_e32 v162, 1.0, v162
	v_add_f32_e32 v163, 1.0, v163
	v_rcp_f32_e32 v129, v129
	v_rcp_f32_e32 v131, v131
	v_rcp_f32_e32 v133, v133
	v_rcp_f32_e32 v135, v135
	v_add_f32_e32 v155, 1.0, v155
	v_add_f32_e32 v157, 1.0, v157
	v_rcp_f32_e32 v162, v162
	v_rcp_f32_e32 v163, v163
	v_rcp_f32_e32 v155, v155
	v_rcp_f32_e32 v157, v157
	v_mov_b32_e32 v159, v145
	v_mul_f32_e32 v129, v108, v129
	v_mul_f32_e32 v131, v109, v131
	v_mul_f32_e32 v133, v110, v133
	v_mul_f32_e32 v135, v111, v135
	v_mul_f32_e32 v165, v106, v162
	v_mul_f32_e32 v168, v107, v163
	v_lshl_add_u64 v[166:167], v[160:161], 0, v[158:159]
	v_cvt_pk_bf16_f32 v162, v129, v131
	v_cvt_pk_bf16_f32 v163, v133, v135
	v_mul_f32_e32 v155, v104, v155
	v_mul_f32_e32 v157, v105, v157
	v_cvt_pk_bf16_f32 v164, v155, v157
	v_mul_f32_e32 v129, 0xbfb8aa3b, v84
	v_cvt_pk_bf16_f32 v165, v165, v168
	flat_store_dwordx4 v[166:167], v[162:165] sc1
	v_mul_f32_e32 v131, 0xbfb8aa3b, v85
	v_mul_f32_e32 v133, 0xbfb8aa3b, v86
	v_mul_f32_e32 v135, 0xbfb8aa3b, v87
	v_mul_f32_e32 v162, 0xbfb8aa3b, v82
	v_mul_f32_e32 v163, 0xbfb8aa3b, v83
	v_exp_f32_e32 v129, v129
	v_exp_f32_e32 v131, v131
	v_exp_f32_e32 v133, v133
	v_exp_f32_e32 v135, v135
	v_mul_f32_e32 v155, 0xbfb8aa3b, v80
	v_mul_f32_e32 v159, 0xbfb8aa3b, v81
	v_exp_f32_e32 v162, v162
	v_exp_f32_e32 v163, v163
	v_exp_f32_e32 v155, v155
	v_exp_f32_e32 v159, v159
	v_add_f32_e32 v129, 1.0, v129
	v_add_f32_e32 v131, 1.0, v131
	v_add_f32_e32 v133, 1.0, v133
	v_add_f32_e32 v135, 1.0, v135
	v_add_f32_e32 v162, 1.0, v162
	v_add_f32_e32 v163, 1.0, v163
	v_rcp_f32_e32 v129, v129
	v_rcp_f32_e32 v131, v131
	v_rcp_f32_e32 v133, v133
	v_rcp_f32_e32 v135, v135
	v_add_f32_e32 v155, 1.0, v155
	v_add_f32_e32 v159, 1.0, v159
	v_rcp_f32_e32 v162, v162
	v_rcp_f32_e32 v163, v163
	v_rcp_f32_e32 v155, v155
	v_rcp_f32_e32 v159, v159
	v_mov_b32_e32 v157, v145
	v_mul_f32_e32 v129, v92, v129
	v_mul_f32_e32 v131, v93, v131
	v_mul_f32_e32 v133, v94, v133
	v_mul_f32_e32 v135, v95, v135
	v_mul_f32_e32 v165, v90, v162
	v_mul_f32_e32 v168, v91, v163
	v_lshl_add_u64 v[166:167], v[160:161], 0, v[156:157]
	v_cvt_pk_bf16_f32 v162, v129, v131
	v_cvt_pk_bf16_f32 v163, v133, v135
	v_mul_f32_e32 v155, v88, v155
	v_mul_f32_e32 v159, v89, v159
	v_cvt_pk_bf16_f32 v164, v155, v159
	v_mul_f32_e32 v129, 0xbfb8aa3b, v68
	v_cvt_pk_bf16_f32 v165, v165, v168
	flat_store_dwordx4 v[166:167], v[162:165] sc1
	v_mul_f32_e32 v131, 0xbfb8aa3b, v69
	v_mul_f32_e32 v133, 0xbfb8aa3b, v70
	v_mul_f32_e32 v135, 0xbfb8aa3b, v71
	v_mul_f32_e32 v162, 0xbfb8aa3b, v66
	v_mul_f32_e32 v163, 0xbfb8aa3b, v67
	v_exp_f32_e32 v129, v129
	v_exp_f32_e32 v131, v131
	v_exp_f32_e32 v133, v133
	v_exp_f32_e32 v135, v135
	v_mul_f32_e32 v157, 0xbfb8aa3b, v64
	v_mul_f32_e32 v159, 0xbfb8aa3b, v65
	v_exp_f32_e32 v162, v162
	v_exp_f32_e32 v163, v163
	v_exp_f32_e32 v157, v157
	v_exp_f32_e32 v159, v159
; __device__ __forceinline__ unsigned cvt_pk_bf16(float lo, float hi) { unsigned r; asm volatile("v_cvt_pk_bf16_f32 %0, %1, %2" : "=v"(r) : "v"(lo), "v"(hi)); return r; }
;     __device__ __forceinline__ void operator()(const f32x4 (&acc)[2][2][4][2], const Unit& u, int wr, int wc, int fr, int fq) const {
;     ...
;             unsigned char* base = wb + OFF_U + (unsigned)((pn - 6) * 128 + cl) * 2u;
; #pragma unroll
;             for (int ai = 0; ai < 2; ++ai)
; #pragma unroll
;                 for (int m = 0; m < 4; ++m) { unsigned char* rowp = base + (unsigned)((row0 + ai * HALF + m * 16) * 512) * 2u;
;                     float o[8];
; #pragma unroll
;                     for (int n = 0; n < 2; ++n)
; #pragma unroll
;                         for (int e = 0; e < 4; ++e) { const float a = acc[ai][0][m][n][e], g = acc[ai][1][m][n][e];
;                             o[4 * n + e] = a * __builtin_amdgcn_rcpf(1.0f + __builtin_amdgcn_exp2f(-1.4426950408889634f * g)); }
;                     u32x4 w; w.x = cvt_pk_bf16(o[0], o[1]); w.y = cvt_pk_bf16(o[2], o[3]); w.z = cvt_pk_bf16(o[4], o[5]); w.w = cvt_pk_bf16(o[6], o[7]);
;                     *(u32x4*)rowp = w; }
	v_add_f32_e32 v129, 1.0, v129
	v_add_f32_e32 v131, 1.0, v131
	v_add_f32_e32 v133, 1.0, v133
	v_add_f32_e32 v135, 1.0, v135
	v_add_f32_e32 v162, 1.0, v162
	v_add_f32_e32 v163, 1.0, v163
	v_rcp_f32_e32 v129, v129
	v_rcp_f32_e32 v131, v131
	v_rcp_f32_e32 v133, v133
	v_rcp_f32_e32 v135, v135
	v_add_f32_e32 v157, 1.0, v157
	v_add_f32_e32 v159, 1.0, v159
	v_rcp_f32_e32 v162, v162
	v_rcp_f32_e32 v163, v163
	v_rcp_f32_e32 v157, v157
	v_rcp_f32_e32 v159, v159
	v_mov_b32_e32 v155, v145
	v_mul_f32_e32 v129, v76, v129
	v_mul_f32_e32 v131, v77, v131
	v_mul_f32_e32 v133, v78, v133
	v_mul_f32_e32 v135, v79, v135
	v_mul_f32_e32 v165, v74, v162
	v_mul_f32_e32 v168, v75, v163
	v_lshl_add_u64 v[166:167], v[160:161], 0, v[154:155]
	v_cvt_pk_bf16_f32 v162, v129, v131
	v_cvt_pk_bf16_f32 v163, v133, v135
	v_mul_f32_e32 v157, v72, v157
	v_mul_f32_e32 v159, v73, v159
	v_cvt_pk_bf16_f32 v164, v157, v159
	v_mul_f32_e32 v129, 0xbfb8aa3b, v52
	v_cvt_pk_bf16_f32 v165, v165, v168
	flat_store_dwordx4 v[166:167], v[162:165] sc1
	v_mul_f32_e32 v131, 0xbfb8aa3b, v53
	v_mul_f32_e32 v133, 0xbfb8aa3b, v54
	v_mul_f32_e32 v155, 0xbfb8aa3b, v55
	v_mul_f32_e32 v162, 0xbfb8aa3b, v50
	v_mul_f32_e32 v163, 0xbfb8aa3b, v51
	v_exp_f32_e32 v129, v129
	v_exp_f32_e32 v131, v131
	v_exp_f32_e32 v133, v133
	v_exp_f32_e32 v155, v155
	v_mul_f32_e32 v157, 0xbfb8aa3b, v48
	v_mul_f32_e32 v159, 0xbfb8aa3b, v49
	v_exp_f32_e32 v162, v162
	v_exp_f32_e32 v163, v163
	v_exp_f32_e32 v157, v157
	v_exp_f32_e32 v159, v159
	v_add_f32_e32 v129, 1.0, v129
	v_add_f32_e32 v131, 1.0, v131
	v_add_f32_e32 v133, 1.0, v133
	v_add_f32_e32 v155, 1.0, v155
	v_add_f32_e32 v162, 1.0, v162
	v_add_f32_e32 v163, 1.0, v163
	v_rcp_f32_e32 v129, v129
	v_rcp_f32_e32 v131, v131
	v_rcp_f32_e32 v133, v133
	v_rcp_f32_e32 v155, v155
	v_add_f32_e32 v157, 1.0, v157
	v_add_f32_e32 v159, 1.0, v159
	v_rcp_f32_e32 v162, v162
	v_rcp_f32_e32 v163, v163
	v_rcp_f32_e32 v157, v157
	v_rcp_f32_e32 v159, v159
	v_mov_b32_e32 v135, v145
	v_mul_f32_e32 v129, v60, v129
	v_mul_f32_e32 v131, v61, v131
	v_mul_f32_e32 v133, v62, v133
	v_mul_f32_e32 v155, v63, v155
	v_mul_f32_e32 v165, v58, v162
	v_mul_f32_e32 v168, v59, v163
	v_lshl_add_u64 v[166:167], v[160:161], 0, v[134:135]
	v_cvt_pk_bf16_f32 v162, v129, v131
	v_cvt_pk_bf16_f32 v163, v133, v155
	v_mul_f32_e32 v157, v56, v157
	v_mul_f32_e32 v159, v57, v159
	v_cvt_pk_bf16_f32 v164, v157, v159
	v_mul_f32_e32 v129, 0xbfb8aa3b, v36
	v_cvt_pk_bf16_f32 v165, v165, v168
	flat_store_dwordx4 v[166:167], v[162:165] sc1
	v_mul_f32_e32 v131, 0xbfb8aa3b, v37
	v_mul_f32_e32 v135, 0xbfb8aa3b, v38
	v_mul_f32_e32 v155, 0xbfb8aa3b, v39
	v_mul_f32_e32 v162, 0xbfb8aa3b, v34
	v_mul_f32_e32 v163, 0xbfb8aa3b, v35
	v_exp_f32_e32 v129, v129
	v_exp_f32_e32 v131, v131
	v_exp_f32_e32 v135, v135
	v_exp_f32_e32 v155, v155
	v_mul_f32_e32 v157, 0xbfb8aa3b, v32
	v_mul_f32_e32 v159, 0xbfb8aa3b, v33
	v_exp_f32_e32 v162, v162
	v_exp_f32_e32 v163, v163
	v_exp_f32_e32 v157, v157
	v_exp_f32_e32 v159, v159
	v_add_f32_e32 v129, 1.0, v129
	v_add_f32_e32 v131, 1.0, v131
	v_add_f32_e32 v135, 1.0, v135
	v_add_f32_e32 v155, 1.0, v155
	v_add_f32_e32 v162, 1.0, v162
	v_add_f32_e32 v163, 1.0, v163
	v_rcp_f32_e32 v129, v129
	v_rcp_f32_e32 v131, v131
	v_rcp_f32_e32 v135, v135
	v_rcp_f32_e32 v155, v155
	v_add_f32_e32 v157, 1.0, v157
	v_add_f32_e32 v159, 1.0, v159
	v_rcp_f32_e32 v162, v162
	v_rcp_f32_e32 v163, v163
	v_rcp_f32_e32 v157, v157
	v_rcp_f32_e32 v159, v159
	v_mov_b32_e32 v133, v145
	v_mul_f32_e32 v129, v44, v129
	v_mul_f32_e32 v131, v45, v131
	v_mul_f32_e32 v135, v46, v135
	v_mul_f32_e32 v155, v47, v155
	v_mul_f32_e32 v165, v42, v162
	v_mul_f32_e32 v168, v43, v163
	v_lshl_add_u64 v[166:167], v[160:161], 0, v[132:133]
	v_cvt_pk_bf16_f32 v162, v129, v131
	v_cvt_pk_bf16_f32 v163, v135, v155
	v_mul_f32_e32 v157, v40, v157
	v_mul_f32_e32 v159, v41, v159
	v_cvt_pk_bf16_f32 v164, v157, v159
	v_mul_f32_e32 v129, 0xbfb8aa3b, v20
	v_cvt_pk_bf16_f32 v165, v165, v168
	flat_store_dwordx4 v[166:167], v[162:165] sc1
	v_mul_f32_e32 v133, 0xbfb8aa3b, v21
	v_mul_f32_e32 v135, 0xbfb8aa3b, v22
	v_mul_f32_e32 v155, 0xbfb8aa3b, v23
	v_mul_f32_e32 v162, 0xbfb8aa3b, v18
	v_mul_f32_e32 v163, 0xbfb8aa3b, v19
	v_exp_f32_e32 v129, v129
	v_exp_f32_e32 v133, v133
	v_exp_f32_e32 v135, v135
	v_exp_f32_e32 v155, v155
	v_mul_f32_e32 v157, 0xbfb8aa3b, v16
	v_mul_f32_e32 v159, 0xbfb8aa3b, v17
	v_exp_f32_e32 v162, v162
	v_exp_f32_e32 v163, v163
	v_exp_f32_e32 v157, v157
	v_exp_f32_e32 v159, v159
	v_add_f32_e32 v129, 1.0, v129
	v_add_f32_e32 v133, 1.0, v133
	v_add_f32_e32 v135, 1.0, v135
	v_add_f32_e32 v155, 1.0, v155
	v_add_f32_e32 v162, 1.0, v162
	v_add_f32_e32 v163, 1.0, v163
	v_rcp_f32_e32 v129, v129
	v_rcp_f32_e32 v133, v133
	v_rcp_f32_e32 v135, v135
	v_rcp_f32_e32 v155, v155
	v_add_f32_e32 v157, 1.0, v157
	v_add_f32_e32 v159, 1.0, v159
	v_rcp_f32_e32 v162, v162
	v_rcp_f32_e32 v163, v163
	v_rcp_f32_e32 v157, v157
	v_rcp_f32_e32 v159, v159
	v_mov_b32_e32 v131, v145
	v_mul_f32_e32 v129, v28, v129
	v_mul_f32_e32 v133, v29, v133
	v_mul_f32_e32 v135, v30, v135
	v_mul_f32_e32 v155, v31, v155
	v_mul_f32_e32 v165, v26, v162
	v_mul_f32_e32 v168, v27, v163
	v_lshl_add_u64 v[166:167], v[160:161], 0, v[130:131]
	v_cvt_pk_bf16_f32 v162, v129, v133
	v_cvt_pk_bf16_f32 v163, v135, v155
	v_mul_f32_e32 v157, v24, v157
	v_mul_f32_e32 v159, v25, v159
	v_cvt_pk_bf16_f32 v164, v157, v159
	v_cvt_pk_bf16_f32 v165, v165, v168
	flat_store_dwordx4 v[166:167], v[162:165] sc1
	v_mul_f32_e32 v129, 0xbfb8aa3b, v4
	v_mul_f32_e32 v133, 0xbfb8aa3b, v5
	v_mul_f32_e32 v163, 0xbfb8aa3b, v3
	v_mul_f32_e32 v135, 0xbfb8aa3b, v6
	v_mul_f32_e32 v155, 0xbfb8aa3b, v7
	v_mul_f32_e32 v157, 0xbfb8aa3b, v0
	v_mul_f32_e32 v159, 0xbfb8aa3b, v1
	v_mul_f32_e32 v162, 0xbfb8aa3b, v2
	v_exp_f32_e32 v163, v163
	v_exp_f32_e32 v131, v129
	v_exp_f32_e32 v133, v133
	v_exp_f32_e32 v135, v135
	v_exp_f32_e32 v155, v155
	v_exp_f32_e32 v157, v157
	v_exp_f32_e32 v159, v159
	v_exp_f32_e32 v162, v162
	v_add_f32_e32 v163, 1.0, v163
	v_add_f32_e32 v131, 1.0, v131
	v_add_f32_e32 v133, 1.0, v133
	v_add_f32_e32 v135, 1.0, v135
	v_add_f32_e32 v155, 1.0, v155
	v_add_f32_e32 v157, 1.0, v157
	v_add_f32_e32 v159, 1.0, v159
	v_add_f32_e32 v162, 1.0, v162
	v_rcp_f32_e32 v163, v163
	v_rcp_f32_e32 v131, v131
	v_rcp_f32_e32 v133, v133
	v_rcp_f32_e32 v135, v135
	v_rcp_f32_e32 v155, v155
	v_rcp_f32_e32 v157, v157
	v_rcp_f32_e32 v159, v159
	v_rcp_f32_e32 v162, v162
	v_mov_b32_e32 v129, v145
	v_mul_f32_e32 v163, v11, v163
	v_lshl_add_u64 v[164:165], v[160:161], 0, v[128:129]
	v_mul_f32_e32 v131, v12, v131
	v_mul_f32_e32 v133, v13, v133
	v_mul_f32_e32 v135, v14, v135
	v_mul_f32_e32 v155, v15, v155
	v_mul_f32_e32 v157, v8, v157
	v_mul_f32_e32 v159, v9, v159
	v_mul_f32_e32 v166, v10, v162
	v_cvt_pk_bf16_f32 v160, v131, v133
	v_cvt_pk_bf16_f32 v161, v135, v155
	v_cvt_pk_bf16_f32 v162, v157, v159
	v_cvt_pk_bf16_f32 v163, v166, v163
	flat_store_dwordx4 v[164:165], v[160:163] sc1
	s_mov_b64 s[8:9], 0
; __device__ __forceinline__ unsigned cvt_pk_bf16(float lo, float hi) { unsigned r; asm volatile("v_cvt_pk_bf16_f32 %0, %1, %2" : "=v"(r) : "v"(lo), "v"(hi)); return r; }
;     __device__ __forceinline__ void operator()(const f32x4 (&acc)[2][2][4][2], const Unit& u, int wr, int wc, int fr, int fq) const {
;     ...
;         } else if (pn < 6) {
;             unsigned char* base = wb + OFF_V + (unsigned)((pn - 4) * 256 + cl) * 2u;
; #pragma unroll
;             for (int ai = 0; ai < 2; ++ai)
; #pragma unroll
;                 for (int m = 0; m < 4; ++m) { unsigned char* rowp = base + (unsigned)((row0 + ai * HALF + m * 16) * 512) * 2u;
; #pragma unroll
;                     for (int bj = 0; bj < 2; ++bj) { const f32x4 v0 = acc[ai][bj][m][0], v1 = acc[ai][bj][m][1];
;                         u32x4 w; w.x = cvt_pk_bf16(v0[0], v0[1]); w.y = cvt_pk_bf16(v0[2], v0[3]); w.z = cvt_pk_bf16(v1[0], v1[1]); w.w = cvt_pk_bf16(v1[2], v1[3]);
;                         *(u32x4*)(rowp + bj * HALF * 2) = w; } }
.LBB0_130:
	s_andn2_b64 vcc, exec, s[8:9]
	s_cbranch_vccnz .LBB0_132
	v_lshl_add_u32 v160, s48, 9, v184
	v_mov_b32_e32 v161, v145
	v_lshl_add_u64 v[160:161], s[46:47], 0, v[160:161]
	v_lshl_add_u64 v[160:161], v[160:161], 0, s[24:25]
	v_lshl_add_u64 v[166:167], v[160:161], 0, v[144:145]
	v_cvt_pk_bf16_f32 v162, v124, v125
	v_cvt_pk_bf16_f32 v163, v126, v127
	v_cvt_pk_bf16_f32 v164, v120, v121
	v_cvt_pk_bf16_f32 v165, v122, v123
	flat_store_dwordx4 v[166:167], v[162:165] sc1
	v_mov_b32_e32 v159, v145
	v_lshl_add_u64 v[158:159], v[160:161], 0, v[158:159]
	v_cvt_pk_bf16_f32 v162, v116, v117
	v_cvt_pk_bf16_f32 v163, v118, v119
	v_cvt_pk_bf16_f32 v164, v112, v113
	v_cvt_pk_bf16_f32 v165, v114, v115
	flat_store_dwordx4 v[166:167], v[162:165] offset:256 sc1
	v_mov_b32_e32 v157, v145
	v_mov_b32_e32 v155, v145
	v_cvt_pk_bf16_f32 v162, v108, v109
	v_cvt_pk_bf16_f32 v163, v110, v111
	v_cvt_pk_bf16_f32 v164, v104, v105
	v_cvt_pk_bf16_f32 v165, v106, v107
	flat_store_dwordx4 v[158:159], v[162:165] sc1
	v_mov_b32_e32 v135, v145
	v_lshl_add_u64 v[134:135], v[160:161], 0, v[134:135]
	v_cvt_pk_bf16_f32 v162, v100, v101
	v_cvt_pk_bf16_f32 v163, v102, v103
	v_cvt_pk_bf16_f32 v164, v96, v97
	v_cvt_pk_bf16_f32 v165, v98, v99
	flat_store_dwordx4 v[158:159], v[162:165] offset:256 sc1
	v_mov_b32_e32 v133, v145
	v_mov_b32_e32 v131, v145
	v_lshl_add_u64 v[162:163], v[160:161], 0, v[156:157]
	v_cvt_pk_bf16_f32 v156, v92, v93
	v_cvt_pk_bf16_f32 v157, v94, v95
	v_cvt_pk_bf16_f32 v158, v88, v89
	v_cvt_pk_bf16_f32 v159, v90, v91
	flat_store_dwordx4 v[162:163], v[156:159] sc1
	v_mov_b32_e32 v129, v145
	s_nop 0
	v_cvt_pk_bf16_f32 v156, v84, v85
	v_cvt_pk_bf16_f32 v157, v86, v87
	v_cvt_pk_bf16_f32 v158, v80, v81
	v_cvt_pk_bf16_f32 v159, v82, v83
	flat_store_dwordx4 v[162:163], v[156:159] offset:256 sc1
	s_nop 1
	v_lshl_add_u64 v[158:159], v[160:161], 0, v[154:155]
	v_cvt_pk_bf16_f32 v154, v76, v77
	v_cvt_pk_bf16_f32 v155, v78, v79
	v_cvt_pk_bf16_f32 v156, v72, v73
	v_cvt_pk_bf16_f32 v157, v74, v75
	flat_store_dwordx4 v[158:159], v[154:157] sc1
	s_nop 1
	v_cvt_pk_bf16_f32 v154, v68, v69
	v_cvt_pk_bf16_f32 v155, v70, v71
	v_cvt_pk_bf16_f32 v156, v64, v65
	v_cvt_pk_bf16_f32 v157, v66, v67
	flat_store_dwordx4 v[158:159], v[154:157] offset:256 sc1
	s_nop 1
	v_cvt_pk_bf16_f32 v154, v60, v61
	v_cvt_pk_bf16_f32 v155, v62, v63
	v_cvt_pk_bf16_f32 v156, v56, v57
	v_cvt_pk_bf16_f32 v157, v58, v59
	flat_store_dwordx4 v[134:135], v[154:157] sc1
	s_nop 1
	v_cvt_pk_bf16_f32 v154, v52, v53
	v_cvt_pk_bf16_f32 v155, v54, v55
	v_cvt_pk_bf16_f32 v156, v48, v49
	v_cvt_pk_bf16_f32 v157, v50, v51
	flat_store_dwordx4 v[134:135], v[154:157] offset:256 sc1
	s_nop 1
	v_lshl_add_u64 v[154:155], v[160:161], 0, v[132:133]
	v_cvt_pk_bf16_f32 v132, v44, v45
	v_cvt_pk_bf16_f32 v133, v46, v47
	v_cvt_pk_bf16_f32 v134, v40, v41
	v_cvt_pk_bf16_f32 v135, v42, v43
	flat_store_dwordx4 v[154:155], v[132:135] sc1
	s_nop 1
	v_cvt_pk_bf16_f32 v132, v36, v37
	v_cvt_pk_bf16_f32 v133, v38, v39
	v_cvt_pk_bf16_f32 v134, v32, v33
	v_cvt_pk_bf16_f32 v135, v34, v35
	flat_store_dwordx4 v[154:155], v[132:135] offset:256 sc1
	s_nop 1
	v_lshl_add_u64 v[134:135], v[160:161], 0, v[130:131]
	v_cvt_pk_bf16_f32 v130, v28, v29
	v_cvt_pk_bf16_f32 v131, v30, v31
	v_cvt_pk_bf16_f32 v132, v24, v25
	v_cvt_pk_bf16_f32 v133, v26, v27
	flat_store_dwordx4 v[134:135], v[130:133] sc1
	s_nop 1
	v_cvt_pk_bf16_f32 v130, v20, v21
	v_cvt_pk_bf16_f32 v131, v22, v23
	v_cvt_pk_bf16_f32 v132, v16, v17
	v_cvt_pk_bf16_f32 v133, v18, v19
	flat_store_dwordx4 v[134:135], v[130:133] offset:256 sc1
	s_nop 1
	v_lshl_add_u64 v[132:133], v[160:161], 0, v[128:129]
	v_cvt_pk_bf16_f32 v128, v12, v13
	v_cvt_pk_bf16_f32 v129, v14, v15
	v_cvt_pk_bf16_f32 v130, v8, v9
	v_cvt_pk_bf16_f32 v131, v10, v11
	flat_store_dwordx4 v[132:133], v[128:131] sc1
	s_nop 1
	v_cvt_pk_bf16_f32 v128, v4, v5
	v_cvt_pk_bf16_f32 v129, v6, v7
	v_cvt_pk_bf16_f32 v130, v0, v1
	v_cvt_pk_bf16_f32 v131, v2, v3
	flat_store_dwordx4 v[132:133], v[128:131] offset:256 sc1

; __device__ __forceinline__ unsigned cvt_pk_bf16(float lo, float hi) { unsigned r; asm volatile("v_cvt_pk_bf16_f32 %0, %1, %2" : "=v"(r) : "v"(lo), "v"(hi)); return r; }
;     __device__ __forceinline__ void operator()(const f32x4 (&acc)[2][2][4][2], const Unit& u, int wr, int wc, int fr, int fq) const {
;     ...
;             for (int ai = 0; ai < 2; ++ai)
; #pragma unroll
;                 for (int m = 0; m < 4; ++m) {
;                     const int row = row0 + ai * HALF + m * 16, pos = row & 4095;
;                     const unsigned ro = (unsigned)(pos * 32 + i0) * 4u; const f32x4 c4 = *(const f32x4*)(cs + ro), s4 = *(const f32x4*)(sn + ro);
; #pragma unroll
;                     for (int bj = 0; bj < 2; ++bj) {
;                         const f32x4 v0 = acc[ai][bj][m][0], v1 = acc[ai][bj][m][1];
;                         float o[8];
;                         o[0] = v0[0] * c4[0] - v0[1] * s4[0]; o[1] = v0[1] * c4[0] + v0[0] * s4[0];
;                         o[2] = v0[2] * c4[1] - v0[3] * s4[1]; o[3] = v0[3] * c4[1] + v0[2] * s4[1];
;                         o[4] = v1[0] * c4[2] - v1[1] * s4[2]; o[5] = v1[1] * c4[2] + v1[0] * s4[2];
;                         o[6] = v1[2] * c4[3] - v1[3] * s4[3]; o[7] = v1[3] * c4[3] + v1[2] * s4[3];
;                         if (!isq) {
; #pragma unroll
;                             for (int e = 0; e < 8; ++e) ks[bj][e] += o[e]; }
;                         u32x4 w; w.x = cvt_pk_bf16(o[0] * sc, o[1] * sc); w.y = cvt_pk_bf16(o[2] * sc, o[3] * sc); w.z = cvt_pk_bf16(o[4] * sc, o[5] * sc); w.w = cvt_pk_bf16(o[6] * sc, o[7] * sc);
;                         *(u32x4*)(base + (unsigned)(row * 512 + bj * HALF) * 2u) = w;
.LBB0_137:
	v_cndmask_b32_e64 v167, 1.0, v188, s[8:9]
	v_mul_f32_e32 v125, v167, v171
	v_mul_f32_e32 v127, v167, v166
	v_cvt_pk_bf16_f32 v168, v125, v127
	v_mul_f32_e32 v125, v167, v169
	v_mul_f32_e32 v127, v167, v160
	v_cvt_pk_bf16_f32 v169, v125, v127
	v_mul_f32_e32 v125, v167, v163
	v_mul_f32_e32 v124, v167, v124
	v_mov_b32_e32 v192, v132
	v_mov_b32_e32 v193, v132
	s_and_b64 s[34:35], s[8:9], exec
	v_cvt_pk_bf16_f32 v170, v125, v124
	v_mul_f32_e32 v124, v167, v165
	v_mul_f32_e32 v125, v167, v126
	v_mov_b32_e32 v194, v128
	v_mov_b32_e32 v195, v128
	v_mov_b32_e32 v132, v133
	s_cselect_b32 s27, s79, 0x9000000
	v_cvt_pk_bf16_f32 v171, v124, v125
	v_pk_mul_f32 v[124:125], v[116:117], v[192:193]
	v_mov_b32_e32 v128, v129
	v_mov_b32_e32 v196, v134
	v_mov_b32_e32 v197, v134
	s_add_u32 s34, s46, s27
	v_pk_fma_f32 v[162:163], v[116:117], v[194:195], v[124:125] op_sel:[0,0,1] op_sel_hi:[1,1,0]
	v_pk_fma_f32 v[116:117], v[116:117], v[194:195], v[124:125] op_sel:[0,0,1] op_sel_hi:[1,1,0] neg_lo:[1,0,0] neg_hi:[1,0,0]
	v_pk_mul_f32 v[124:125], v[118:119], v[132:133]
	v_mov_b32_e32 v198, v130
	v_mov_b32_e32 v199, v130
	s_addc_u32 s35, s47, 0
	s_and_b32 s27, s48, 1
	v_pk_fma_f32 v[132:133], v[118:119], v[128:129], v[124:125] op_sel:[0,0,1] op_sel_hi:[1,1,0]
	v_pk_fma_f32 v[164:165], v[118:119], v[128:129], v[124:125] op_sel:[0,0,1] op_sel_hi:[1,1,0] neg_lo:[1,0,0] neg_hi:[1,0,0]
	v_pk_mul_f32 v[124:125], v[112:113], v[196:197]
	v_mov_b32_e32 v134, v135
	v_lshl_or_b32 v158, s27, 9, v181
	v_mov_b32_e32 v159, v145
	v_pk_fma_f32 v[118:119], v[112:113], v[198:199], v[124:125] op_sel:[0,0,1] op_sel_hi:[1,1,0]
	v_pk_fma_f32 v[112:113], v[112:113], v[198:199], v[124:125] op_sel:[0,0,1] op_sel_hi:[1,1,0] neg_lo:[1,0,0] neg_hi:[1,0,0]
	v_mov_b32_e32 v130, v131
	v_lshl_add_u64 v[158:159], s[34:35], 0, v[158:159]
	v_pk_mul_f32 v[124:125], v[114:115], v[134:135]
	v_cndmask_b32_e64 v112, 0, 1, s[50:51]
	v_lshl_add_u64 v[160:161], v[158:159], 0, v[144:145]
	v_pk_fma_f32 v[134:135], v[114:115], v[130:131], v[124:125] op_sel:[0,0,1] op_sel_hi:[1,1,0]
	v_cmp_ne_u32_e64 s[8:9], 1, v112
	s_andn2_b64 vcc, exec, s[50:51]
	v_pk_fma_f32 v[114:115], v[114:115], v[130:131], v[124:125] op_sel:[0,0,1] op_sel_hi:[1,1,0] neg_lo:[1,0,0] neg_hi:[1,0,0]
	flat_store_dwordx4 v[160:161], v[168:171] sc1
	s_cbranch_vccnz .LBB0_139
	v_mov_b32_e32 v135, v115
	v_mov_b32_e32 v119, v113
	v_mov_b32_e32 v133, v165
	v_mov_b32_e32 v163, v117
	v_pk_add_f32 v[130:131], v[162:163], 0 op_sel_hi:[1,0]
	v_pk_add_f32 v[128:129], v[132:133], 0 op_sel_hi:[1,0]
	v_pk_add_f32 v[126:127], v[118:119], 0 op_sel_hi:[1,0]
	v_pk_add_f32 v[124:125], v[134:135], 0 op_sel_hi:[1,0]
	s_branch .LBB0_140

; __device__ __forceinline__ unsigned cvt_pk_bf16(float lo, float hi) { unsigned r; asm volatile("v_cvt_pk_bf16_f32 %0, %1, %2" : "=v"(r) : "v"(lo), "v"(hi)); return r; }
;     __device__ __forceinline__ void operator()(const f32x4 (&acc)[2][2][4][2], const Unit& u, int wr, int wc, int fr, int fq) const {
;     ...
;                 for (int m = 0; m < 4; ++m) {
;                     const int row = row0 + ai * HALF + m * 16, pos = row & 4095;
;                     const unsigned ro = (unsigned)(pos * 32 + i0) * 4u; const f32x4 c4 = *(const f32x4*)(cs + ro), s4 = *(const f32x4*)(sn + ro);
; #pragma unroll
;                     for (int bj = 0; bj < 2; ++bj) {
;                         const f32x4 v0 = acc[ai][bj][m][0], v1 = acc[ai][bj][m][1];
;                         float o[8];
;                         o[0] = v0[0] * c4[0] - v0[1] * s4[0]; o[1] = v0[1] * c4[0] + v0[0] * s4[0];
;                         o[2] = v0[2] * c4[1] - v0[3] * s4[1]; o[3] = v0[3] * c4[1] + v0[2] * s4[1];
;                         o[4] = v1[0] * c4[2] - v1[1] * s4[2]; o[5] = v1[1] * c4[2] + v1[0] * s4[2];
;                         o[6] = v1[2] * c4[3] - v1[3] * s4[3]; o[7] = v1[3] * c4[3] + v1[2] * s4[3];
;                         if (!isq) {
; #pragma unroll
;                             for (int e = 0; e < 8; ++e) ks[bj][e] += o[e]; }
;                         u32x4 w; w.x = cvt_pk_bf16(o[0] * sc, o[1] * sc); w.y = cvt_pk_bf16(o[2] * sc, o[3] * sc); w.z = cvt_pk_bf16(o[4] * sc, o[5] * sc); w.w = cvt_pk_bf16(o[6] * sc, o[7] * sc);
;                         *(u32x4*)(base + (unsigned)(row * 512 + bj * HALF) * 2u) = w;
.LBB0_140:
	v_mul_f32_e32 v112, v167, v117
	v_mul_f32_e32 v114, v167, v162
	v_cvt_pk_bf16_f32 v168, v112, v114
	v_mul_f32_e32 v112, v167, v165
	v_mul_f32_e32 v114, v167, v132
	v_cvt_pk_bf16_f32 v169, v112, v114
	v_mul_f32_e32 v112, v167, v113
	v_mul_f32_e32 v113, v167, v118
	v_cvt_pk_bf16_f32 v170, v112, v113
	v_mul_f32_e32 v112, v167, v115
	v_add_u32_e32 v164, 16, v190
	v_mul_f32_e32 v113, v167, v134
	v_cvt_pk_bf16_f32 v171, v112, v113
	v_lshlrev_b32_e32 v112, 7, v164
	v_and_or_b32 v144, v112, s78, v182
	v_lshl_add_u64 v[112:113], s[54:55], 0, v[144:145]
	flat_load_dwordx4 v[112:115], v[112:113]
	v_lshl_add_u64 v[116:117], s[52:53], 0, v[144:145]
	flat_load_dwordx4 v[116:119], v[116:117]
	s_and_b64 vcc, exec, s[8:9]
	flat_store_dwordx4 v[160:161], v[168:171] offset:256 sc1
	s_waitcnt vmcnt(0) lgkmcnt(0)
	v_pk_mul_f32 v[132:133], v[108:109], v[112:113] op_sel_hi:[1,0]
	v_pk_mul_f32 v[160:161], v[110:111], v[112:113] op_sel:[0,1]
	v_pk_mul_f32 v[168:169], v[104:105], v[114:115] op_sel_hi:[1,0]
	v_mov_b32_e32 v144, v115
	v_mov_b32_e32 v166, v119
	v_pk_fma_f32 v[134:135], v[108:109], v[116:117], v[132:133] op_sel:[0,0,1] op_sel_hi:[1,0,0]
	v_pk_fma_f32 v[162:163], v[108:109], v[116:117], v[132:133] op_sel:[0,0,1] op_sel_hi:[1,0,0] neg_lo:[1,0,0] neg_hi:[1,0,0]
	v_pk_fma_f32 v[132:133], v[110:111], v[116:117], v[160:161] op_sel:[0,1,1] op_sel_hi:[1,1,0]
	v_pk_fma_f32 v[160:161], v[110:111], v[116:117], v[160:161] op_sel:[0,1,1] op_sel_hi:[1,1,0] neg_lo:[1,0,0] neg_hi:[1,0,0]
	v_pk_fma_f32 v[108:109], v[104:105], v[118:119], v[168:169] op_sel:[0,0,1] op_sel_hi:[1,0,0]
	v_pk_fma_f32 v[110:111], v[104:105], v[118:119], v[168:169] op_sel:[0,0,1] op_sel_hi:[1,0,0] neg_lo:[1,0,0] neg_hi:[1,0,0]
	v_pk_mul_f32 v[168:169], v[106:107], v[144:145] op_sel_hi:[1,0]
	s_nop 0
	v_pk_fma_f32 v[104:105], v[106:107], v[166:167], v[168:169] op_sel:[0,0,1] op_sel_hi:[1,0,0]
	v_pk_fma_f32 v[106:107], v[106:107], v[166:167], v[168:169] op_sel:[0,0,1] op_sel_hi:[1,0,0] neg_lo:[1,0,0] neg_hi:[1,0,0]
	s_cbranch_vccnz .LBB0_142
	v_mov_b32_e32 v105, v107
	v_mov_b32_e32 v109, v111
	v_mov_b32_e32 v133, v161
	v_mov_b32_e32 v135, v163
	v_pk_add_f32 v[156:157], v[156:157], v[134:135]
	v_pk_add_f32 v[154:155], v[154:155], v[132:133]
	v_pk_add_f32 v[122:123], v[122:123], v[108:109]
	v_pk_add_f32 v[120:121], v[120:121], v[104:105]
.LBB0_142:
	v_mul_f32_e32 v105, v167, v163
	v_mul_f32_e32 v106, v167, v134
	v_cvt_pk_bf16_f32 v160, v105, v106
	v_mul_f32_e32 v105, v167, v161
	v_mov_b32_e32 v168, v112
	v_mov_b32_e32 v169, v112
	v_mov_b32_e32 v112, v113
	v_mov_b32_e32 v192, v114
	v_mov_b32_e32 v193, v114
	v_mov_b32_e32 v114, v115
	v_mul_f32_e32 v106, v167, v132
	v_cvt_pk_bf16_f32 v161, v105, v106
	v_mul_f32_e32 v105, v167, v111
	v_mov_b32_e32 v170, v116
	v_mov_b32_e32 v171, v116
	v_mov_b32_e32 v116, v117
	v_mov_b32_e32 v194, v118
	v_mov_b32_e32 v195, v118
	v_mov_b32_e32 v118, v119
	v_lshlrev_b32_e32 v144, 10, v164
	v_mul_f32_e32 v106, v167, v108
	v_cvt_pk_bf16_f32 v162, v105, v106
	v_mul_f32_e32 v105, v167, v107
	v_mul_f32_e32 v104, v167, v104
	v_pk_mul_f32 v[108:109], v[100:101], v[168:169]
	v_pk_mul_f32 v[110:111], v[102:103], v[112:113]
	v_pk_mul_f32 v[112:113], v[96:97], v[192:193]
	v_pk_mul_f32 v[114:115], v[98:99], v[114:115]
	v_cvt_pk_bf16_f32 v163, v105, v104
	v_lshl_add_u64 v[104:105], v[158:159], 0, v[144:145]
	v_pk_fma_f32 v[106:107], v[100:101], v[170:171], v[108:109] op_sel:[0,0,1] op_sel_hi:[1,1,0]
	v_pk_fma_f32 v[100:101], v[100:101], v[170:171], v[108:109] op_sel:[0,0,1] op_sel_hi:[1,1,0] neg_lo:[1,0,0] neg_hi:[1,0,0]
	v_pk_fma_f32 v[108:109], v[102:103], v[116:117], v[110:111] op_sel:[0,0,1] op_sel_hi:[1,1,0]
	v_pk_fma_f32 v[110:111], v[102:103], v[116:117], v[110:111] op_sel:[0,0,1] op_sel_hi:[1,1,0] neg_lo:[1,0,0] neg_hi:[1,0,0]
	v_pk_fma_f32 v[102:103], v[96:97], v[194:195], v[112:113] op_sel:[0,0,1] op_sel_hi:[1,1,0]
	v_pk_fma_f32 v[96:97], v[96:97], v[194:195], v[112:113] op_sel:[0,0,1] op_sel_hi:[1,1,0] neg_lo:[1,0,0] neg_hi:[1,0,0]
	v_pk_fma_f32 v[112:113], v[98:99], v[118:119], v[114:115] op_sel:[0,0,1] op_sel_hi:[1,1,0]
	s_and_b64 vcc, exec, s[8:9]
	v_pk_fma_f32 v[98:99], v[98:99], v[118:119], v[114:115] op_sel:[0,0,1] op_sel_hi:[1,1,0] neg_lo:[1,0,0] neg_hi:[1,0,0]
	flat_store_dwordx4 v[104:105], v[160:163] sc1
	s_cbranch_vccnz .LBB0_144
	v_mov_b32_e32 v113, v99
	v_mov_b32_e32 v103, v97
	v_mov_b32_e32 v109, v111
	v_mov_b32_e32 v107, v101
	v_pk_add_f32 v[130:131], v[130:131], v[106:107]
	v_pk_add_f32 v[128:129], v[128:129], v[108:109]
	v_pk_add_f32 v[126:127], v[126:127], v[102:103]
	v_pk_add_f32 v[124:125], v[124:125], v[112:113]
; __device__ __forceinline__ unsigned cvt_pk_bf16(float lo, float hi) { unsigned r; asm volatile("v_cvt_pk_bf16_f32 %0, %1, %2" : "=v"(r) : "v"(lo), "v"(hi)); return r; }
;     __device__ __forceinline__ void operator()(const f32x4 (&acc)[2][2][4][2], const Unit& u, int wr, int wc, int fr, int fq) const {
;     ...
;                 for (int m = 0; m < 4; ++m) {
;                     const int row = row0 + ai * HALF + m * 16, pos = row & 4095;
;                     const unsigned ro = (unsigned)(pos * 32 + i0) * 4u; const f32x4 c4 = *(const f32x4*)(cs + ro), s4 = *(const f32x4*)(sn + ro);
; #pragma unroll
;                     for (int bj = 0; bj < 2; ++bj) {
;                         const f32x4 v0 = acc[ai][bj][m][0], v1 = acc[ai][bj][m][1];
;                         float o[8];
;                         o[0] = v0[0] * c4[0] - v0[1] * s4[0]; o[1] = v0[1] * c4[0] + v0[0] * s4[0];
;                         o[2] = v0[2] * c4[1] - v0[3] * s4[1]; o[3] = v0[3] * c4[1] + v0[2] * s4[1];
;                         o[4] = v1[0] * c4[2] - v1[1] * s4[2]; o[5] = v1[1] * c4[2] + v1[0] * s4[2];
;                         o[6] = v1[2] * c4[3] - v1[3] * s4[3]; o[7] = v1[3] * c4[3] + v1[2] * s4[3];
;                         if (!isq) {
; #pragma unroll
;                             for (int e = 0; e < 8; ++e) ks[bj][e] += o[e]; }
;                         u32x4 w; w.x = cvt_pk_bf16(o[0] * sc, o[1] * sc); w.y = cvt_pk_bf16(o[2] * sc, o[3] * sc); w.z = cvt_pk_bf16(o[4] * sc, o[5] * sc); w.w = cvt_pk_bf16(o[6] * sc, o[7] * sc);
;                         *(u32x4*)(base + (unsigned)(row * 512 + bj * HALF) * 2u) = w;
.LBB0_144:
	v_mul_f32_e32 v96, v167, v101
	v_mul_f32_e32 v98, v167, v106
	v_cvt_pk_bf16_f32 v106, v96, v98
	v_mul_f32_e32 v96, v167, v111
	v_mul_f32_e32 v98, v167, v108
	v_cvt_pk_bf16_f32 v107, v96, v98
	v_mul_f32_e32 v96, v167, v97
	v_mul_f32_e32 v97, v167, v102
	v_cvt_pk_bf16_f32 v108, v96, v97
	v_mul_f32_e32 v96, v167, v99
	v_mul_f32_e32 v97, v167, v112
	v_add_u32_e32 v112, 32, v190
	v_cvt_pk_bf16_f32 v109, v96, v97
	v_lshlrev_b32_e32 v96, 7, v112
	v_and_or_b32 v144, v96, s78, v182
	v_lshl_add_u64 v[96:97], s[54:55], 0, v[144:145]
	flat_load_dwordx4 v[96:99], v[96:97]
	v_lshl_add_u64 v[100:101], s[52:53], 0, v[144:145]
	flat_load_dwordx4 v[100:103], v[100:101]
	s_and_b64 vcc, exec, s[8:9]
	flat_store_dwordx4 v[104:105], v[106:109] offset:256 sc1
	s_waitcnt vmcnt(0) lgkmcnt(0)
	v_pk_mul_f32 v[104:105], v[92:93], v[96:97] op_sel_hi:[1,0]
	v_pk_mul_f32 v[108:109], v[94:95], v[96:97] op_sel:[0,1]
	v_pk_mul_f32 v[114:115], v[88:89], v[98:99] op_sel_hi:[1,0]
	v_mov_b32_e32 v116, v99
	v_mov_b32_e32 v118, v103
	v_pk_fma_f32 v[106:107], v[92:93], v[100:101], v[104:105] op_sel:[0,0,1] op_sel_hi:[1,0,0]
	v_pk_fma_f32 v[110:111], v[92:93], v[100:101], v[104:105] op_sel:[0,0,1] op_sel_hi:[1,0,0] neg_lo:[1,0,0] neg_hi:[1,0,0]
	v_pk_fma_f32 v[104:105], v[94:95], v[100:101], v[108:109] op_sel:[0,1,1] op_sel_hi:[1,1,0]
	v_pk_fma_f32 v[108:109], v[94:95], v[100:101], v[108:109] op_sel:[0,1,1] op_sel_hi:[1,1,0] neg_lo:[1,0,0] neg_hi:[1,0,0]
	v_pk_fma_f32 v[92:93], v[88:89], v[102:103], v[114:115] op_sel:[0,0,1] op_sel_hi:[1,0,0]
	v_pk_fma_f32 v[94:95], v[88:89], v[102:103], v[114:115] op_sel:[0,0,1] op_sel_hi:[1,0,0] neg_lo:[1,0,0] neg_hi:[1,0,0]
	v_pk_mul_f32 v[114:115], v[90:91], v[116:117] op_sel_hi:[1,0]
	s_nop 0
	v_pk_fma_f32 v[88:89], v[90:91], v[118:119], v[114:115] op_sel:[0,0,1] op_sel_hi:[1,0,0]
	v_pk_fma_f32 v[90:91], v[90:91], v[118:119], v[114:115] op_sel:[0,0,1] op_sel_hi:[1,0,0] neg_lo:[1,0,0] neg_hi:[1,0,0]
	s_cbranch_vccnz .LBB0_146
	v_mov_b32_e32 v89, v91
	v_mov_b32_e32 v93, v95
	v_mov_b32_e32 v105, v109
	v_mov_b32_e32 v107, v111
	v_pk_add_f32 v[156:157], v[156:157], v[106:107]
	v_pk_add_f32 v[154:155], v[154:155], v[104:105]
	v_pk_add_f32 v[122:123], v[122:123], v[92:93]
	v_pk_add_f32 v[120:121], v[120:121], v[88:89]
.LBB0_146:
	v_mul_f32_e32 v89, v167, v111
	v_mul_f32_e32 v90, v167, v106
	v_cvt_pk_bf16_f32 v106, v89, v90
	v_mul_f32_e32 v89, v167, v109
	v_mov_b32_e32 v114, v96
	v_mov_b32_e32 v115, v96
	v_mov_b32_e32 v96, v97
	v_mov_b32_e32 v118, v98
	v_mov_b32_e32 v119, v98
	v_mov_b32_e32 v98, v99
	v_mul_f32_e32 v90, v167, v104
	v_cvt_pk_bf16_f32 v107, v89, v90
	v_mul_f32_e32 v89, v167, v95
	v_mov_b32_e32 v116, v100
	v_mov_b32_e32 v117, v100
	v_mov_b32_e32 v100, v101
	v_mov_b32_e32 v132, v102
	v_mov_b32_e32 v133, v102
	v_mov_b32_e32 v102, v103
	v_lshlrev_b32_e32 v144, 10, v112
	v_mul_f32_e32 v90, v167, v92
	v_cvt_pk_bf16_f32 v108, v89, v90
	v_mul_f32_e32 v89, v167, v91
	v_mul_f32_e32 v88, v167, v88
	v_pk_mul_f32 v[92:93], v[84:85], v[114:115]
	v_pk_mul_f32 v[94:95], v[86:87], v[96:97]
	v_pk_mul_f32 v[96:97], v[80:81], v[118:119]
	v_pk_mul_f32 v[98:99], v[82:83], v[98:99]
	v_cvt_pk_bf16_f32 v109, v89, v88
	v_lshl_add_u64 v[88:89], v[158:159], 0, v[144:145]
	v_pk_fma_f32 v[90:91], v[84:85], v[116:117], v[92:93] op_sel:[0,0,1] op_sel_hi:[1,1,0]
	v_pk_fma_f32 v[84:85], v[84:85], v[116:117], v[92:93] op_sel:[0,0,1] op_sel_hi:[1,1,0] neg_lo:[1,0,0] neg_hi:[1,0,0]
	v_pk_fma_f32 v[92:93], v[86:87], v[100:101], v[94:95] op_sel:[0,0,1] op_sel_hi:[1,1,0]
	v_pk_fma_f32 v[94:95], v[86:87], v[100:101], v[94:95] op_sel:[0,0,1] op_sel_hi:[1,1,0] neg_lo:[1,0,0] neg_hi:[1,0,0]
	v_pk_fma_f32 v[86:87], v[80:81], v[132:133], v[96:97] op_sel:[0,0,1] op_sel_hi:[1,1,0]
	v_pk_fma_f32 v[80:81], v[80:81], v[132:133], v[96:97] op_sel:[0,0,1] op_sel_hi:[1,1,0] neg_lo:[1,0,0] neg_hi:[1,0,0]
	v_pk_fma_f32 v[96:97], v[82:83], v[102:103], v[98:99] op_sel:[0,0,1] op_sel_hi:[1,1,0]
	s_and_b64 vcc, exec, s[8:9]
	v_pk_fma_f32 v[82:83], v[82:83], v[102:103], v[98:99] op_sel:[0,0,1] op_sel_hi:[1,1,0] neg_lo:[1,0,0] neg_hi:[1,0,0]
	flat_store_dwordx4 v[88:89], v[106:109] sc1
	s_cbranch_vccnz .LBB0_148
	v_mov_b32_e32 v97, v83
	v_mov_b32_e32 v87, v81
	v_mov_b32_e32 v93, v95
	v_mov_b32_e32 v91, v85
	v_pk_add_f32 v[130:131], v[130:131], v[90:91]
	v_pk_add_f32 v[128:129], v[128:129], v[92:93]
	v_pk_add_f32 v[126:127], v[126:127], v[86:87]
	v_pk_add_f32 v[124:125], v[124:125], v[96:97]
.LBB0_148:
	v_mul_f32_e32 v80, v167, v85
	v_mul_f32_e32 v82, v167, v90
	v_cvt_pk_bf16_f32 v90, v80, v82
	v_mul_f32_e32 v80, v167, v95
	v_mul_f32_e32 v82, v167, v92
	v_cvt_pk_bf16_f32 v91, v80, v82
	v_mul_f32_e32 v80, v167, v81
	v_mul_f32_e32 v81, v167, v86
	v_cvt_pk_bf16_f32 v92, v80, v81
	v_mul_f32_e32 v80, v167, v83
	v_mul_f32_e32 v81, v167, v96
	v_add_u32_e32 v96, 48, v190
	v_cvt_pk_bf16_f32 v93, v80, v81
	v_lshlrev_b32_e32 v80, 7, v96
	v_and_or_b32 v144, v80, s78, v182
	v_lshl_add_u64 v[80:81], s[54:55], 0, v[144:145]
	flat_load_dwordx4 v[80:83], v[80:81]
	v_lshl_add_u64 v[84:85], s[52:53], 0, v[144:145]
	flat_load_dwordx4 v[84:87], v[84:85]
	s_and_b64 vcc, exec, s[8:9]
	flat_store_dwordx4 v[88:89], v[90:93] offset:256 sc1
	s_waitcnt vmcnt(0) lgkmcnt(0)
	v_pk_mul_f32 v[88:89], v[76:77], v[80:81] op_sel_hi:[1,0]
	v_pk_mul_f32 v[92:93], v[78:79], v[80:81] op_sel:[0,1]
	v_pk_mul_f32 v[98:99], v[72:73], v[82:83] op_sel_hi:[1,0]
	v_mov_b32_e32 v100, v83
	v_mov_b32_e32 v102, v87
	v_pk_fma_f32 v[90:91], v[76:77], v[84:85], v[88:89] op_sel:[0,0,1] op_sel_hi:[1,0,0]
	v_pk_fma_f32 v[94:95], v[76:77], v[84:85], v[88:89] op_sel:[0,0,1] op_sel_hi:[1,0,0] neg_lo:[1,0,0] neg_hi:[1,0,0]
	v_pk_fma_f32 v[88:89], v[78:79], v[84:85], v[92:93] op_sel:[0,1,1] op_sel_hi:[1,1,0]
	v_pk_fma_f32 v[92:93], v[78:79], v[84:85], v[92:93] op_sel:[0,1,1] op_sel_hi:[1,1,0] neg_lo:[1,0,0] neg_hi:[1,0,0]
	v_pk_fma_f32 v[76:77], v[72:73], v[86:87], v[98:99] op_sel:[0,0,1] op_sel_hi:[1,0,0]
	v_pk_fma_f32 v[78:79], v[72:73], v[86:87], v[98:99] op_sel:[0,0,1] op_sel_hi:[1,0,0] neg_lo:[1,0,0] neg_hi:[1,0,0]
	v_pk_mul_f32 v[98:99], v[74:75], v[100:101] op_sel_hi:[1,0]
	s_nop 0
	v_pk_fma_f32 v[72:73], v[74:75], v[102:103], v[98:99] op_sel:[0,0,1] op_sel_hi:[1,0,0]
	v_pk_fma_f32 v[74:75], v[74:75], v[102:103], v[98:99] op_sel:[0,0,1] op_sel_hi:[1,0,0] neg_lo:[1,0,0] neg_hi:[1,0,0]
	s_cbranch_vccnz .LBB0_150
	v_mov_b32_e32 v73, v75
	v_mov_b32_e32 v77, v79
	v_mov_b32_e32 v89, v93
	v_mov_b32_e32 v91, v95
	v_pk_add_f32 v[156:157], v[156:157], v[90:91]
	v_pk_add_f32 v[154:155], v[154:155], v[88:89]
	v_pk_add_f32 v[122:123], v[122:123], v[76:77]
	v_pk_add_f32 v[120:121], v[120:121], v[72:73]
; __device__ __forceinline__ unsigned cvt_pk_bf16(float lo, float hi) { unsigned r; asm volatile("v_cvt_pk_bf16_f32 %0, %1, %2" : "=v"(r) : "v"(lo), "v"(hi)); return r; }
;     __device__ __forceinline__ void operator()(const f32x4 (&acc)[2][2][4][2], const Unit& u, int wr, int wc, int fr, int fq) const {
;     ...
;                 for (int m = 0; m < 4; ++m) {
;                     const int row = row0 + ai * HALF + m * 16, pos = row & 4095;
;                     const unsigned ro = (unsigned)(pos * 32 + i0) * 4u; const f32x4 c4 = *(const f32x4*)(cs + ro), s4 = *(const f32x4*)(sn + ro);
; #pragma unroll
;                     for (int bj = 0; bj < 2; ++bj) {
;                         const f32x4 v0 = acc[ai][bj][m][0], v1 = acc[ai][bj][m][1];
;                         float o[8];
;                         o[0] = v0[0] * c4[0] - v0[1] * s4[0]; o[1] = v0[1] * c4[0] + v0[0] * s4[0];
;                         o[2] = v0[2] * c4[1] - v0[3] * s4[1]; o[3] = v0[3] * c4[1] + v0[2] * s4[1];
;                         o[4] = v1[0] * c4[2] - v1[1] * s4[2]; o[5] = v1[1] * c4[2] + v1[0] * s4[2];
;                         o[6] = v1[2] * c4[3] - v1[3] * s4[3]; o[7] = v1[3] * c4[3] + v1[2] * s4[3];
;                         if (!isq) {
; #pragma unroll
;                             for (int e = 0; e < 8; ++e) ks[bj][e] += o[e]; }
;                         u32x4 w; w.x = cvt_pk_bf16(o[0] * sc, o[1] * sc); w.y = cvt_pk_bf16(o[2] * sc, o[3] * sc); w.z = cvt_pk_bf16(o[4] * sc, o[5] * sc); w.w = cvt_pk_bf16(o[6] * sc, o[7] * sc);
;                         *(u32x4*)(base + (unsigned)(row * 512 + bj * HALF) * 2u) = w;
.LBB0_150:
	v_mul_f32_e32 v73, v167, v95
	v_mul_f32_e32 v74, v167, v90
	v_cvt_pk_bf16_f32 v90, v73, v74
	v_mul_f32_e32 v73, v167, v93
	v_mov_b32_e32 v98, v80
	v_mov_b32_e32 v99, v80
	v_mov_b32_e32 v80, v81
	v_mov_b32_e32 v102, v82
	v_mov_b32_e32 v103, v82
	v_mov_b32_e32 v82, v83
	v_mul_f32_e32 v74, v167, v88
	v_cvt_pk_bf16_f32 v91, v73, v74
	v_mul_f32_e32 v73, v167, v79
	v_mov_b32_e32 v100, v84
	v_mov_b32_e32 v101, v84
	v_mov_b32_e32 v84, v85
	v_mov_b32_e32 v104, v86
	v_mov_b32_e32 v105, v86
	v_mov_b32_e32 v86, v87
	v_lshlrev_b32_e32 v144, 10, v96
	v_mul_f32_e32 v74, v167, v76
	v_cvt_pk_bf16_f32 v92, v73, v74
	v_mul_f32_e32 v73, v167, v75
	v_mul_f32_e32 v72, v167, v72
	v_pk_mul_f32 v[76:77], v[68:69], v[98:99]
	v_pk_mul_f32 v[78:79], v[70:71], v[80:81]
	v_pk_mul_f32 v[80:81], v[64:65], v[102:103]
	v_pk_mul_f32 v[82:83], v[66:67], v[82:83]
	v_cvt_pk_bf16_f32 v93, v73, v72
	v_lshl_add_u64 v[72:73], v[158:159], 0, v[144:145]
	v_pk_fma_f32 v[74:75], v[68:69], v[100:101], v[76:77] op_sel:[0,0,1] op_sel_hi:[1,1,0]
	v_pk_fma_f32 v[68:69], v[68:69], v[100:101], v[76:77] op_sel:[0,0,1] op_sel_hi:[1,1,0] neg_lo:[1,0,0] neg_hi:[1,0,0]
	v_pk_fma_f32 v[76:77], v[70:71], v[84:85], v[78:79] op_sel:[0,0,1] op_sel_hi:[1,1,0]
	v_pk_fma_f32 v[78:79], v[70:71], v[84:85], v[78:79] op_sel:[0,0,1] op_sel_hi:[1,1,0] neg_lo:[1,0,0] neg_hi:[1,0,0]
	v_pk_fma_f32 v[70:71], v[64:65], v[104:105], v[80:81] op_sel:[0,0,1] op_sel_hi:[1,1,0]
	v_pk_fma_f32 v[64:65], v[64:65], v[104:105], v[80:81] op_sel:[0,0,1] op_sel_hi:[1,1,0] neg_lo:[1,0,0] neg_hi:[1,0,0]
	v_pk_fma_f32 v[80:81], v[66:67], v[86:87], v[82:83] op_sel:[0,0,1] op_sel_hi:[1,1,0]
	s_and_b64 vcc, exec, s[8:9]
	v_pk_fma_f32 v[66:67], v[66:67], v[86:87], v[82:83] op_sel:[0,0,1] op_sel_hi:[1,1,0] neg_lo:[1,0,0] neg_hi:[1,0,0]
	flat_store_dwordx4 v[72:73], v[90:93] sc1
	s_cbranch_vccnz .LBB0_152
	v_mov_b32_e32 v81, v67
	v_mov_b32_e32 v71, v65
	v_mov_b32_e32 v77, v79
	v_mov_b32_e32 v75, v69
	v_pk_add_f32 v[130:131], v[130:131], v[74:75]
	v_pk_add_f32 v[128:129], v[128:129], v[76:77]
	v_pk_add_f32 v[126:127], v[126:127], v[70:71]
	v_pk_add_f32 v[124:125], v[124:125], v[80:81]
.LBB0_152:
	v_mul_f32_e32 v64, v167, v69
	v_mul_f32_e32 v66, v167, v74
	v_cvt_pk_bf16_f32 v74, v64, v66
	v_mul_f32_e32 v64, v167, v79
	v_mul_f32_e32 v66, v167, v76
	v_cvt_pk_bf16_f32 v75, v64, v66
	v_mul_f32_e32 v64, v167, v65
	v_mul_f32_e32 v65, v167, v70
	v_cvt_pk_bf16_f32 v76, v64, v65
	v_mul_f32_e32 v64, v167, v67
	v_mul_f32_e32 v65, v167, v80
	v_add_u32_e32 v80, 0x80, v190
	v_cvt_pk_bf16_f32 v77, v64, v65
	v_lshlrev_b32_e32 v64, 7, v80
	v_and_or_b32 v144, v64, s78, v182
	v_lshl_add_u64 v[64:65], s[54:55], 0, v[144:145]
	flat_load_dwordx4 v[64:67], v[64:65]
	v_lshl_add_u64 v[68:69], s[52:53], 0, v[144:145]
	flat_load_dwordx4 v[68:71], v[68:69]
	s_and_b64 vcc, exec, s[8:9]
	flat_store_dwordx4 v[72:73], v[74:77] offset:256 sc1
	s_waitcnt vmcnt(0) lgkmcnt(0)
	v_pk_mul_f32 v[72:73], v[60:61], v[64:65] op_sel_hi:[1,0]
	v_pk_mul_f32 v[76:77], v[62:63], v[64:65] op_sel:[0,1]
	v_pk_mul_f32 v[82:83], v[56:57], v[66:67] op_sel_hi:[1,0]
	v_mov_b32_e32 v84, v67
	v_mov_b32_e32 v86, v71
	v_pk_fma_f32 v[74:75], v[60:61], v[68:69], v[72:73] op_sel:[0,0,1] op_sel_hi:[1,0,0]
	v_pk_fma_f32 v[78:79], v[60:61], v[68:69], v[72:73] op_sel:[0,0,1] op_sel_hi:[1,0,0] neg_lo:[1,0,0] neg_hi:[1,0,0]
	v_pk_fma_f32 v[72:73], v[62:63], v[68:69], v[76:77] op_sel:[0,1,1] op_sel_hi:[1,1,0]
	v_pk_fma_f32 v[76:77], v[62:63], v[68:69], v[76:77] op_sel:[0,1,1] op_sel_hi:[1,1,0] neg_lo:[1,0,0] neg_hi:[1,0,0]
	v_pk_fma_f32 v[60:61], v[56:57], v[70:71], v[82:83] op_sel:[0,0,1] op_sel_hi:[1,0,0]
	v_pk_fma_f32 v[62:63], v[56:57], v[70:71], v[82:83] op_sel:[0,0,1] op_sel_hi:[1,0,0] neg_lo:[1,0,0] neg_hi:[1,0,0]
	v_pk_mul_f32 v[82:83], v[58:59], v[84:85] op_sel_hi:[1,0]
	s_nop 0
	v_pk_fma_f32 v[56:57], v[58:59], v[86:87], v[82:83] op_sel:[0,0,1] op_sel_hi:[1,0,0]
	v_pk_fma_f32 v[58:59], v[58:59], v[86:87], v[82:83] op_sel:[0,0,1] op_sel_hi:[1,0,0] neg_lo:[1,0,0] neg_hi:[1,0,0]
	s_cbranch_vccnz .LBB0_154
	v_mov_b32_e32 v57, v59
	v_mov_b32_e32 v61, v63
	v_mov_b32_e32 v73, v77
	v_mov_b32_e32 v75, v79
	v_pk_add_f32 v[156:157], v[156:157], v[74:75]
	v_pk_add_f32 v[154:155], v[154:155], v[72:73]
	v_pk_add_f32 v[122:123], v[122:123], v[60:61]
	v_pk_add_f32 v[120:121], v[120:121], v[56:57]
.LBB0_154:
	v_mul_f32_e32 v57, v167, v79
	v_mul_f32_e32 v58, v167, v74
	v_cvt_pk_bf16_f32 v74, v57, v58
	v_mul_f32_e32 v57, v167, v77
	v_mov_b32_e32 v82, v64
	v_mov_b32_e32 v83, v64
	v_mov_b32_e32 v64, v65
	v_mov_b32_e32 v86, v66
	v_mov_b32_e32 v87, v66
	v_mov_b32_e32 v66, v67
	v_mul_f32_e32 v58, v167, v72
	v_cvt_pk_bf16_f32 v75, v57, v58
	v_mul_f32_e32 v57, v167, v63
	v_mov_b32_e32 v84, v68
	v_mov_b32_e32 v85, v68
	v_mov_b32_e32 v68, v69
	v_mov_b32_e32 v88, v70
	v_mov_b32_e32 v89, v70
	v_mov_b32_e32 v70, v71
	v_lshlrev_b32_e32 v144, 10, v80
	v_mul_f32_e32 v58, v167, v60
	v_cvt_pk_bf16_f32 v76, v57, v58
	v_mul_f32_e32 v57, v167, v59
	v_mul_f32_e32 v56, v167, v56
	v_pk_mul_f32 v[60:61], v[52:53], v[82:83]
	v_pk_mul_f32 v[62:63], v[54:55], v[64:65]
	v_pk_mul_f32 v[64:65], v[48:49], v[86:87]
	v_pk_mul_f32 v[66:67], v[50:51], v[66:67]
	v_cvt_pk_bf16_f32 v77, v57, v56
	v_lshl_add_u64 v[56:57], v[158:159], 0, v[144:145]
	v_pk_fma_f32 v[58:59], v[52:53], v[84:85], v[60:61] op_sel:[0,0,1] op_sel_hi:[1,1,0]
	v_pk_fma_f32 v[52:53], v[52:53], v[84:85], v[60:61] op_sel:[0,0,1] op_sel_hi:[1,1,0] neg_lo:[1,0,0] neg_hi:[1,0,0]
	v_pk_fma_f32 v[60:61], v[54:55], v[68:69], v[62:63] op_sel:[0,0,1] op_sel_hi:[1,1,0]
	v_pk_fma_f32 v[62:63], v[54:55], v[68:69], v[62:63] op_sel:[0,0,1] op_sel_hi:[1,1,0] neg_lo:[1,0,0] neg_hi:[1,0,0]
	v_pk_fma_f32 v[54:55], v[48:49], v[88:89], v[64:65] op_sel:[0,0,1] op_sel_hi:[1,1,0]
	v_pk_fma_f32 v[48:49], v[48:49], v[88:89], v[64:65] op_sel:[0,0,1] op_sel_hi:[1,1,0] neg_lo:[1,0,0] neg_hi:[1,0,0]
	v_pk_fma_f32 v[64:65], v[50:51], v[70:71], v[66:67] op_sel:[0,0,1] op_sel_hi:[1,1,0]
	s_and_b64 vcc, exec, s[8:9]
	v_pk_fma_f32 v[50:51], v[50:51], v[70:71], v[66:67] op_sel:[0,0,1] op_sel_hi:[1,1,0] neg_lo:[1,0,0] neg_hi:[1,0,0]
	flat_store_dwordx4 v[56:57], v[74:77] sc1
	s_cbranch_vccnz .LBB0_156
	v_mov_b32_e32 v65, v51
	v_mov_b32_e32 v55, v49
	v_mov_b32_e32 v61, v63
	v_mov_b32_e32 v59, v53
	v_pk_add_f32 v[130:131], v[130:131], v[58:59]
	v_pk_add_f32 v[128:129], v[128:129], v[60:61]
	v_pk_add_f32 v[126:127], v[126:127], v[54:55]
	v_pk_add_f32 v[124:125], v[124:125], v[64:65]
; __device__ __forceinline__ unsigned cvt_pk_bf16(float lo, float hi) { unsigned r; asm volatile("v_cvt_pk_bf16_f32 %0, %1, %2" : "=v"(r) : "v"(lo), "v"(hi)); return r; }
;     __device__ __forceinline__ void operator()(const f32x4 (&acc)[2][2][4][2], const Unit& u, int wr, int wc, int fr, int fq) const {
;     ...
;                 for (int m = 0; m < 4; ++m) {
;                     const int row = row0 + ai * HALF + m * 16, pos = row & 4095;
;                     const unsigned ro = (unsigned)(pos * 32 + i0) * 4u; const f32x4 c4 = *(const f32x4*)(cs + ro), s4 = *(const f32x4*)(sn + ro);
; #pragma unroll
;                     for (int bj = 0; bj < 2; ++bj) {
;                         const f32x4 v0 = acc[ai][bj][m][0], v1 = acc[ai][bj][m][1];
;                         float o[8];
;                         o[0] = v0[0] * c4[0] - v0[1] * s4[0]; o[1] = v0[1] * c4[0] + v0[0] * s4[0];
;                         o[2] = v0[2] * c4[1] - v0[3] * s4[1]; o[3] = v0[3] * c4[1] + v0[2] * s4[1];
;                         o[4] = v1[0] * c4[2] - v1[1] * s4[2]; o[5] = v1[1] * c4[2] + v1[0] * s4[2];
;                         o[6] = v1[2] * c4[3] - v1[3] * s4[3]; o[7] = v1[3] * c4[3] + v1[2] * s4[3];
;                         if (!isq) {
; #pragma unroll
;                             for (int e = 0; e < 8; ++e) ks[bj][e] += o[e]; }
;                         u32x4 w; w.x = cvt_pk_bf16(o[0] * sc, o[1] * sc); w.y = cvt_pk_bf16(o[2] * sc, o[3] * sc); w.z = cvt_pk_bf16(o[4] * sc, o[5] * sc); w.w = cvt_pk_bf16(o[6] * sc, o[7] * sc);
;                         *(u32x4*)(base + (unsigned)(row * 512 + bj * HALF) * 2u) = w;
.LBB0_156:
	v_mul_f32_e32 v48, v167, v53
	v_mul_f32_e32 v50, v167, v58
	v_cvt_pk_bf16_f32 v58, v48, v50
	v_mul_f32_e32 v48, v167, v63
	v_mul_f32_e32 v50, v167, v60
	v_cvt_pk_bf16_f32 v59, v48, v50
	v_mul_f32_e32 v48, v167, v49
	v_mul_f32_e32 v49, v167, v54
	v_cvt_pk_bf16_f32 v60, v48, v49
	v_mul_f32_e32 v48, v167, v51
	v_mul_f32_e32 v49, v167, v64
	v_add_u32_e32 v64, 0x90, v190
	v_cvt_pk_bf16_f32 v61, v48, v49
	v_lshlrev_b32_e32 v48, 7, v64
	v_and_or_b32 v144, v48, s78, v182
	v_lshl_add_u64 v[48:49], s[54:55], 0, v[144:145]
	flat_load_dwordx4 v[48:51], v[48:49]
	v_lshl_add_u64 v[52:53], s[52:53], 0, v[144:145]
	flat_load_dwordx4 v[52:55], v[52:53]
	s_and_b64 vcc, exec, s[8:9]
	flat_store_dwordx4 v[56:57], v[58:61] offset:256 sc1
	s_waitcnt vmcnt(0) lgkmcnt(0)
	v_pk_mul_f32 v[56:57], v[44:45], v[48:49] op_sel_hi:[1,0]
	v_pk_mul_f32 v[60:61], v[46:47], v[48:49] op_sel:[0,1]
	v_pk_mul_f32 v[66:67], v[40:41], v[50:51] op_sel_hi:[1,0]
	v_mov_b32_e32 v68, v51
	v_mov_b32_e32 v70, v55
	v_pk_fma_f32 v[58:59], v[44:45], v[52:53], v[56:57] op_sel:[0,0,1] op_sel_hi:[1,0,0]
	v_pk_fma_f32 v[62:63], v[44:45], v[52:53], v[56:57] op_sel:[0,0,1] op_sel_hi:[1,0,0] neg_lo:[1,0,0] neg_hi:[1,0,0]
	v_pk_fma_f32 v[56:57], v[46:47], v[52:53], v[60:61] op_sel:[0,1,1] op_sel_hi:[1,1,0]
	v_pk_fma_f32 v[60:61], v[46:47], v[52:53], v[60:61] op_sel:[0,1,1] op_sel_hi:[1,1,0] neg_lo:[1,0,0] neg_hi:[1,0,0]
	v_pk_fma_f32 v[44:45], v[40:41], v[54:55], v[66:67] op_sel:[0,0,1] op_sel_hi:[1,0,0]
	v_pk_fma_f32 v[46:47], v[40:41], v[54:55], v[66:67] op_sel:[0,0,1] op_sel_hi:[1,0,0] neg_lo:[1,0,0] neg_hi:[1,0,0]
	v_pk_mul_f32 v[66:67], v[42:43], v[68:69] op_sel_hi:[1,0]
	s_nop 0
	v_pk_fma_f32 v[40:41], v[42:43], v[70:71], v[66:67] op_sel:[0,0,1] op_sel_hi:[1,0,0]
	v_pk_fma_f32 v[42:43], v[42:43], v[70:71], v[66:67] op_sel:[0,0,1] op_sel_hi:[1,0,0] neg_lo:[1,0,0] neg_hi:[1,0,0]
	s_cbranch_vccnz .LBB0_158
	v_mov_b32_e32 v41, v43
	v_mov_b32_e32 v45, v47
	v_mov_b32_e32 v57, v61
	v_mov_b32_e32 v59, v63
	v_pk_add_f32 v[156:157], v[156:157], v[58:59]
	v_pk_add_f32 v[154:155], v[154:155], v[56:57]
	v_pk_add_f32 v[122:123], v[122:123], v[44:45]
	v_pk_add_f32 v[120:121], v[120:121], v[40:41]
.LBB0_158:
	v_mul_f32_e32 v41, v167, v63
	v_mul_f32_e32 v42, v167, v58
	v_cvt_pk_bf16_f32 v58, v41, v42
	v_mul_f32_e32 v41, v167, v61
	v_mov_b32_e32 v66, v48
	v_mov_b32_e32 v67, v48
	v_mov_b32_e32 v48, v49
	v_mov_b32_e32 v70, v50
	v_mov_b32_e32 v71, v50
	v_mov_b32_e32 v50, v51
	v_mul_f32_e32 v42, v167, v56
	v_cvt_pk_bf16_f32 v59, v41, v42
	v_mul_f32_e32 v41, v167, v47
	v_mov_b32_e32 v68, v52
	v_mov_b32_e32 v69, v52
	v_mov_b32_e32 v52, v53
	v_mov_b32_e32 v72, v54
	v_mov_b32_e32 v73, v54
	v_mov_b32_e32 v54, v55
	v_lshlrev_b32_e32 v144, 10, v64
	v_mul_f32_e32 v42, v167, v44
	v_cvt_pk_bf16_f32 v60, v41, v42
	v_mul_f32_e32 v41, v167, v43
	v_mul_f32_e32 v40, v167, v40
	v_pk_mul_f32 v[44:45], v[36:37], v[66:67]
	v_pk_mul_f32 v[46:47], v[38:39], v[48:49]
	v_pk_mul_f32 v[48:49], v[32:33], v[70:71]
	v_pk_mul_f32 v[50:51], v[34:35], v[50:51]
	v_cvt_pk_bf16_f32 v61, v41, v40
	v_lshl_add_u64 v[40:41], v[158:159], 0, v[144:145]
	v_pk_fma_f32 v[42:43], v[36:37], v[68:69], v[44:45] op_sel:[0,0,1] op_sel_hi:[1,1,0]
	v_pk_fma_f32 v[36:37], v[36:37], v[68:69], v[44:45] op_sel:[0,0,1] op_sel_hi:[1,1,0] neg_lo:[1,0,0] neg_hi:[1,0,0]
	v_pk_fma_f32 v[44:45], v[38:39], v[52:53], v[46:47] op_sel:[0,0,1] op_sel_hi:[1,1,0]
	v_pk_fma_f32 v[46:47], v[38:39], v[52:53], v[46:47] op_sel:[0,0,1] op_sel_hi:[1,1,0] neg_lo:[1,0,0] neg_hi:[1,0,0]
	v_pk_fma_f32 v[38:39], v[32:33], v[72:73], v[48:49] op_sel:[0,0,1] op_sel_hi:[1,1,0]
	v_pk_fma_f32 v[32:33], v[32:33], v[72:73], v[48:49] op_sel:[0,0,1] op_sel_hi:[1,1,0] neg_lo:[1,0,0] neg_hi:[1,0,0]
	v_pk_fma_f32 v[48:49], v[34:35], v[54:55], v[50:51] op_sel:[0,0,1] op_sel_hi:[1,1,0]
	s_and_b64 vcc, exec, s[8:9]
	v_pk_fma_f32 v[34:35], v[34:35], v[54:55], v[50:51] op_sel:[0,0,1] op_sel_hi:[1,1,0] neg_lo:[1,0,0] neg_hi:[1,0,0]
	flat_store_dwordx4 v[40:41], v[58:61] sc1
	s_cbranch_vccnz .LBB0_160
	v_mov_b32_e32 v49, v35
	v_mov_b32_e32 v39, v33
	v_mov_b32_e32 v45, v47
	v_mov_b32_e32 v43, v37
	v_pk_add_f32 v[130:131], v[130:131], v[42:43]
	v_pk_add_f32 v[128:129], v[128:129], v[44:45]
	v_pk_add_f32 v[126:127], v[126:127], v[38:39]
	v_pk_add_f32 v[124:125], v[124:125], v[48:49]
.LBB0_160:
	v_mul_f32_e32 v32, v167, v37
	v_mul_f32_e32 v34, v167, v42
	v_cvt_pk_bf16_f32 v42, v32, v34
	v_mul_f32_e32 v32, v167, v47
	v_mul_f32_e32 v34, v167, v44
	v_cvt_pk_bf16_f32 v43, v32, v34
	v_mul_f32_e32 v32, v167, v33
	v_mul_f32_e32 v33, v167, v38
	v_cvt_pk_bf16_f32 v44, v32, v33
	v_mul_f32_e32 v32, v167, v35
	v_mul_f32_e32 v33, v167, v48
	v_add_u32_e32 v48, 0xa0, v190
	v_cvt_pk_bf16_f32 v45, v32, v33
	v_lshlrev_b32_e32 v32, 7, v48
	v_and_or_b32 v144, v32, s78, v182
	v_lshl_add_u64 v[32:33], s[54:55], 0, v[144:145]
	flat_load_dwordx4 v[32:35], v[32:33]
	v_lshl_add_u64 v[36:37], s[52:53], 0, v[144:145]
	flat_load_dwordx4 v[36:39], v[36:37]
	s_and_b64 vcc, exec, s[8:9]
	flat_store_dwordx4 v[40:41], v[42:45] offset:256 sc1
	s_waitcnt vmcnt(0) lgkmcnt(0)
	v_pk_mul_f32 v[40:41], v[28:29], v[32:33] op_sel_hi:[1,0]
	v_pk_mul_f32 v[44:45], v[30:31], v[32:33] op_sel:[0,1]
	v_pk_mul_f32 v[50:51], v[24:25], v[34:35] op_sel_hi:[1,0]
	v_mov_b32_e32 v52, v35
	v_mov_b32_e32 v54, v39
	v_pk_fma_f32 v[42:43], v[28:29], v[36:37], v[40:41] op_sel:[0,0,1] op_sel_hi:[1,0,0]
	v_pk_fma_f32 v[46:47], v[28:29], v[36:37], v[40:41] op_sel:[0,0,1] op_sel_hi:[1,0,0] neg_lo:[1,0,0] neg_hi:[1,0,0]
	v_pk_fma_f32 v[40:41], v[30:31], v[36:37], v[44:45] op_sel:[0,1,1] op_sel_hi:[1,1,0]
	v_pk_fma_f32 v[44:45], v[30:31], v[36:37], v[44:45] op_sel:[0,1,1] op_sel_hi:[1,1,0] neg_lo:[1,0,0] neg_hi:[1,0,0]
	v_pk_fma_f32 v[28:29], v[24:25], v[38:39], v[50:51] op_sel:[0,0,1] op_sel_hi:[1,0,0]
	v_pk_fma_f32 v[30:31], v[24:25], v[38:39], v[50:51] op_sel:[0,0,1] op_sel_hi:[1,0,0] neg_lo:[1,0,0] neg_hi:[1,0,0]
	v_pk_mul_f32 v[50:51], v[26:27], v[52:53] op_sel_hi:[1,0]
	s_nop 0
	v_pk_fma_f32 v[24:25], v[26:27], v[54:55], v[50:51] op_sel:[0,0,1] op_sel_hi:[1,0,0]
	v_pk_fma_f32 v[26:27], v[26:27], v[54:55], v[50:51] op_sel:[0,0,1] op_sel_hi:[1,0,0] neg_lo:[1,0,0] neg_hi:[1,0,0]
	s_cbranch_vccnz .LBB0_162
	v_mov_b32_e32 v25, v27
	v_mov_b32_e32 v29, v31
	v_mov_b32_e32 v41, v45
	v_mov_b32_e32 v43, v47
	v_pk_add_f32 v[156:157], v[156:157], v[42:43]
	v_pk_add_f32 v[154:155], v[154:155], v[40:41]
	v_pk_add_f32 v[122:123], v[122:123], v[28:29]
	v_pk_add_f32 v[120:121], v[120:121], v[24:25]
; __device__ __forceinline__ unsigned cvt_pk_bf16(float lo, float hi) { unsigned r; asm volatile("v_cvt_pk_bf16_f32 %0, %1, %2" : "=v"(r) : "v"(lo), "v"(hi)); return r; }
;     __device__ __forceinline__ void operator()(const f32x4 (&acc)[2][2][4][2], const Unit& u, int wr, int wc, int fr, int fq) const {
;     ...
;                 for (int m = 0; m < 4; ++m) {
;                     const int row = row0 + ai * HALF + m * 16, pos = row & 4095;
;                     const unsigned ro = (unsigned)(pos * 32 + i0) * 4u; const f32x4 c4 = *(const f32x4*)(cs + ro), s4 = *(const f32x4*)(sn + ro);
; #pragma unroll
;                     for (int bj = 0; bj < 2; ++bj) {
;                         const f32x4 v0 = acc[ai][bj][m][0], v1 = acc[ai][bj][m][1];
;                         float o[8];
;                         o[0] = v0[0] * c4[0] - v0[1] * s4[0]; o[1] = v0[1] * c4[0] + v0[0] * s4[0];
;                         o[2] = v0[2] * c4[1] - v0[3] * s4[1]; o[3] = v0[3] * c4[1] + v0[2] * s4[1];
;                         o[4] = v1[0] * c4[2] - v1[1] * s4[2]; o[5] = v1[1] * c4[2] + v1[0] * s4[2];
;                         o[6] = v1[2] * c4[3] - v1[3] * s4[3]; o[7] = v1[3] * c4[3] + v1[2] * s4[3];
;                         if (!isq) {
; #pragma unroll
;                             for (int e = 0; e < 8; ++e) ks[bj][e] += o[e]; }
;                         u32x4 w; w.x = cvt_pk_bf16(o[0] * sc, o[1] * sc); w.y = cvt_pk_bf16(o[2] * sc, o[3] * sc); w.z = cvt_pk_bf16(o[4] * sc, o[5] * sc); w.w = cvt_pk_bf16(o[6] * sc, o[7] * sc);
;                         *(u32x4*)(base + (unsigned)(row * 512 + bj * HALF) * 2u) = w;
.LBB0_162:
	v_mul_f32_e32 v25, v167, v47
	v_mul_f32_e32 v26, v167, v42
	v_cvt_pk_bf16_f32 v42, v25, v26
	v_mul_f32_e32 v25, v167, v45
	v_mov_b32_e32 v50, v32
	v_mov_b32_e32 v51, v32
	v_mov_b32_e32 v32, v33
	v_mov_b32_e32 v54, v34
	v_mov_b32_e32 v55, v34
	v_mov_b32_e32 v34, v35
	v_mul_f32_e32 v26, v167, v40
	v_cvt_pk_bf16_f32 v43, v25, v26
	v_mul_f32_e32 v25, v167, v31
	v_mov_b32_e32 v52, v36
	v_mov_b32_e32 v53, v36
	v_mov_b32_e32 v36, v37
	v_mov_b32_e32 v56, v38
	v_mov_b32_e32 v57, v38
	v_mov_b32_e32 v38, v39
	v_lshlrev_b32_e32 v144, 10, v48
	v_mul_f32_e32 v26, v167, v28
	v_cvt_pk_bf16_f32 v44, v25, v26
	v_mul_f32_e32 v25, v167, v27
	v_mul_f32_e32 v24, v167, v24
	v_pk_mul_f32 v[28:29], v[20:21], v[50:51]
	v_pk_mul_f32 v[30:31], v[22:23], v[32:33]
	v_pk_mul_f32 v[32:33], v[16:17], v[54:55]
	v_pk_mul_f32 v[34:35], v[18:19], v[34:35]
	v_cvt_pk_bf16_f32 v45, v25, v24
	v_lshl_add_u64 v[24:25], v[158:159], 0, v[144:145]
	v_pk_fma_f32 v[26:27], v[20:21], v[52:53], v[28:29] op_sel:[0,0,1] op_sel_hi:[1,1,0]
	v_pk_fma_f32 v[20:21], v[20:21], v[52:53], v[28:29] op_sel:[0,0,1] op_sel_hi:[1,1,0] neg_lo:[1,0,0] neg_hi:[1,0,0]
	v_pk_fma_f32 v[28:29], v[22:23], v[36:37], v[30:31] op_sel:[0,0,1] op_sel_hi:[1,1,0]
	v_pk_fma_f32 v[30:31], v[22:23], v[36:37], v[30:31] op_sel:[0,0,1] op_sel_hi:[1,1,0] neg_lo:[1,0,0] neg_hi:[1,0,0]
	v_pk_fma_f32 v[22:23], v[16:17], v[56:57], v[32:33] op_sel:[0,0,1] op_sel_hi:[1,1,0]
	v_pk_fma_f32 v[16:17], v[16:17], v[56:57], v[32:33] op_sel:[0,0,1] op_sel_hi:[1,1,0] neg_lo:[1,0,0] neg_hi:[1,0,0]
	v_pk_fma_f32 v[32:33], v[18:19], v[38:39], v[34:35] op_sel:[0,0,1] op_sel_hi:[1,1,0]
	s_and_b64 vcc, exec, s[8:9]
	v_pk_fma_f32 v[18:19], v[18:19], v[38:39], v[34:35] op_sel:[0,0,1] op_sel_hi:[1,1,0] neg_lo:[1,0,0] neg_hi:[1,0,0]
	flat_store_dwordx4 v[24:25], v[42:45] sc1
	s_cbranch_vccnz .LBB0_164
	v_mov_b32_e32 v33, v19
	v_mov_b32_e32 v23, v17
	v_mov_b32_e32 v29, v31
	v_mov_b32_e32 v27, v21
	v_pk_add_f32 v[130:131], v[130:131], v[26:27]
	v_pk_add_f32 v[128:129], v[128:129], v[28:29]
	v_pk_add_f32 v[126:127], v[126:127], v[22:23]
	v_pk_add_f32 v[124:125], v[124:125], v[32:33]
.LBB0_164:
	v_mul_f32_e32 v16, v167, v21
	v_mul_f32_e32 v18, v167, v26
	v_cvt_pk_bf16_f32 v26, v16, v18
	v_mul_f32_e32 v16, v167, v31
	v_mul_f32_e32 v18, v167, v28
	v_cvt_pk_bf16_f32 v27, v16, v18
	v_mul_f32_e32 v16, v167, v17
	v_mul_f32_e32 v17, v167, v22
	v_cvt_pk_bf16_f32 v28, v16, v17
	v_mul_f32_e32 v16, v167, v19
	v_mul_f32_e32 v17, v167, v32
	v_add_u32_e32 v32, 0xb0, v190
	v_cvt_pk_bf16_f32 v29, v16, v17
	v_lshlrev_b32_e32 v16, 7, v32
	v_and_or_b32 v144, v16, s78, v182
	v_lshl_add_u64 v[16:17], s[54:55], 0, v[144:145]
	flat_load_dwordx4 v[16:19], v[16:17]
	v_lshl_add_u64 v[20:21], s[52:53], 0, v[144:145]
	flat_load_dwordx4 v[20:23], v[20:21]
	s_and_b64 vcc, exec, s[8:9]
	flat_store_dwordx4 v[24:25], v[26:29] offset:256 sc1
	s_waitcnt vmcnt(0) lgkmcnt(0)
	v_pk_mul_f32 v[24:25], v[12:13], v[16:17] op_sel_hi:[1,0]
	v_pk_mul_f32 v[28:29], v[14:15], v[16:17] op_sel:[0,1]
	v_pk_mul_f32 v[34:35], v[8:9], v[18:19] op_sel_hi:[1,0]
	v_mov_b32_e32 v36, v19
	v_mov_b32_e32 v38, v23
	v_pk_fma_f32 v[26:27], v[12:13], v[20:21], v[24:25] op_sel:[0,0,1] op_sel_hi:[1,0,0]
	v_pk_fma_f32 v[30:31], v[12:13], v[20:21], v[24:25] op_sel:[0,0,1] op_sel_hi:[1,0,0] neg_lo:[1,0,0] neg_hi:[1,0,0]
	v_pk_fma_f32 v[24:25], v[14:15], v[20:21], v[28:29] op_sel:[0,1,1] op_sel_hi:[1,1,0]
	v_pk_fma_f32 v[28:29], v[14:15], v[20:21], v[28:29] op_sel:[0,1,1] op_sel_hi:[1,1,0] neg_lo:[1,0,0] neg_hi:[1,0,0]
	v_pk_fma_f32 v[12:13], v[8:9], v[22:23], v[34:35] op_sel:[0,0,1] op_sel_hi:[1,0,0]
	v_pk_fma_f32 v[14:15], v[8:9], v[22:23], v[34:35] op_sel:[0,0,1] op_sel_hi:[1,0,0] neg_lo:[1,0,0] neg_hi:[1,0,0]
	v_pk_mul_f32 v[34:35], v[10:11], v[36:37] op_sel_hi:[1,0]
	s_nop 0
	v_pk_fma_f32 v[8:9], v[10:11], v[38:39], v[34:35] op_sel:[0,0,1] op_sel_hi:[1,0,0]
	v_pk_fma_f32 v[10:11], v[10:11], v[38:39], v[34:35] op_sel:[0,0,1] op_sel_hi:[1,0,0] neg_lo:[1,0,0] neg_hi:[1,0,0]
	s_cbranch_vccnz .LBB0_166
	v_mov_b32_e32 v9, v11
	v_mov_b32_e32 v13, v15
	v_mov_b32_e32 v25, v29
	v_mov_b32_e32 v27, v31
	v_pk_add_f32 v[156:157], v[156:157], v[26:27]
	v_pk_add_f32 v[154:155], v[154:155], v[24:25]
	v_pk_add_f32 v[122:123], v[122:123], v[12:13]
	v_pk_add_f32 v[120:121], v[120:121], v[8:9]
.LBB0_166:
	v_mul_f32_e32 v9, v167, v31
	v_mul_f32_e32 v10, v167, v26
	v_cvt_pk_bf16_f32 v26, v9, v10
	v_mul_f32_e32 v9, v167, v29
	v_mov_b32_e32 v34, v16
	v_mov_b32_e32 v35, v16
	v_mov_b32_e32 v16, v17
	v_mov_b32_e32 v38, v18
	v_mov_b32_e32 v39, v18
	v_mov_b32_e32 v18, v19
	v_mul_f32_e32 v10, v167, v24
	v_cvt_pk_bf16_f32 v27, v9, v10
	v_mul_f32_e32 v9, v167, v15
	v_mov_b32_e32 v36, v20
	v_mov_b32_e32 v37, v20
	v_mov_b32_e32 v20, v21
	v_mov_b32_e32 v40, v22
	v_mov_b32_e32 v41, v22
	v_mov_b32_e32 v22, v23
	v_lshlrev_b32_e32 v144, 10, v32
	v_mul_f32_e32 v10, v167, v12
	v_cvt_pk_bf16_f32 v28, v9, v10
	v_mul_f32_e32 v9, v167, v11
	v_mul_f32_e32 v8, v167, v8
	v_pk_mul_f32 v[12:13], v[4:5], v[34:35]
	v_pk_mul_f32 v[14:15], v[6:7], v[16:17]
	v_pk_mul_f32 v[16:17], v[0:1], v[38:39]
	v_pk_mul_f32 v[18:19], v[2:3], v[18:19]
	v_cvt_pk_bf16_f32 v29, v9, v8
	v_lshl_add_u64 v[8:9], v[158:159], 0, v[144:145]
	v_pk_fma_f32 v[10:11], v[4:5], v[36:37], v[12:13] op_sel:[0,0,1] op_sel_hi:[1,1,0]
	v_pk_fma_f32 v[4:5], v[4:5], v[36:37], v[12:13] op_sel:[0,0,1] op_sel_hi:[1,1,0] neg_lo:[1,0,0] neg_hi:[1,0,0]
	v_pk_fma_f32 v[12:13], v[6:7], v[20:21], v[14:15] op_sel:[0,0,1] op_sel_hi:[1,1,0]
	v_pk_fma_f32 v[14:15], v[6:7], v[20:21], v[14:15] op_sel:[0,0,1] op_sel_hi:[1,1,0] neg_lo:[1,0,0] neg_hi:[1,0,0]
	v_pk_fma_f32 v[6:7], v[0:1], v[40:41], v[16:17] op_sel:[0,0,1] op_sel_hi:[1,1,0]
	v_pk_fma_f32 v[0:1], v[0:1], v[40:41], v[16:17] op_sel:[0,0,1] op_sel_hi:[1,1,0] neg_lo:[1,0,0] neg_hi:[1,0,0]
	v_pk_fma_f32 v[16:17], v[2:3], v[22:23], v[18:19] op_sel:[0,0,1] op_sel_hi:[1,1,0]
	s_and_b64 vcc, exec, s[8:9]
	v_pk_fma_f32 v[2:3], v[2:3], v[22:23], v[18:19] op_sel:[0,0,1] op_sel_hi:[1,1,0] neg_lo:[1,0,0] neg_hi:[1,0,0]
	flat_store_dwordx4 v[8:9], v[26:29] sc1
	s_cbranch_vccnz .LBB0_168
	v_mov_b32_e32 v17, v3
	v_mov_b32_e32 v7, v1
	v_mov_b32_e32 v13, v15
	v_mov_b32_e32 v11, v5
	v_pk_add_f32 v[130:131], v[130:131], v[10:11]
	v_pk_add_f32 v[128:129], v[128:129], v[12:13]
	v_pk_add_f32 v[126:127], v[126:127], v[6:7]
	v_pk_add_f32 v[124:125], v[124:125], v[16:17]
;     __device__ __forceinline__ void operator()(const f32x4 (&acc)[2][2][4][2], const Unit& u, int wr, int wc, int fr, int fq) const {
;     ...
;                         *(u32x4*)(base + (unsigned)(row * 512 + bj * HALF) * 2u) = w;
;                     }
;                 }
;             if (!isq) {
; #pragma unroll
;                 for (int bj = 0; bj < 2; ++bj)
; #pragma unroll
;                     for (int e = 0; e < 8; ++e) { float s = ks[bj][e]; s += __shfl_xor(s, 1); s += __shfl_xor(s, 2); s += __shfl_xor(s, 4); s += __shfl_xor(s, 8); ks[bj][e] = s; }
;                 if (fr == 0 && do_km) {
;                     const int b = u.pm >> 4, nb = u.pm & 15;
; #pragma unroll
;                     for (int bj = 0; bj < 2; ++bj) { const int h = (pn & 1) * 4 + 2 * bj + (wc >> 1); float* kp = (float*)(wb + OFF_KMEAN + (unsigned)(layer * 32768 + ((b * 8 + h) * 16 + nb) * 64 + 32 * (wc & 1) + 8 * fq) * 4u);
; #pragma unroll
;                         for (int e = 0; e < 8; ++e) unsafeAtomicAdd(kp + e, ks[bj][e] * (1.0f / 256.0f)); }
;                 }
.LBB0_168:
	v_mul_f32_e32 v0, v167, v5
	v_mul_f32_e32 v2, v167, v10
	v_cvt_pk_bf16_f32 v4, v0, v2
	v_mul_f32_e32 v0, v167, v15
	v_mul_f32_e32 v2, v167, v12
	v_cvt_pk_bf16_f32 v5, v0, v2
	v_mul_f32_e32 v0, v167, v1
	v_mul_f32_e32 v1, v167, v6
	s_and_b64 vcc, exec, s[50:51]
	v_cvt_pk_bf16_f32 v6, v0, v1
	v_mul_f32_e32 v0, v167, v3
	v_mul_f32_e32 v1, v167, v16
	v_cvt_pk_bf16_f32 v7, v0, v1
	flat_store_dwordx4 v[8:9], v[4:7] offset:256 sc1
	s_cbranch_vccz .LBB0_172
	ds_bpermute_b32 v1, v173, v156
	ds_bpermute_b32 v2, v173, v155
	ds_bpermute_b32 v5, v173, v154
	ds_bpermute_b32 v8, v173, v123
	ds_bpermute_b32 v11, v173, v122
	s_waitcnt lgkmcnt(0)
	v_add_f32_e32 v1, v156, v1
	ds_bpermute_b32 v4, v174, v1
	v_add_f32_e32 v6, v155, v2
	v_add_f32_e32 v8, v123, v8
	ds_bpermute_b32 v10, v174, v8
	ds_bpermute_b32 v18, v173, v130
	s_waitcnt lgkmcnt(0)
	v_add_f32_e32 v1, v1, v4
	v_add_f32_e32 v4, v154, v5
	ds_bpermute_b32 v5, v174, v6
	ds_bpermute_b32 v7, v174, v4
	v_add_f32_e32 v8, v8, v10
	v_add_f32_e32 v11, v122, v11
	ds_bpermute_b32 v10, v175, v8
	s_waitcnt lgkmcnt(0)
	v_add_f32_e32 v5, v6, v5
	v_add_f32_e32 v7, v4, v7
	ds_bpermute_b32 v6, v175, v5
	ds_bpermute_b32 v9, v175, v7
	ds_bpermute_b32 v12, v174, v11
	v_add_f32_e32 v18, v130, v18
	ds_bpermute_b32 v20, v174, v18
	s_waitcnt lgkmcnt(0)
	v_add_f32_e32 v4, v5, v6
	v_add_f32_e32 v6, v7, v9
	ds_bpermute_b32 v9, v173, v121
	ds_bpermute_b32 v21, v173, v129
	v_add_f32_e32 v8, v8, v10
	v_add_f32_e32 v10, v11, v12
	ds_bpermute_b32 v15, v173, v131
	s_waitcnt lgkmcnt(0)
	v_add_f32_e32 v13, v121, v9
	ds_bpermute_b32 v14, v174, v13
	v_add_f32_e32 v18, v18, v20
	v_add_f32_e32 v20, v129, v21
	v_add_f32_e32 v15, v131, v15
	ds_bpermute_b32 v21, v174, v20
	s_waitcnt lgkmcnt(0)
	v_add_f32_e32 v12, v13, v14
	ds_bpermute_b32 v14, v173, v120
	ds_bpermute_b32 v22, v173, v128
	ds_bpermute_b32 v17, v174, v15
	v_add_f32_e32 v20, v20, v21
	ds_bpermute_b32 v0, v173, v157
	s_waitcnt lgkmcnt(0)
	v_add_f32_e32 v14, v120, v14
	ds_bpermute_b32 v16, v174, v14
	v_add_f32_e32 v21, v128, v22
	v_add_f32_e32 v17, v15, v17
	ds_bpermute_b32 v22, v174, v21
	ds_bpermute_b32 v19, v175, v17
	s_waitcnt lgkmcnt(0)
	v_add_f32_e32 v14, v14, v16
	ds_bpermute_b32 v16, v175, v14
	ds_bpermute_b32 v27, v173, v125
	v_add_f32_e32 v22, v21, v22
	ds_bpermute_b32 v26, v175, v22
	ds_bpermute_b32 v28, v173, v124
	s_waitcnt lgkmcnt(0)
	v_add_f32_e32 v14, v14, v16
	v_add_f32_e32 v16, v17, v19
	ds_bpermute_b32 v19, v175, v18
	v_add_f32_e32 v22, v22, v26
	ds_bpermute_b32 v26, v173, v126
	v_add_f32_e32 v0, v157, v0
	v_add_f32_e32 v27, v125, v27
	s_waitcnt lgkmcnt(0)
	v_add_f32_e32 v18, v18, v19
	ds_bpermute_b32 v19, v173, v127
	v_add_f32_e32 v26, v126, v26
	v_add_f32_e32 v28, v124, v28
	ds_bpermute_b32 v3, v174, v0
	ds_bpermute_b32 v29, v174, v26
	s_waitcnt lgkmcnt(0)
	v_add_f32_e32 v24, v127, v19
	ds_bpermute_b32 v25, v174, v24
	ds_bpermute_b32 v30, v174, v27
	ds_bpermute_b32 v31, v174, v28
	v_add_f32_e32 v0, v0, v3
	v_add_f32_e32 v26, v26, v29
	s_waitcnt lgkmcnt(0)
	v_add_f32_e32 v24, v24, v25
	v_add_f32_e32 v30, v27, v30
	v_add_f32_e32 v31, v28, v31
	ds_bpermute_b32 v2, v175, v0
	ds_bpermute_b32 v3, v175, v1
	ds_bpermute_b32 v11, v175, v10
	ds_bpermute_b32 v13, v175, v12
	ds_bpermute_b32 v23, v175, v20
	ds_bpermute_b32 v25, v175, v24
	ds_bpermute_b32 v29, v175, v26
	ds_bpermute_b32 v32, v175, v30
	ds_bpermute_b32 v33, v175, v31
	s_waitcnt lgkmcnt(0)
	v_add_f32_e32 v0, v0, v2
	v_add_f32_e32 v2, v1, v3
	v_add_f32_e32 v10, v10, v11
	v_add_f32_e32 v12, v12, v13
	v_add_f32_e32 v20, v20, v23
	v_add_f32_e32 v24, v24, v25
	v_add_f32_e32 v26, v26, v29
	v_add_f32_e32 v28, v30, v32
	v_add_f32_e32 v30, v31, v33
	ds_bpermute_b32 v1, v176, v0
	ds_bpermute_b32 v3, v176, v2
	ds_bpermute_b32 v5, v176, v4
	ds_bpermute_b32 v7, v176, v6
	ds_bpermute_b32 v9, v176, v8
	ds_bpermute_b32 v11, v176, v10
	ds_bpermute_b32 v13, v176, v12
	ds_bpermute_b32 v15, v176, v14
	ds_bpermute_b32 v17, v176, v16
	ds_bpermute_b32 v19, v176, v18
	ds_bpermute_b32 v21, v176, v20
	ds_bpermute_b32 v23, v176, v22
	ds_bpermute_b32 v25, v176, v24
	ds_bpermute_b32 v27, v176, v26
	ds_bpermute_b32 v29, v176, v28
	ds_bpermute_b32 v31, v176, v30
	s_and_saveexec_b64 s[8:9], s[4:5]
	s_cbranch_execz .LBB0_171
	s_lshl_b32 s27, s27, 2
	s_or_b32 s27, s27, s73
	s_add_u32 s34, s46, 0x80000
	s_addc_u32 s35, s47, 0
	s_lshr_b32 s29, s14, 1
	s_and_b32 s29, s29, 0x3ffff8
	s_lshl_b32 s14, s14, 6
	s_or_b32 s27, s27, s29
	s_and_b32 s14, s14, 0x3c0
	s_or_b32 s14, s14, s74
	s_lshl_b32 s27, s27, 10
	s_or_b32 s29, s14, s27
	s_waitcnt lgkmcnt(0)
	v_add_f32_e32 v2, v2, v3
	v_add_f32_e32 v3, v0, v1
	v_or_b32_e32 v0, s29, v179
	v_lshlrev_b32_e32 v144, 2, v0
	v_lshl_add_u64 v[0:1], s[34:35], 0, v[144:145]
	v_mul_f32_e32 v3, 0x3b800000, v3
	v_add_f32_e32 v4, v4, v5
	flat_atomic_add_f32 v[0:1], v3
	v_mul_f32_e32 v2, 0x3b800000, v2
	v_add_f32_e32 v6, v6, v7
	flat_atomic_add_f32 v[0:1], v2 offset:4
	v_mul_f32_e32 v2, 0x3b800000, v4
	v_add_f32_e32 v8, v8, v9
	flat_atomic_add_f32 v[0:1], v2 offset:8
	v_mul_f32_e32 v2, 0x3b800000, v6
	v_add_f32_e32 v10, v10, v11
	flat_atomic_add_f32 v[0:1], v2 offset:12
	v_mul_f32_e32 v2, 0x3b800000, v8
	v_add_f32_e32 v12, v12, v13
	flat_atomic_add_f32 v[0:1], v2 offset:16
	v_mul_f32_e32 v2, 0x3b800000, v10
	v_add_f32_e32 v14, v14, v15
	flat_atomic_add_f32 v[0:1], v2 offset:20
	v_mul_f32_e32 v2, 0x3b800000, v12
	flat_atomic_add_f32 v[0:1], v2 offset:24
	v_mul_f32_e32 v2, 0x3b800000, v14
	flat_atomic_add_f32 v[0:1], v2 offset:28
	v_or_b32_e32 v0, s14, v179
	v_or_b32_e32 v0, s27, v0
	v_add_f32_e32 v16, v16, v17
	v_lshl_or_b32 v144, v0, 2, v189
	v_add_f32_e32 v18, v18, v19
	v_lshl_add_u64 v[0:1], s[34:35], 0, v[144:145]
	v_mul_f32_e32 v2, 0x3b800000, v16
	v_add_f32_e32 v20, v20, v21
	flat_atomic_add_f32 v[0:1], v2
	v_mul_f32_e32 v2, 0x3b800000, v18
	v_add_f32_e32 v22, v22, v23
	flat_atomic_add_f32 v[0:1], v2 offset:4
	v_mul_f32_e32 v2, 0x3b800000, v20
	v_add_f32_e32 v24, v24, v25
	flat_atomic_add_f32 v[0:1], v2 offset:8
	v_mul_f32_e32 v2, 0x3b800000, v22
	v_add_f32_e32 v26, v26, v27
	flat_atomic_add_f32 v[0:1], v2 offset:12
	v_mul_f32_e32 v2, 0x3b800000, v24
	v_add_f32_e32 v28, v28, v29
	flat_atomic_add_f32 v[0:1], v2 offset:16
	v_mul_f32_e32 v2, 0x3b800000, v26
	v_add_f32_e32 v30, v30, v31
	flat_atomic_add_f32 v[0:1], v2 offset:20
	v_mul_f32_e32 v2, 0x3b800000, v28
	flat_atomic_add_f32 v[0:1], v2 offset:24
	v_mul_f32_e32 v2, 0x3b800000, v30
	flat_atomic_add_f32 v[0:1], v2 offset:28

; #define GAS __attribute__((address_space(1)))
; #define LAS __attribute__((address_space(3)))
; __device__ __forceinline__ void p0_vslice_item(LAS unsigned char* lds, int wave, int tid, const float* vt_l, unsigned char* VS_l, float* vsc_l, int item) {
;     ...
; #pragma unroll 1
;     for (int p = tid; p < 4096; p += 512) { const int cs = p >> 5, k = p & 31;
;         const mk_u32x2 a = *(const LAS mk_u32x2*)(lds + (2 * k) * 1032 + cs * 8), b = *(const LAS mk_u32x2*)(lds + (2 * k + 1) * 1032 + cs * 8);
;         *(GAS v4u*)(VS_l + ((size_t)cs * 16384 + e0 + 2 * k) * 8) = (v4u){a.x, a.y, b.x, b.y}; }
.LBB0_190:
	v_ashrrev_i32_e32 v16, 5, v5
	v_and_b32_e32 v9, 62, v4
	v_add_u32_e32 v12, 0x200, v5
	v_mul_u32_u24_e32 v13, 0x408, v9
	v_lshlrev_b32_e32 v14, 3, v16
	v_cmp_lt_i32_e32 vcc, s27, v5
	v_mov_b32_e32 v5, v12
	v_add3_u32 v12, 0, v13, v14
	v_ashrrev_i32_e32 v17, 31, v16
	ds_read2_b64 v[12:15], v12 offset1:129
	v_lshlrev_b64 v[16:17], 14, v[16:17]
	v_or_b32_e32 v16, s9, v16
	v_or_b32_e32 v16, v16, v9
	v_add_u32_e32 v4, 0x400, v4
	s_or_b64 s[20:21], vcc, s[20:21]
	v_lshl_add_u64 v[16:17], v[16:17], 3, s[16:17]
	s_waitcnt lgkmcnt(0)
	global_store_dwordx4 v[16:17], v[12:15], off sc1
	s_andn2_b64 exec, exec, s[20:21]
	s_cbranch_execnz .LBB0_190
	s_branch .LBB0_183

; __device__ __forceinline__ int crow(int r,int hi){return (r&3)+8*(r>>2)+4*hi;}
; template<int THRL> __device__ __forceinline__ void attn_unit(int wave_id,int b,int h,int qb,const bf16*Q,const bf16*__restrict__ K,const bf16*__restrict__ V,bf16*O,const float*__restrict__ KM,char*shm){
;     ...
;   if(hi==0)wsf[32+r32]=l_reg;asm volatile("s_waitcnt lgkmcnt(0)":::"memory");
;   float rli[16];
;   #pragma unroll
;   for(int r=0;r<16;++r)rli[r]=__builtin_amdgcn_rcpf(wsf[32+crow(r,hi)]);
;   bf16*Ow=O+(rowbase+q0+wid*QBLK)*ODM+h*D;
;   { bf16*stg=(bf16*)(shm+LDS_OST)+wid*2048;
;     #pragma unroll
;     for(int r=0;r<16;++r){const int orow=crow(r,hi);
;       #pragma unroll
;       for(int d0=0;d0<2;++d0)stg[orow*64+d0*32+r32]=__float2bfloat16(o[d0][r]*rli[r]);}
;     asm volatile("s_waitcnt lgkmcnt(0)":::"memory");
;     #pragma unroll
;     for(int i=0;i<4;++i){const int row=i*8+(lane>>3),ch=lane&7; const u32x4 v=*(const u32x4*)(stg+row*64+ch*8); ATTN_STORE16(Ow+(long)row*ODM+ch*8,v);} }
;   asm volatile("s_waitcnt lgkmcnt(0)\n\ts_barrier":::"memory");
.LBB0_252:
	s_or_b64 exec, exec, s[6:7]
	s_waitcnt lgkmcnt(0)
	v_lshl_add_u32 v40, v208, 2, s85
	ds_read_b128 v[32:35], v40 offset:49280
	ds_read_b128 v[36:39], v40 offset:49312
	s_lshl_b64 s[4:5], s[54:55], 11
	s_add_u32 s4, s64, s4
	s_addc_u32 s5, s65, s5
	s_waitcnt lgkmcnt(1)
	v_rcp_f32_e32 v41, v32
	v_rcp_f32_e32 v42, v33
	v_rcp_f32_e32 v43, v34
	v_rcp_f32_e32 v44, v35
	s_waitcnt lgkmcnt(0)
	v_rcp_f32_e32 v45, v36
	ds_read_b128 v[32:35], v40 offset:49344
	v_rcp_f32_e32 v46, v37
	v_rcp_f32_e32 v47, v38
	v_rcp_f32_e32 v48, v39
	ds_read_b128 v[36:39], v40 offset:49376
	v_lshl_add_u32 v40, v200, 1, s86
	v_mul_f32_e32 v0, v0, v41
	v_lshl_add_u32 v49, v201, 9, v40
	v_cvt_pk_bf16_f32 v0, v0, s0
	ds_write_b16 v49, v0 offset:51264
	v_mul_f32_e32 v0, v17, v42
	v_cvt_pk_bf16_f32 v0, v0, s0
	ds_write_b16 v49, v0 offset:51328
	v_mul_f32_e32 v0, v1, v42
	v_cvt_pk_bf16_f32 v0, v0, s0
	v_mul_f32_e32 v1, v18, v43
	ds_write_b16 v49, v0 offset:51392
	v_lshl_add_u32 v0, v207, 7, v40
	v_cvt_pk_bf16_f32 v1, v1, s0
	ds_write_b16 v0, v1 offset:51200
	v_mul_f32_e32 v1, v2, v43
	v_cvt_pk_bf16_f32 v1, v1, s0
	ds_write_b16 v0, v1 offset:51264
	v_mul_f32_e32 v1, v19, v44
	v_lshl_add_u32 v0, v206, 7, v40
	v_cvt_pk_bf16_f32 v1, v1, s0
	ds_write_b16 v0, v1 offset:51200
	v_mul_f32_e32 v1, v3, v44
	v_cvt_pk_bf16_f32 v1, v1, s0
	ds_write_b16 v0, v1 offset:51264
	v_mul_f32_e32 v1, v20, v45
	v_lshl_add_u32 v0, v205, 7, v40
	v_cvt_pk_bf16_f32 v1, v1, s0
	ds_write_b16 v0, v1 offset:51200
	v_mul_f32_e32 v1, v4, v45
	v_cvt_pk_bf16_f32 v1, v1, s0
	ds_write_b16 v0, v1 offset:51264
	v_mul_f32_e32 v0, v21, v46
	v_cvt_pk_bf16_f32 v0, v0, s0
	ds_write_b16 v49, v0 offset:52352
	v_mul_f32_e32 v0, v5, v46
	v_cvt_pk_bf16_f32 v0, v0, s0
	ds_write_b16 v49, v0 offset:52416
	v_mul_f32_e32 v0, v22, v47
	v_cvt_pk_bf16_f32 v0, v0, s0
	ds_write_b16 v49, v0 offset:52480
	v_mul_f32_e32 v0, v6, v47
	s_waitcnt lgkmcnt(13)
	v_rcp_f32_e32 v32, v32
	v_cvt_pk_bf16_f32 v0, v0, s0
	ds_write_b16 v49, v0 offset:52544
	v_mul_f32_e32 v0, v23, v48
	v_cvt_pk_bf16_f32 v0, v0, s0
	ds_write_b16 v49, v0 offset:52608
	v_mul_f32_e32 v0, v7, v48
	v_rcp_f32_e32 v33, v33
	v_cvt_pk_bf16_f32 v0, v0, s0
	v_mul_f32_e32 v1, v24, v32
	ds_write_b16 v49, v0 offset:52672
	v_lshl_add_u32 v0, v193, 7, v40
	v_cvt_pk_bf16_f32 v1, v1, s0
	ds_write_b16 v0, v1 offset:51200
	v_mul_f32_e32 v1, v8, v32
	v_cvt_pk_bf16_f32 v1, v1, s0
	v_rcp_f32_e32 v34, v34
	ds_write_b16 v0, v1 offset:51264
	v_mul_f32_e32 v0, v25, v33
	v_cvt_pk_bf16_f32 v0, v0, s0
	ds_write_b16 v49, v0 offset:53376
	v_mul_f32_e32 v0, v9, v33
	v_cvt_pk_bf16_f32 v0, v0, s0
	v_rcp_f32_e32 v35, v35
	ds_write_b16 v49, v0 offset:53440
	v_mul_f32_e32 v0, v26, v34
	v_cvt_pk_bf16_f32 v0, v0, s0
	ds_write_b16 v49, v0 offset:53504
	v_mul_f32_e32 v0, v10, v34
	s_waitcnt lgkmcnt(14)
	v_rcp_f32_e32 v36, v36
	v_cvt_pk_bf16_f32 v0, v0, s0
	ds_write_b16 v49, v0 offset:53568
	v_mul_f32_e32 v0, v27, v35
	v_cvt_pk_bf16_f32 v0, v0, s0
	ds_write_b16 v49, v0 offset:53632
	v_mul_f32_e32 v0, v11, v35
	v_rcp_f32_e32 v37, v37
	v_cvt_pk_bf16_f32 v0, v0, s0
	v_mul_f32_e32 v1, v28, v36
	ds_write_b16 v49, v0 offset:53696
	v_lshl_add_u32 v0, v190, 7, v40
	v_cvt_pk_bf16_f32 v1, v1, s0
	ds_write_b16 v0, v1 offset:51200
	v_mul_f32_e32 v1, v12, v36
	v_cvt_pk_bf16_f32 v1, v1, s0
	v_rcp_f32_e32 v38, v38
	ds_write_b16 v0, v1 offset:51264
	v_mul_f32_e32 v0, v29, v37
	v_cvt_pk_bf16_f32 v0, v0, s0
	ds_write_b16 v49, v0 offset:54400
	v_mul_f32_e32 v0, v13, v37
	v_cvt_pk_bf16_f32 v0, v0, s0
	v_rcp_f32_e32 v39, v39
	ds_write_b16 v49, v0 offset:54464
	v_mul_f32_e32 v0, v30, v38
	v_cvt_pk_bf16_f32 v0, v0, s0
	ds_write_b16 v49, v0 offset:54528
	v_mul_f32_e32 v0, v14, v38
	v_cvt_pk_bf16_f32 v0, v0, s0
	ds_write_b16 v49, v0 offset:54592
	v_mul_f32_e32 v0, v31, v39
	v_cvt_pk_bf16_f32 v0, v0, s0
	ds_write_b16 v49, v0 offset:54656
	v_mul_f32_e32 v0, v15, v39
	v_cvt_pk_bf16_f32 v0, v0, s0
	v_mul_f32_e32 v16, v16, v41
	ds_write_b16 v49, v0 offset:54720
	v_lshlrev_b32_e32 v0, 1, v199
	v_cvt_pk_bf16_f32 v16, v16, s0
	v_and_b32_e32 v190, 0x70, v0
	ds_write_b16 v49, v16 offset:51200
	s_add_u32 s4, s4, s52
	v_ashrrev_i32_e32 v8, 3, v192
	v_add_u32_e32 v16, s86, v190
	s_addc_u32 s5, s5, s53
	s_waitcnt lgkmcnt(0)
	v_lshl_add_u32 v0, v8, 7, v16
	v_ashrrev_i32_e32 v9, 31, v8
	v_lshl_add_u64 v[10:11], s[4:5], 0, v[190:191]
	ds_read_b128 v[0:3], v0 offset:51200
	v_lshlrev_b64 v[4:5], 11, v[8:9]
	v_add_u32_e32 v14, 8, v8
	v_lshl_add_u64 v[12:13], v[10:11], 0, v[4:5]
	v_lshl_add_u32 v4, v14, 7, v16
	ds_read_b128 v[4:7], v4 offset:51200
	v_ashrrev_i32_e32 v15, 31, v14
	s_waitcnt lgkmcnt(1)
	global_store_dwordx4 v[12:13], v[0:3], off sc1
	s_or_b32 s6, s63, s75
	s_and_b64 s[4:5], s[50:51], exec
	v_lshlrev_b64 v[0:1], 11, v[14:15]
	v_lshl_add_u64 v[0:1], v[10:11], 0, v[0:1]
	s_waitcnt lgkmcnt(0)
	global_store_dwordx4 v[0:1], v[4:7], off sc1
	s_cselect_b32 s74, s76, s74
	s_cselect_b32 s92, s6, s92
	v_add_u32_e32 v4, 16, v8
	v_lshl_add_u32 v0, v4, 7, v16
	v_ashrrev_i32_e32 v5, 31, v4
	ds_read_b128 v[0:3], v0 offset:51200
	v_lshlrev_b64 v[4:5], 11, v[4:5]
	v_add_u32_e32 v8, 24, v8
	v_lshl_add_u64 v[12:13], v[10:11], 0, v[4:5]
	v_lshl_add_u32 v4, v8, 7, v16
	ds_read_b128 v[4:7], v4 offset:51200
	v_ashrrev_i32_e32 v9, 31, v8
	s_waitcnt lgkmcnt(1)
	global_store_dwordx4 v[12:13], v[0:3], off sc1
	s_mov_b64 s[50:51], 0
	s_andn2_b64 vcc, exec, s[48:49]
	v_lshlrev_b64 v[0:1], 11, v[8:9]
	v_lshl_add_u64 v[0:1], v[10:11], 0, v[0:1]
	s_waitcnt lgkmcnt(0)
	global_store_dwordx4 v[0:1], v[4:7], off sc1
	s_waitcnt lgkmcnt(0)
	s_barrier
	s_mov_b64 s[48:49], -1
	s_mov_b32 s63, 2
	s_cbranch_vccz .LBB0_367

; #define GAS __attribute__((address_space(1)))
; #define LAS __attribute__((address_space(3)))
; __device__ __forceinline__ unsigned pk2(float lo, float hi) { return f2bf(lo) | (f2bf(hi) << 16); }
; __device__ __forceinline__ void conv_phase(LAS unsigned char* lds, int tile, int tid, const bf16* __restrict__ U, const float* __restrict__ cw, const float* __restrict__ cb, ...
;     ...
;         for (int q = 0; q < 4; ++q) {
;             const int tk = wave * 4 + q;
;             const f32x4 a0 = *(const LAS f32x4*)(obuf + tk * CH + lane * 8), a1 = *(const LAS f32x4*)(obuf + tk * CH + lane * 8 + 4);
;             float v[8] = {a0.x, a0.y, a0.z, a0.w, a1.x, a1.y, a1.z, a1.w};
;             float s = 0.f;
; #pragma unroll
;             for (int e = 0; e < 8; ++e) s += v[e];
; #pragma unroll
;             for (int o = 1; o < 64; o <<= 1) s += __shfl_xor(s, o);
;             const float mean = s * (1.0f / CH); float sq = 0.f;
; #pragma unroll
;             for (int e = 0; e < 8; ++e) { v[e] -= mean; sq += v[e] * v[e]; }
; #pragma unroll
;             for (int o = 1; o < 64; o <<= 1) sq += __shfl_xor(sq, o);
;             const float rstd = 1.0f / sqrtf(sq * (1.0f / CH) + 1e-5f);
;             const f32x4 g0 = *(const GAS f32x4*)(cg + lane * 8), g1 = *(const GAS f32x4*)(cg + lane * 8 + 4), b0 = *(const GAS f32x4*)(cbeta + lane * 8), b1 = *(const GAS f32x4*)(cbeta + lane * 8 + 4);
;             const float gg[8] = {g0.x, g0.y, g0.z, g0.w, g1.x, g1.y, g1.z, g1.w}, bb[8] = {b0.x, b0.y, b0.z, b0.w, b1.x, b1.y, b1.z, b1.w};
;             float y[8];
; #pragma unroll
;             for (int e = 0; e < 8; ++e) { const float z = v[e] * rstd * gg[e] + bb[e]; y[e] = z * __builtin_amdgcn_rcpf(1.0f + __builtin_amdgcn_exp2f(-1.4426950408889634f * z)); }
;             v4u o; o.x = pk2(y[0], y[1]); o.y = pk2(y[2], y[3]); o.z = pk2(y[4], y[5]); o.w = pk2(y[6], y[7]);
;             *(GAS v4u*)(MIX + (size_t)(t0 + tk) * 1024 + 512 + lane * 8) = o;
;         }
.LBB0_374:
	v_add_u32_e32 v72, s12, v69
	ds_read_b128 v[14:17], v72
	ds_read_b128 v[72:75], v72 offset:16
	s_addk_i32 s12, 0x800
	s_cmpk_eq_i32 s12, 0x2000
	s_waitcnt lgkmcnt(1)
	v_add_f32_e32 v80, 0, v14
	v_mov_b32_e32 v76, v14
	v_add_f32_e32 v14, v15, v80
	v_add_f32_e32 v14, v16, v14
	v_add_f32_e32 v14, v17, v14
	s_waitcnt lgkmcnt(0)
	v_add_f32_e32 v14, v72, v14
	v_add_f32_e32 v14, v73, v14
	v_add_f32_e32 v14, v74, v14
	v_add_f32_e32 v14, v75, v14
	v_mov_b32_e32 v77, v16
	v_mov_b32_e32 v16, v15
	v_mov_b32_e32 v78, v72
	v_mov_b32_e32 v79, v74
	v_mov_b32_e32 v74, v73
	s_nop 1
	v_add_f32_dpp v14, v14, v14 row_shr:1 row_mask:0xf bank_mask:0xf
	s_nop 1
	v_add_f32_dpp v14, v14, v14 row_shr:2 row_mask:0xf bank_mask:0xf
	s_nop 1
	v_add_f32_dpp v14, v14, v14 row_shr:4 row_mask:0xf bank_mask:0xf
	s_nop 1
	v_add_f32_dpp v14, v14, v14 row_shr:8 row_mask:0xf bank_mask:0xf
	s_nop 1
	v_add_f32_dpp v14, v14, v14 row_bcast:15 row_mask:0xa bank_mask:0xf
	s_nop 1
	v_add_f32_dpp v14, v14, v14 row_bcast:31 row_mask:0xc bank_mask:0xf
	s_nop 1
	v_readlane_b32 s98, v14, 63
	s_nop 1
	v_mov_b32_e32 v14, s98
	v_mul_f32_e32 v14, 0x3b000000, v14
	v_pk_add_f32 v[72:73], v[76:77], v[14:15] op_sel_hi:[1,0] neg_lo:[0,1] neg_hi:[0,1]
	v_pk_add_f32 v[16:17], v[16:17], v[14:15] op_sel_hi:[1,0] neg_lo:[0,1] neg_hi:[0,1]
	v_pk_add_f32 v[76:77], v[78:79], v[14:15] op_sel_hi:[1,0] neg_lo:[0,1] neg_hi:[0,1]
	v_pk_add_f32 v[14:15], v[74:75], v[14:15] op_sel_hi:[1,0] neg_lo:[0,1] neg_hi:[0,1]
	v_pk_mul_f32 v[74:75], v[72:73], v[72:73]
	v_pk_mul_f32 v[78:79], v[16:17], v[16:17]
	v_mov_b32_e32 v80, v15
	v_add_f32_e32 v74, v74, v78
	v_add_f32_e32 v74, v75, v74
	v_add_f32_e32 v74, v79, v74
	v_mov_b32_e32 v81, v77
	v_fmac_f32_e32 v74, v76, v76
	v_pk_mul_f32 v[80:81], v[80:81], v[80:81]
	v_fmac_f32_e32 v74, v14, v14
	v_add_f32_e32 v74, v81, v74
	v_add_f32_e32 v74, v80, v74
	s_nop 1
	v_add_f32_dpp v74, v74, v74 row_shr:1 row_mask:0xf bank_mask:0xf
	s_nop 1
	v_add_f32_dpp v74, v74, v74 row_shr:2 row_mask:0xf bank_mask:0xf
	s_nop 1
	v_add_f32_dpp v74, v74, v74 row_shr:4 row_mask:0xf bank_mask:0xf
	s_nop 1
	v_add_f32_dpp v74, v74, v74 row_shr:8 row_mask:0xf bank_mask:0xf
	s_nop 1
	v_add_f32_dpp v74, v74, v74 row_bcast:15 row_mask:0xa bank_mask:0xf
	s_nop 1
	v_add_f32_dpp v74, v74, v74 row_bcast:31 row_mask:0xc bank_mask:0xf
	s_nop 1
	v_readlane_b32 s98, v74, 63
	s_nop 1
	v_mov_b32_e32 v74, s98
	v_fmamk_f32 v74, v74, 0x3b000000, v70
	v_mul_f32_e32 v75, 0x4f800000, v74
	v_cmp_gt_f32_e32 vcc, s18, v74
	s_nop 1
	v_cndmask_b32_e32 v74, v74, v75, vcc
	v_sqrt_f32_e32 v75, v74
	s_nop 0
	v_add_u32_e32 v78, -1, v75
	v_add_u32_e32 v79, 1, v75
	v_fma_f32 v80, -v78, v75, v74
	v_fma_f32 v81, -v79, v75, v74
	v_cmp_ge_f32_e64 s[6:7], 0, v80
	s_nop 1
	v_cndmask_b32_e64 v75, v75, v78, s[6:7]
	v_cmp_lt_f32_e64 s[6:7], 0, v81
	s_nop 1
	v_cndmask_b32_e64 v75, v75, v79, s[6:7]
	v_mul_f32_e32 v78, 0x37800000, v75
	v_cndmask_b32_e32 v75, v75, v78, vcc
	v_cmp_class_f32_e32 vcc, v74, v71
	s_nop 1
	v_cndmask_b32_e32 v74, v75, v74, vcc
	v_div_scale_f32 v75, s[6:7], v74, v74, 1.0
	v_rcp_f32_e32 v79, v75
	v_div_scale_f32 v78, vcc, 1.0, v74, 1.0
	v_fma_f32 v80, -v75, v79, 1.0
	v_fmac_f32_e32 v79, v80, v79
	v_mul_f32_e32 v80, v78, v79
	v_fma_f32 v81, -v75, v80, v78
	v_fmac_f32_e32 v80, v81, v79
	v_fma_f32 v75, -v75, v80, v78
	v_div_fmas_f32 v75, v75, v79, v80
	v_div_fixup_f32 v74, v75, v74, 1.0
	v_pk_mul_f32 v[72:73], v[72:73], v[74:75] op_sel_hi:[1,0]
	v_pk_mul_f32 v[16:17], v[16:17], v[74:75] op_sel_hi:[1,0]
	v_pk_mul_f32 v[76:77], v[76:77], v[74:75] op_sel_hi:[1,0]
	v_pk_mul_f32 v[14:15], v[14:15], v[74:75] op_sel_hi:[1,0]
	v_pk_fma_f32 v[72:73], v[8:9], v[72:73], v[12:13]
	v_pk_fma_f32 v[16:17], v[24:25], v[16:17], v[22:23]
	v_pk_fma_f32 v[74:75], v[0:1], v[76:77], v[4:5]
	v_pk_fma_f32 v[14:15], v[26:27], v[14:15], v[10:11]
	v_mul_f32_e32 v76, 0xbfb8aa3b, v72
	v_mul_f32_e32 v77, 0xbfb8aa3b, v16
	v_mul_f32_e32 v78, 0xbfb8aa3b, v73
	v_mul_f32_e32 v79, 0xbfb8aa3b, v17
	v_mul_f32_e32 v80, 0xbfb8aa3b, v74
	v_mul_f32_e32 v81, 0xbfb8aa3b, v14
	v_mul_f32_e32 v82, 0xbfb8aa3b, v75
	v_mul_f32_e32 v83, 0xbfb8aa3b, v15
	v_exp_f32_e32 v76, v76
	v_exp_f32_e32 v77, v77
	v_exp_f32_e32 v78, v78
	v_exp_f32_e32 v79, v79
	v_exp_f32_e32 v80, v80
	v_exp_f32_e32 v81, v81
	v_exp_f32_e32 v82, v82
	v_exp_f32_e32 v83, v83
	v_add_f32_e32 v76, 1.0, v76
	v_add_f32_e32 v77, 1.0, v77
	v_add_f32_e32 v84, 1.0, v78
	v_add_f32_e32 v79, 1.0, v79
	v_add_f32_e32 v80, 1.0, v80
	v_add_f32_e32 v81, 1.0, v81
	v_add_f32_e32 v85, 1.0, v82
	v_add_f32_e32 v83, 1.0, v83
	v_rcp_f32_e32 v76, v76
	v_rcp_f32_e32 v78, v77
	v_rcp_f32_e32 v77, v84
	v_rcp_f32_e32 v79, v79
	v_rcp_f32_e32 v80, v80
	v_rcp_f32_e32 v82, v81
	v_rcp_f32_e32 v81, v85
	v_rcp_f32_e32 v83, v83
	v_pk_mul_f32 v[72:73], v[72:73], v[76:77]
	v_pk_mul_f32 v[16:17], v[16:17], v[78:79]
	v_pk_mul_f32 v[74:75], v[74:75], v[80:81]
	v_pk_mul_f32 v[14:15], v[14:15], v[82:83]
	v_bfe_u32 v78, v17, 16, 1
	v_bfe_u32 v79, v16, 16, 1
	v_bfe_u32 v80, v72, 16, 1
	v_bfe_u32 v81, v73, 16, 1
	v_bfe_u32 v82, v74, 16, 1
	v_bfe_u32 v83, v75, 16, 1
	v_bfe_u32 v76, v15, 16, 1
	v_bfe_u32 v77, v14, 16, 1
	v_add3_u32 v79, v16, v79, s19
	v_add3_u32 v78, v17, v78, s19
	v_add3_u32 v16, v75, v83, s19
	v_add3_u32 v17, v74, v82, s19
	v_add3_u32 v73, v73, v81, s19
	v_add3_u32 v72, v72, v80, s19
	v_add3_u32 v14, v14, v77, s19
	v_add3_u32 v15, v15, v76, s19
	v_lshrrev_b32_e32 v72, 16, v72
	v_lshrrev_b32_e32 v73, 16, v73
	v_lshrrev_b32_e32 v74, 16, v17
	v_lshrrev_b32_e32 v16, 16, v16
	v_and_or_b32 v17, v15, s20, v16
	v_and_or_b32 v16, v14, s20, v74
	v_and_or_b32 v15, v78, s20, v73
	v_and_or_b32 v14, v79, s20, v72
	global_store_dwordx4 v[6:7], v[14:17], off sc1
	v_lshl_add_u64 v[6:7], v[6:7], 0, s[8:9]
	s_cbranch_scc0 .LBB0_374
; __device__ __forceinline__ int mk_lane() { int l_ = (int)__builtin_amdgcn_mbcnt_hi(~0u, __builtin_amdgcn_mbcnt_lo(~0u, 0u)); asm volatile("" : "+v"(l_)); return l_; }
; #define BOTH(k) (IN(k) && IN((k) + 1))
; __device__ __forceinline__ void xcd_barrier(const XcdBarrier& b, int wave_id, int pair = -1) {
;     asm volatile("s_waitcnt vmcnt(0)" ::: "memory");
;     __syncthreads();
;     if (wave_id == 0 && mk_lane() == 0) {
;         unsigned* bar = b.bar;
;         __builtin_amdgcn_s_waitcnt(0);
;         unsigned nloc = b.st[0], nx = b.st[1];
;         if (nloc == 0u) { xcd_barrier_complete(bar, b.x, nloc, nx); b.st[0] = nloc; b.st[1] = nx; }
; template <int K> __device__ __forceinline__ void run_phase(Frame& F, const XcdBarrier& bar, int lo, int hi, unsigned char* lds) {
;     ...
;         if (BOTH(k)) {
;             constexpr bool LOCAL_SEAM = MK_LOCALBAR && (sub == 2 || (sub == 6 && l == 0));
;             bool local = false;
;             if (LOCAL_SEAM) local = __hip_atomic_load((unsigned*)(F.ctl + CW_LBAR + 24 * 64), __ATOMIC_RELAXED, __HIP_MEMORY_SCOPE_AGENT) == 0u;
;             constexpr bool PAIR_SEAM = MK_LOCALBAR && (sub == 0 || sub == 1);
;             bool pairok = false;
;             if (PAIR_SEAM) pairok = __hip_atomic_load((unsigned*)(F.ctl + CW_LBAR + 24 * 64), __ATOMIC_RELAXED, __HIP_MEMORY_SCOPE_AGENT) == 0u;
;             if (local) xcd_local_barrier((unsigned*)(F.ctl + CW_LBAR + ((sub == 2 ? l : 2) * 8 + (bx & 7)) * 64), (unsigned)(G >> 3), (unsigned*)(F.ctl + CW_BAR) + XB_TMO, F.wave);
;             else xcd_barrier(bar, F.wave, pairok ? ((bx & 7) >> 1) : -1);
	s_mov_b32 s21, 32
	s_mov_b64 s[6:7], 0
	s_and_b64 vcc, exec, s[10:11]
	s_cbranch_vccz .LBB0_368
	s_cmp_lt_i32 s41, 4
	s_barrier
	s_cbranch_scc1 .LBB0_433
	v_mov_b32_e32 v0, 0x31000
	global_load_dword v0, v0, s[30:31] offset:2048 sc1
	s_waitcnt vmcnt(0)
	s_andn2_b64 vcc, exec, s[38:39]
	s_barrier
	s_cbranch_vccnz .LBB0_432
	s_nop 0
	v_cmp_eq_u32_e32 vcc, 0, v194
	s_and_saveexec_b64 s[6:7], vcc
	s_cbranch_execz .LBB0_431
	s_add_i32 s4, 0, 0x27f60
	v_mov_b32_e32 v1, s4
	s_waitcnt vmcnt(0) expcnt(0) lgkmcnt(0)
	ds_read_b32 v3, v1
	s_add_i32 s4, 0, 0x27f64
	v_mov_b32_e32 v1, s4
	ds_read_b32 v1, v1
	s_waitcnt lgkmcnt(1)
	v_cmp_ne_u32_e32 vcc, 0, v3
	s_cbranch_vccnz .LBB0_395
	v_readlane_b32 s4, v248, 0
	v_readlane_b32 s5, v248, 1
	s_load_dwordx2 s[10:11], s[4:5], 0x4
	s_add_u32 s4, s30, 0x4200
	s_addc_u32 s5, s31, 0
	s_add_u32 s8, s30, 0x4400
	s_addc_u32 s9, s31, 0
	s_waitcnt lgkmcnt(0)
	s_mul_i32 s58, s10, s60
	s_add_u32 s10, s30, 0x4500
	s_mul_i32 s58, s58, s11
	s_addc_u32 s11, s31, 0
	s_add_u32 s12, s30, 0x4600
	s_addc_u32 s13, s31, 0
	s_add_u32 s14, s30, 0x4700
	s_addc_u32 s15, s31, 0
	s_add_u32 s16, s30, 0x4800
	s_addc_u32 s17, s31, 0
	s_add_u32 s18, s30, 0x4900
	s_addc_u32 s19, s31, 0
	s_add_u32 s20, s30, 0x4a00
	s_addc_u32 s21, s31, 0
	s_add_u32 s22, s30, 0x4b00
	s_addc_u32 s23, s31, 0
	s_add_u32 s24, s30, 0x4c00
	s_addc_u32 s25, s31, 0
	s_add_u32 s26, s30, 0x4d00
	s_addc_u32 s27, s31, 0
	s_add_u32 s28, s30, 0x4e00
	s_addc_u32 s29, s31, 0
	s_add_u32 s42, s30, 0x4f00
	s_addc_u32 s43, s31, 0
	s_add_u32 s44, s30, 0x5000
	s_addc_u32 s45, s31, 0
	s_add_u32 s46, s30, 0x5100
	s_addc_u32 s47, s31, 0
	s_add_u32 s48, s30, 0x5200
	s_addc_u32 s49, s31, 0
	s_add_u32 s50, s30, 0x5300
	s_addc_u32 s51, s31, 0
	s_mov_b32 s59, 1
	v_mov_b32_e32 v17, 0
	s_branch .LBB0_382

; __device__ __forceinline__ unsigned cvt_pk_bf16(float lo, float hi) { unsigned r; asm volatile("v_cvt_pk_bf16_f32 %0, %1, %2" : "=v"(r) : "v"(lo), "v"(hi)); return r; }
;     __device__ __forceinline__ void operator()(const f32x4 (&acc)[2][2][4][2], const Unit& u, int wr, int wc, int fr, int fq) const {
;     ...
;         } else {
;             unsigned char* base = wb + OFF_U + (unsigned)((pn - 6) * 128 + cl) * 2u;
; #pragma unroll
;             for (int ai = 0; ai < 2; ++ai)
; #pragma unroll
;                 for (int m = 0; m < 4; ++m) { unsigned char* rowp = base + (unsigned)((row0 + ai * HALF + m * 16) * 512) * 2u;
;                     float o[8];
; #pragma unroll
;                     for (int n = 0; n < 2; ++n)
; #pragma unroll
;                         for (int e = 0; e < 4; ++e) { const float a = acc[ai][0][m][n][e], g = acc[ai][1][m][n][e];
;                             o[4 * n + e] = a * __builtin_amdgcn_rcpf(1.0f + __builtin_amdgcn_exp2f(-1.4426950408889634f * g)); }
;                     u32x4 w; w.x = cvt_pk_bf16(o[0], o[1]); w.y = cvt_pk_bf16(o[2], o[3]); w.z = cvt_pk_bf16(o[4], o[5]); w.w = cvt_pk_bf16(o[6], o[7]);
;                     *(u32x4*)rowp = w; }
.LBB0_1123:
	s_lshl_b32 s8, s14, 8
	s_mov_b64 s[46:47], s[10:11]
	v_mov_b32_e32 v128, v178
	s_add_i32 s8, s8, s70
	s_cmp_gt_i32 s48, 3
	v_add_u32_e32 v191, s8, v128
	s_mov_b64 s[8:9], -1
	v_lshlrev_b32_e32 v144, 10, v191
	s_cbranch_scc0 .LBB0_1129
	s_cmp_gt_u32 s48, 5
	v_add_u32_e32 v158, 0x4000, v144
	v_add_u32_e32 v156, 0x8000, v144
	v_add_u32_e32 v154, 0xc000, v144
	v_add_u32_e32 v134, 0x20000, v144
	v_add_u32_e32 v132, 0x24000, v144
	v_add_u32_e32 v130, 0x28000, v144
	v_add_u32_e32 v128, 0x2c000, v144
	s_cbranch_scc0 .LBB0_1126
	v_mul_f32_e32 v129, 0xbfb8aa3b, v116
	v_mul_f32_e32 v131, 0xbfb8aa3b, v117
	v_mul_f32_e32 v133, 0xbfb8aa3b, v118
	v_mul_f32_e32 v135, 0xbfb8aa3b, v119
	v_mul_f32_e32 v162, 0xbfb8aa3b, v115
	v_exp_f32_e32 v129, v129
	v_exp_f32_e32 v131, v131
	v_exp_f32_e32 v133, v133
	v_exp_f32_e32 v135, v135
	v_mul_f32_e32 v155, 0xbfb8aa3b, v112
	v_mul_f32_e32 v157, 0xbfb8aa3b, v113
	v_mul_f32_e32 v159, 0xbfb8aa3b, v114
	v_exp_f32_e32 v162, v162
	v_exp_f32_e32 v155, v155
	v_exp_f32_e32 v157, v157
	v_exp_f32_e32 v159, v159
	v_add_f32_e32 v129, 1.0, v129
	v_add_f32_e32 v131, 1.0, v131
	v_add_f32_e32 v133, 1.0, v133
	v_add_f32_e32 v135, 1.0, v135
	v_add_f32_e32 v162, 1.0, v162
	v_rcp_f32_e32 v129, v129
	v_rcp_f32_e32 v131, v131
	v_rcp_f32_e32 v133, v133
	v_rcp_f32_e32 v135, v135
	v_add_f32_e32 v155, 1.0, v155
	v_add_f32_e32 v157, 1.0, v157
	v_add_f32_e32 v159, 1.0, v159
	v_rcp_f32_e32 v162, v162
	v_lshl_add_u32 v160, s48, 8, v183
	v_mov_b32_e32 v161, v145
	v_rcp_f32_e32 v155, v155
	v_rcp_f32_e32 v157, v157
	v_rcp_f32_e32 v159, v159
	v_lshl_add_u64 v[160:161], s[46:47], 0, v[160:161]
	v_lshl_add_u64 v[160:161], v[160:161], 0, s[22:23]
	v_mul_f32_e32 v129, v124, v129
	v_mul_f32_e32 v131, v125, v131
	v_mul_f32_e32 v133, v126, v133
	v_mul_f32_e32 v135, v127, v135
	v_mul_f32_e32 v165, v123, v162
	v_lshl_add_u64 v[166:167], v[160:161], 0, v[144:145]
	v_cvt_pk_bf16_f32 v162, v129, v131
	v_cvt_pk_bf16_f32 v163, v133, v135
	v_mul_f32_e32 v155, v120, v155
	v_mul_f32_e32 v157, v121, v157
	v_mul_f32_e32 v159, v122, v159
	v_cvt_pk_bf16_f32 v164, v155, v157
	v_mul_f32_e32 v129, 0xbfb8aa3b, v100
	v_cvt_pk_bf16_f32 v165, v159, v165
	flat_store_dwordx4 v[166:167], v[162:165] sc1
	v_mul_f32_e32 v131, 0xbfb8aa3b, v101
	v_mul_f32_e32 v133, 0xbfb8aa3b, v102
	v_mul_f32_e32 v135, 0xbfb8aa3b, v103
	v_mul_f32_e32 v162, 0xbfb8aa3b, v98
	v_mul_f32_e32 v163, 0xbfb8aa3b, v99
	v_exp_f32_e32 v129, v129
	v_exp_f32_e32 v131, v131
	v_exp_f32_e32 v133, v133
	v_exp_f32_e32 v135, v135
	v_mul_f32_e32 v155, 0xbfb8aa3b, v96
	v_mul_f32_e32 v157, 0xbfb8aa3b, v97
	v_exp_f32_e32 v162, v162
	v_exp_f32_e32 v163, v163
	v_exp_f32_e32 v155, v155
	v_exp_f32_e32 v157, v157
	v_add_f32_e32 v129, 1.0, v129
	v_add_f32_e32 v131, 1.0, v131
	v_add_f32_e32 v133, 1.0, v133
	v_add_f32_e32 v135, 1.0, v135
	v_add_f32_e32 v162, 1.0, v162
	v_add_f32_e32 v163, 1.0, v163
	v_rcp_f32_e32 v129, v129
	v_rcp_f32_e32 v131, v131
	v_rcp_f32_e32 v133, v133
	v_rcp_f32_e32 v135, v135
	v_add_f32_e32 v155, 1.0, v155
	v_add_f32_e32 v157, 1.0, v157
	v_rcp_f32_e32 v162, v162
	v_rcp_f32_e32 v163, v163
	v_rcp_f32_e32 v155, v155
	v_rcp_f32_e32 v157, v157
	v_mov_b32_e32 v159, v145
	v_mul_f32_e32 v129, v108, v129
	v_mul_f32_e32 v131, v109, v131
	v_mul_f32_e32 v133, v110, v133
	v_mul_f32_e32 v135, v111, v135
	v_mul_f32_e32 v165, v106, v162
	v_mul_f32_e32 v168, v107, v163
	v_lshl_add_u64 v[166:167], v[160:161], 0, v[158:159]
	v_cvt_pk_bf16_f32 v162, v129, v131
	v_cvt_pk_bf16_f32 v163, v133, v135
	v_mul_f32_e32 v155, v104, v155
	v_mul_f32_e32 v157, v105, v157
	v_cvt_pk_bf16_f32 v164, v155, v157
	v_mul_f32_e32 v129, 0xbfb8aa3b, v84
	v_cvt_pk_bf16_f32 v165, v165, v168
	flat_store_dwordx4 v[166:167], v[162:165] sc1
	v_mul_f32_e32 v131, 0xbfb8aa3b, v85
	v_mul_f32_e32 v133, 0xbfb8aa3b, v86
	v_mul_f32_e32 v135, 0xbfb8aa3b, v87
	v_mul_f32_e32 v162, 0xbfb8aa3b, v82
	v_mul_f32_e32 v163, 0xbfb8aa3b, v83
	v_exp_f32_e32 v129, v129
	v_exp_f32_e32 v131, v131
	v_exp_f32_e32 v133, v133
	v_exp_f32_e32 v135, v135
	v_mul_f32_e32 v155, 0xbfb8aa3b, v80
	v_mul_f32_e32 v159, 0xbfb8aa3b, v81
	v_exp_f32_e32 v162, v162
	v_exp_f32_e32 v163, v163
	v_exp_f32_e32 v155, v155
	v_exp_f32_e32 v159, v159
	v_add_f32_e32 v129, 1.0, v129
	v_add_f32_e32 v131, 1.0, v131
	v_add_f32_e32 v133, 1.0, v133
	v_add_f32_e32 v135, 1.0, v135
	v_add_f32_e32 v162, 1.0, v162
	v_add_f32_e32 v163, 1.0, v163
	v_rcp_f32_e32 v129, v129
	v_rcp_f32_e32 v131, v131
	v_rcp_f32_e32 v133, v133
	v_rcp_f32_e32 v135, v135
	v_add_f32_e32 v155, 1.0, v155
	v_add_f32_e32 v159, 1.0, v159
	v_rcp_f32_e32 v162, v162
	v_rcp_f32_e32 v163, v163
	v_rcp_f32_e32 v155, v155
	v_rcp_f32_e32 v159, v159
	v_mov_b32_e32 v157, v145
	v_mul_f32_e32 v129, v92, v129
	v_mul_f32_e32 v131, v93, v131
	v_mul_f32_e32 v133, v94, v133
	v_mul_f32_e32 v135, v95, v135
	v_mul_f32_e32 v165, v90, v162
	v_mul_f32_e32 v168, v91, v163
	v_lshl_add_u64 v[166:167], v[160:161], 0, v[156:157]
	v_cvt_pk_bf16_f32 v162, v129, v131
	v_cvt_pk_bf16_f32 v163, v133, v135
	v_mul_f32_e32 v155, v88, v155
	v_mul_f32_e32 v159, v89, v159
	v_cvt_pk_bf16_f32 v164, v155, v159
	v_mul_f32_e32 v129, 0xbfb8aa3b, v68
	v_cvt_pk_bf16_f32 v165, v165, v168
	flat_store_dwordx4 v[166:167], v[162:165] sc1
	v_mul_f32_e32 v131, 0xbfb8aa3b, v69
	v_mul_f32_e32 v133, 0xbfb8aa3b, v70
	v_mul_f32_e32 v135, 0xbfb8aa3b, v71
	v_mul_f32_e32 v162, 0xbfb8aa3b, v66
	v_mul_f32_e32 v163, 0xbfb8aa3b, v67
	v_exp_f32_e32 v129, v129
	v_exp_f32_e32 v131, v131
	v_exp_f32_e32 v133, v133
	v_exp_f32_e32 v135, v135
	v_mul_f32_e32 v157, 0xbfb8aa3b, v64
	v_mul_f32_e32 v159, 0xbfb8aa3b, v65
	v_exp_f32_e32 v162, v162
	v_exp_f32_e32 v163, v163
	v_exp_f32_e32 v157, v157
	v_exp_f32_e32 v159, v159
; __device__ __forceinline__ unsigned cvt_pk_bf16(float lo, float hi) { unsigned r; asm volatile("v_cvt_pk_bf16_f32 %0, %1, %2" : "=v"(r) : "v"(lo), "v"(hi)); return r; }
;     __device__ __forceinline__ void operator()(const f32x4 (&acc)[2][2][4][2], const Unit& u, int wr, int wc, int fr, int fq) const {
;     ...
;             unsigned char* base = wb + OFF_U + (unsigned)((pn - 6) * 128 + cl) * 2u;
; #pragma unroll
;             for (int ai = 0; ai < 2; ++ai)
; #pragma unroll
;                 for (int m = 0; m < 4; ++m) { unsigned char* rowp = base + (unsigned)((row0 + ai * HALF + m * 16) * 512) * 2u;
;                     float o[8];
; #pragma unroll
;                     for (int n = 0; n < 2; ++n)
; #pragma unroll
;                         for (int e = 0; e < 4; ++e) { const float a = acc[ai][0][m][n][e], g = acc[ai][1][m][n][e];
;                             o[4 * n + e] = a * __builtin_amdgcn_rcpf(1.0f + __builtin_amdgcn_exp2f(-1.4426950408889634f * g)); }
;                     u32x4 w; w.x = cvt_pk_bf16(o[0], o[1]); w.y = cvt_pk_bf16(o[2], o[3]); w.z = cvt_pk_bf16(o[4], o[5]); w.w = cvt_pk_bf16(o[6], o[7]);
;                     *(u32x4*)rowp = w; }
	v_add_f32_e32 v129, 1.0, v129
	v_add_f32_e32 v131, 1.0, v131
	v_add_f32_e32 v133, 1.0, v133
	v_add_f32_e32 v135, 1.0, v135
	v_add_f32_e32 v162, 1.0, v162
	v_add_f32_e32 v163, 1.0, v163
	v_rcp_f32_e32 v129, v129
	v_rcp_f32_e32 v131, v131
	v_rcp_f32_e32 v133, v133
	v_rcp_f32_e32 v135, v135
	v_add_f32_e32 v157, 1.0, v157
	v_add_f32_e32 v159, 1.0, v159
	v_rcp_f32_e32 v162, v162
	v_rcp_f32_e32 v163, v163
	v_rcp_f32_e32 v157, v157
	v_rcp_f32_e32 v159, v159
	v_mov_b32_e32 v155, v145
	v_mul_f32_e32 v129, v76, v129
	v_mul_f32_e32 v131, v77, v131
	v_mul_f32_e32 v133, v78, v133
	v_mul_f32_e32 v135, v79, v135
	v_mul_f32_e32 v165, v74, v162
	v_mul_f32_e32 v168, v75, v163
	v_lshl_add_u64 v[166:167], v[160:161], 0, v[154:155]
	v_cvt_pk_bf16_f32 v162, v129, v131
	v_cvt_pk_bf16_f32 v163, v133, v135
	v_mul_f32_e32 v157, v72, v157
	v_mul_f32_e32 v159, v73, v159
	v_cvt_pk_bf16_f32 v164, v157, v159
	v_mul_f32_e32 v129, 0xbfb8aa3b, v52
	v_cvt_pk_bf16_f32 v165, v165, v168
	flat_store_dwordx4 v[166:167], v[162:165] sc1
	v_mul_f32_e32 v131, 0xbfb8aa3b, v53
	v_mul_f32_e32 v133, 0xbfb8aa3b, v54
	v_mul_f32_e32 v155, 0xbfb8aa3b, v55
	v_mul_f32_e32 v162, 0xbfb8aa3b, v50
	v_mul_f32_e32 v163, 0xbfb8aa3b, v51
	v_exp_f32_e32 v129, v129
	v_exp_f32_e32 v131, v131
	v_exp_f32_e32 v133, v133
	v_exp_f32_e32 v155, v155
	v_mul_f32_e32 v157, 0xbfb8aa3b, v48
	v_mul_f32_e32 v159, 0xbfb8aa3b, v49
	v_exp_f32_e32 v162, v162
	v_exp_f32_e32 v163, v163
	v_exp_f32_e32 v157, v157
	v_exp_f32_e32 v159, v159
	v_add_f32_e32 v129, 1.0, v129
	v_add_f32_e32 v131, 1.0, v131
	v_add_f32_e32 v133, 1.0, v133
	v_add_f32_e32 v155, 1.0, v155
	v_add_f32_e32 v162, 1.0, v162
	v_add_f32_e32 v163, 1.0, v163
	v_rcp_f32_e32 v129, v129
	v_rcp_f32_e32 v131, v131
	v_rcp_f32_e32 v133, v133
	v_rcp_f32_e32 v155, v155
	v_add_f32_e32 v157, 1.0, v157
	v_add_f32_e32 v159, 1.0, v159
	v_rcp_f32_e32 v162, v162
	v_rcp_f32_e32 v163, v163
	v_rcp_f32_e32 v157, v157
	v_rcp_f32_e32 v159, v159
	v_mov_b32_e32 v135, v145
	v_mul_f32_e32 v129, v60, v129
	v_mul_f32_e32 v131, v61, v131
	v_mul_f32_e32 v133, v62, v133
	v_mul_f32_e32 v155, v63, v155
	v_mul_f32_e32 v165, v58, v162
	v_mul_f32_e32 v168, v59, v163
	v_lshl_add_u64 v[166:167], v[160:161], 0, v[134:135]
	v_cvt_pk_bf16_f32 v162, v129, v131
	v_cvt_pk_bf16_f32 v163, v133, v155
	v_mul_f32_e32 v157, v56, v157
	v_mul_f32_e32 v159, v57, v159
	v_cvt_pk_bf16_f32 v164, v157, v159
	v_mul_f32_e32 v129, 0xbfb8aa3b, v36
	v_cvt_pk_bf16_f32 v165, v165, v168
	flat_store_dwordx4 v[166:167], v[162:165] sc1
	v_mul_f32_e32 v131, 0xbfb8aa3b, v37
	v_mul_f32_e32 v135, 0xbfb8aa3b, v38
	v_mul_f32_e32 v155, 0xbfb8aa3b, v39
	v_mul_f32_e32 v162, 0xbfb8aa3b, v34
	v_mul_f32_e32 v163, 0xbfb8aa3b, v35
	v_exp_f32_e32 v129, v129
	v_exp_f32_e32 v131, v131
	v_exp_f32_e32 v135, v135
	v_exp_f32_e32 v155, v155
	v_mul_f32_e32 v157, 0xbfb8aa3b, v32
	v_mul_f32_e32 v159, 0xbfb8aa3b, v33
	v_exp_f32_e32 v162, v162
	v_exp_f32_e32 v163, v163
	v_exp_f32_e32 v157, v157
	v_exp_f32_e32 v159, v159
	v_add_f32_e32 v129, 1.0, v129
	v_add_f32_e32 v131, 1.0, v131
	v_add_f32_e32 v135, 1.0, v135
	v_add_f32_e32 v155, 1.0, v155
	v_add_f32_e32 v162, 1.0, v162
	v_add_f32_e32 v163, 1.0, v163
	v_rcp_f32_e32 v129, v129
	v_rcp_f32_e32 v131, v131
	v_rcp_f32_e32 v135, v135
	v_rcp_f32_e32 v155, v155
	v_add_f32_e32 v157, 1.0, v157
	v_add_f32_e32 v159, 1.0, v159
	v_rcp_f32_e32 v162, v162
	v_rcp_f32_e32 v163, v163
	v_rcp_f32_e32 v157, v157
	v_rcp_f32_e32 v159, v159
	v_mov_b32_e32 v133, v145
	v_mul_f32_e32 v129, v44, v129
	v_mul_f32_e32 v131, v45, v131
	v_mul_f32_e32 v135, v46, v135
	v_mul_f32_e32 v155, v47, v155
	v_mul_f32_e32 v165, v42, v162
	v_mul_f32_e32 v168, v43, v163
	v_lshl_add_u64 v[166:167], v[160:161], 0, v[132:133]
	v_cvt_pk_bf16_f32 v162, v129, v131
	v_cvt_pk_bf16_f32 v163, v135, v155
	v_mul_f32_e32 v157, v40, v157
	v_mul_f32_e32 v159, v41, v159
	v_cvt_pk_bf16_f32 v164, v157, v159
	v_mul_f32_e32 v129, 0xbfb8aa3b, v20
	v_cvt_pk_bf16_f32 v165, v165, v168
	flat_store_dwordx4 v[166:167], v[162:165] sc1
	v_mul_f32_e32 v133, 0xbfb8aa3b, v21
	v_mul_f32_e32 v135, 0xbfb8aa3b, v22
	v_mul_f32_e32 v155, 0xbfb8aa3b, v23
	v_mul_f32_e32 v162, 0xbfb8aa3b, v18
	v_mul_f32_e32 v163, 0xbfb8aa3b, v19
	v_exp_f32_e32 v129, v129
	v_exp_f32_e32 v133, v133
	v_exp_f32_e32 v135, v135
	v_exp_f32_e32 v155, v155
	v_mul_f32_e32 v157, 0xbfb8aa3b, v16
	v_mul_f32_e32 v159, 0xbfb8aa3b, v17
	v_exp_f32_e32 v162, v162
	v_exp_f32_e32 v163, v163
	v_exp_f32_e32 v157, v157
	v_exp_f32_e32 v159, v159
	v_add_f32_e32 v129, 1.0, v129
	v_add_f32_e32 v133, 1.0, v133
	v_add_f32_e32 v135, 1.0, v135
	v_add_f32_e32 v155, 1.0, v155
	v_add_f32_e32 v162, 1.0, v162
	v_add_f32_e32 v163, 1.0, v163
	v_rcp_f32_e32 v129, v129
	v_rcp_f32_e32 v133, v133
	v_rcp_f32_e32 v135, v135
	v_rcp_f32_e32 v155, v155
	v_add_f32_e32 v157, 1.0, v157
	v_add_f32_e32 v159, 1.0, v159
	v_rcp_f32_e32 v162, v162
	v_rcp_f32_e32 v163, v163
	v_rcp_f32_e32 v157, v157
	v_rcp_f32_e32 v159, v159
	v_mov_b32_e32 v131, v145
	v_mul_f32_e32 v129, v28, v129
	v_mul_f32_e32 v133, v29, v133
	v_mul_f32_e32 v135, v30, v135
	v_mul_f32_e32 v155, v31, v155
	v_mul_f32_e32 v165, v26, v162
	v_mul_f32_e32 v168, v27, v163
	v_lshl_add_u64 v[166:167], v[160:161], 0, v[130:131]
	v_cvt_pk_bf16_f32 v162, v129, v133
	v_cvt_pk_bf16_f32 v163, v135, v155
	v_mul_f32_e32 v157, v24, v157
	v_mul_f32_e32 v159, v25, v159
	v_cvt_pk_bf16_f32 v164, v157, v159
	v_cvt_pk_bf16_f32 v165, v165, v168
	flat_store_dwordx4 v[166:167], v[162:165] sc1
	v_mul_f32_e32 v129, 0xbfb8aa3b, v4
	v_mul_f32_e32 v133, 0xbfb8aa3b, v5
	v_mul_f32_e32 v163, 0xbfb8aa3b, v3
	v_mul_f32_e32 v135, 0xbfb8aa3b, v6
	v_mul_f32_e32 v155, 0xbfb8aa3b, v7
	v_mul_f32_e32 v157, 0xbfb8aa3b, v0
	v_mul_f32_e32 v159, 0xbfb8aa3b, v1
	v_mul_f32_e32 v162, 0xbfb8aa3b, v2
	v_exp_f32_e32 v163, v163
	v_exp_f32_e32 v131, v129
	v_exp_f32_e32 v133, v133
	v_exp_f32_e32 v135, v135
	v_exp_f32_e32 v155, v155
	v_exp_f32_e32 v157, v157
	v_exp_f32_e32 v159, v159
	v_exp_f32_e32 v162, v162
	v_add_f32_e32 v163, 1.0, v163
	v_add_f32_e32 v131, 1.0, v131
	v_add_f32_e32 v133, 1.0, v133
	v_add_f32_e32 v135, 1.0, v135
	v_add_f32_e32 v155, 1.0, v155
	v_add_f32_e32 v157, 1.0, v157
	v_add_f32_e32 v159, 1.0, v159
	v_add_f32_e32 v162, 1.0, v162
	v_rcp_f32_e32 v163, v163
	v_rcp_f32_e32 v131, v131
	v_rcp_f32_e32 v133, v133
	v_rcp_f32_e32 v135, v135
	v_rcp_f32_e32 v155, v155
	v_rcp_f32_e32 v157, v157
	v_rcp_f32_e32 v159, v159
	v_rcp_f32_e32 v162, v162
	v_mov_b32_e32 v129, v145
	v_mul_f32_e32 v163, v11, v163
	v_lshl_add_u64 v[164:165], v[160:161], 0, v[128:129]
	v_mul_f32_e32 v131, v12, v131
	v_mul_f32_e32 v133, v13, v133
	v_mul_f32_e32 v135, v14, v135
	v_mul_f32_e32 v155, v15, v155
	v_mul_f32_e32 v157, v8, v157
	v_mul_f32_e32 v159, v9, v159
	v_mul_f32_e32 v166, v10, v162
	v_cvt_pk_bf16_f32 v160, v131, v133
	v_cvt_pk_bf16_f32 v161, v135, v155
	v_cvt_pk_bf16_f32 v162, v157, v159
	v_cvt_pk_bf16_f32 v163, v166, v163
	flat_store_dwordx4 v[164:165], v[160:163] sc1
	s_mov_b64 s[8:9], 0

; __device__ __forceinline__ unsigned cvt_pk_bf16(float lo, float hi) { unsigned r; asm volatile("v_cvt_pk_bf16_f32 %0, %1, %2" : "=v"(r) : "v"(lo), "v"(hi)); return r; }
;     __device__ __forceinline__ void operator()(const f32x4 (&acc)[2][2][4][2], const Unit& u, int wr, int wc, int fr, int fq) const {
;     ...
;                 for (int m = 0; m < 4; ++m) {
;                     const int row = row0 + ai * HALF + m * 16, pos = row & 4095;
;                     const unsigned ro = (unsigned)(pos * 32 + i0) * 4u; const f32x4 c4 = *(const f32x4*)(cs + ro), s4 = *(const f32x4*)(sn + ro);
; #pragma unroll
;                     for (int bj = 0; bj < 2; ++bj) {
;                         const f32x4 v0 = acc[ai][bj][m][0], v1 = acc[ai][bj][m][1];
;                         float o[8];
;                         o[0] = v0[0] * c4[0] - v0[1] * s4[0]; o[1] = v0[1] * c4[0] + v0[0] * s4[0];
;                         o[2] = v0[2] * c4[1] - v0[3] * s4[1]; o[3] = v0[3] * c4[1] + v0[2] * s4[1];
;                         o[4] = v1[0] * c4[2] - v1[1] * s4[2]; o[5] = v1[1] * c4[2] + v1[0] * s4[2];
;                         o[6] = v1[2] * c4[3] - v1[3] * s4[3]; o[7] = v1[3] * c4[3] + v1[2] * s4[3];
;                         if (!isq) {
; #pragma unroll
;                             for (int e = 0; e < 8; ++e) ks[bj][e] += o[e]; }
;                         u32x4 w; w.x = cvt_pk_bf16(o[0] * sc, o[1] * sc); w.y = cvt_pk_bf16(o[2] * sc, o[3] * sc); w.z = cvt_pk_bf16(o[4] * sc, o[5] * sc); w.w = cvt_pk_bf16(o[6] * sc, o[7] * sc);
;                         *(u32x4*)(base + (unsigned)(row * 512 + bj * HALF) * 2u) = w;
.LBB0_1136:
	v_mul_f32_e32 v112, v167, v117
	v_mul_f32_e32 v114, v167, v162
	v_cvt_pk_bf16_f32 v168, v112, v114
	v_mul_f32_e32 v112, v167, v165
	v_mul_f32_e32 v114, v167, v132
	v_cvt_pk_bf16_f32 v169, v112, v114
	v_mul_f32_e32 v112, v167, v113
	v_mul_f32_e32 v113, v167, v118
	v_cvt_pk_bf16_f32 v170, v112, v113
	v_mul_f32_e32 v112, v167, v115
	v_add_u32_e32 v164, 16, v191
	v_mul_f32_e32 v113, v167, v134
	v_cvt_pk_bf16_f32 v171, v112, v113
	v_lshlrev_b32_e32 v112, 7, v164
	v_and_or_b32 v144, v112, s78, v182
	v_lshl_add_u64 v[112:113], s[54:55], 0, v[144:145]
	flat_load_dwordx4 v[112:115], v[112:113]
	v_lshl_add_u64 v[116:117], s[52:53], 0, v[144:145]
	flat_load_dwordx4 v[116:119], v[116:117]
	s_and_b64 vcc, exec, s[8:9]
	flat_store_dwordx4 v[160:161], v[168:171] offset:256 sc1
	s_waitcnt vmcnt(0) lgkmcnt(0)
	v_pk_mul_f32 v[132:133], v[108:109], v[112:113] op_sel_hi:[1,0]
	v_pk_mul_f32 v[160:161], v[110:111], v[112:113] op_sel:[0,1]
	v_pk_mul_f32 v[168:169], v[104:105], v[114:115] op_sel_hi:[1,0]
	v_mov_b32_e32 v144, v115
	v_mov_b32_e32 v166, v119
	v_pk_fma_f32 v[134:135], v[108:109], v[116:117], v[132:133] op_sel:[0,0,1] op_sel_hi:[1,0,0]
	v_pk_fma_f32 v[162:163], v[108:109], v[116:117], v[132:133] op_sel:[0,0,1] op_sel_hi:[1,0,0] neg_lo:[1,0,0] neg_hi:[1,0,0]
	v_pk_fma_f32 v[132:133], v[110:111], v[116:117], v[160:161] op_sel:[0,1,1] op_sel_hi:[1,1,0]
	v_pk_fma_f32 v[160:161], v[110:111], v[116:117], v[160:161] op_sel:[0,1,1] op_sel_hi:[1,1,0] neg_lo:[1,0,0] neg_hi:[1,0,0]
	v_pk_fma_f32 v[108:109], v[104:105], v[118:119], v[168:169] op_sel:[0,0,1] op_sel_hi:[1,0,0]
	v_pk_fma_f32 v[110:111], v[104:105], v[118:119], v[168:169] op_sel:[0,0,1] op_sel_hi:[1,0,0] neg_lo:[1,0,0] neg_hi:[1,0,0]
	v_pk_mul_f32 v[168:169], v[106:107], v[144:145] op_sel_hi:[1,0]
	s_nop 0
	v_pk_fma_f32 v[104:105], v[106:107], v[166:167], v[168:169] op_sel:[0,0,1] op_sel_hi:[1,0,0]
	v_pk_fma_f32 v[106:107], v[106:107], v[166:167], v[168:169] op_sel:[0,0,1] op_sel_hi:[1,0,0] neg_lo:[1,0,0] neg_hi:[1,0,0]
	s_cbranch_vccnz .LBB0_1138
	v_mov_b32_e32 v105, v107
	v_mov_b32_e32 v109, v111
	v_mov_b32_e32 v133, v161
	v_mov_b32_e32 v135, v163
	v_pk_add_f32 v[156:157], v[156:157], v[134:135]
	v_pk_add_f32 v[154:155], v[154:155], v[132:133]
	v_pk_add_f32 v[122:123], v[122:123], v[108:109]
	v_pk_add_f32 v[120:121], v[120:121], v[104:105]

; __device__ __forceinline__ unsigned cvt_pk_bf16(float lo, float hi) { unsigned r; asm volatile("v_cvt_pk_bf16_f32 %0, %1, %2" : "=v"(r) : "v"(lo), "v"(hi)); return r; }
;     __device__ __forceinline__ void operator()(const f32x4 (&acc)[2][2][4][2], const Unit& u, int wr, int wc, int fr, int fq) const {
;     ...
;                 for (int m = 0; m < 4; ++m) {
;                     const int row = row0 + ai * HALF + m * 16, pos = row & 4095;
;                     const unsigned ro = (unsigned)(pos * 32 + i0) * 4u; const f32x4 c4 = *(const f32x4*)(cs + ro), s4 = *(const f32x4*)(sn + ro);
; #pragma unroll
;                     for (int bj = 0; bj < 2; ++bj) {
;                         const f32x4 v0 = acc[ai][bj][m][0], v1 = acc[ai][bj][m][1];
;                         float o[8];
;                         o[0] = v0[0] * c4[0] - v0[1] * s4[0]; o[1] = v0[1] * c4[0] + v0[0] * s4[0];
;                         o[2] = v0[2] * c4[1] - v0[3] * s4[1]; o[3] = v0[3] * c4[1] + v0[2] * s4[1];
;                         o[4] = v1[0] * c4[2] - v1[1] * s4[2]; o[5] = v1[1] * c4[2] + v1[0] * s4[2];
;                         o[6] = v1[2] * c4[3] - v1[3] * s4[3]; o[7] = v1[3] * c4[3] + v1[2] * s4[3];
;                         if (!isq) {
; #pragma unroll
;                             for (int e = 0; e < 8; ++e) ks[bj][e] += o[e]; }
;                         u32x4 w; w.x = cvt_pk_bf16(o[0] * sc, o[1] * sc); w.y = cvt_pk_bf16(o[2] * sc, o[3] * sc); w.z = cvt_pk_bf16(o[4] * sc, o[5] * sc); w.w = cvt_pk_bf16(o[6] * sc, o[7] * sc);
;                         *(u32x4*)(base + (unsigned)(row * 512 + bj * HALF) * 2u) = w;
.LBB0_1140:
	v_mul_f32_e32 v96, v167, v101
	v_mul_f32_e32 v98, v167, v106
	v_cvt_pk_bf16_f32 v106, v96, v98
	v_mul_f32_e32 v96, v167, v111
	v_mul_f32_e32 v98, v167, v108
	v_cvt_pk_bf16_f32 v107, v96, v98
	v_mul_f32_e32 v96, v167, v97
	v_mul_f32_e32 v97, v167, v102
	v_cvt_pk_bf16_f32 v108, v96, v97
	v_mul_f32_e32 v96, v167, v99
	v_mul_f32_e32 v97, v167, v112
	v_add_u32_e32 v112, 32, v191
	v_cvt_pk_bf16_f32 v109, v96, v97
	v_lshlrev_b32_e32 v96, 7, v112
	v_and_or_b32 v144, v96, s78, v182
	v_lshl_add_u64 v[96:97], s[54:55], 0, v[144:145]
	flat_load_dwordx4 v[96:99], v[96:97]
	v_lshl_add_u64 v[100:101], s[52:53], 0, v[144:145]
	flat_load_dwordx4 v[100:103], v[100:101]
	s_and_b64 vcc, exec, s[8:9]
	flat_store_dwordx4 v[104:105], v[106:109] offset:256 sc1
	s_waitcnt vmcnt(0) lgkmcnt(0)
	v_pk_mul_f32 v[104:105], v[92:93], v[96:97] op_sel_hi:[1,0]
	v_pk_mul_f32 v[108:109], v[94:95], v[96:97] op_sel:[0,1]
	v_pk_mul_f32 v[114:115], v[88:89], v[98:99] op_sel_hi:[1,0]
	v_mov_b32_e32 v116, v99
	v_mov_b32_e32 v118, v103
	v_pk_fma_f32 v[106:107], v[92:93], v[100:101], v[104:105] op_sel:[0,0,1] op_sel_hi:[1,0,0]
	v_pk_fma_f32 v[110:111], v[92:93], v[100:101], v[104:105] op_sel:[0,0,1] op_sel_hi:[1,0,0] neg_lo:[1,0,0] neg_hi:[1,0,0]
	v_pk_fma_f32 v[104:105], v[94:95], v[100:101], v[108:109] op_sel:[0,1,1] op_sel_hi:[1,1,0]
	v_pk_fma_f32 v[108:109], v[94:95], v[100:101], v[108:109] op_sel:[0,1,1] op_sel_hi:[1,1,0] neg_lo:[1,0,0] neg_hi:[1,0,0]
	v_pk_fma_f32 v[92:93], v[88:89], v[102:103], v[114:115] op_sel:[0,0,1] op_sel_hi:[1,0,0]
	v_pk_fma_f32 v[94:95], v[88:89], v[102:103], v[114:115] op_sel:[0,0,1] op_sel_hi:[1,0,0] neg_lo:[1,0,0] neg_hi:[1,0,0]
	v_pk_mul_f32 v[114:115], v[90:91], v[116:117] op_sel_hi:[1,0]
	s_nop 0
	v_pk_fma_f32 v[88:89], v[90:91], v[118:119], v[114:115] op_sel:[0,0,1] op_sel_hi:[1,0,0]
	v_pk_fma_f32 v[90:91], v[90:91], v[118:119], v[114:115] op_sel:[0,0,1] op_sel_hi:[1,0,0] neg_lo:[1,0,0] neg_hi:[1,0,0]
	s_cbranch_vccnz .LBB0_1142
	v_mov_b32_e32 v89, v91
	v_mov_b32_e32 v93, v95
	v_mov_b32_e32 v105, v109
	v_mov_b32_e32 v107, v111
	v_pk_add_f32 v[156:157], v[156:157], v[106:107]
	v_pk_add_f32 v[154:155], v[154:155], v[104:105]
	v_pk_add_f32 v[122:123], v[122:123], v[92:93]
	v_pk_add_f32 v[120:121], v[120:121], v[88:89]

; __device__ __forceinline__ unsigned cvt_pk_bf16(float lo, float hi) { unsigned r; asm volatile("v_cvt_pk_bf16_f32 %0, %1, %2" : "=v"(r) : "v"(lo), "v"(hi)); return r; }
;     __device__ __forceinline__ void operator()(const f32x4 (&acc)[2][2][4][2], const Unit& u, int wr, int wc, int fr, int fq) const {
;     ...
;                 for (int m = 0; m < 4; ++m) {
;                     const int row = row0 + ai * HALF + m * 16, pos = row & 4095;
;                     const unsigned ro = (unsigned)(pos * 32 + i0) * 4u; const f32x4 c4 = *(const f32x4*)(cs + ro), s4 = *(const f32x4*)(sn + ro);
; #pragma unroll
;                     for (int bj = 0; bj < 2; ++bj) {
;                         const f32x4 v0 = acc[ai][bj][m][0], v1 = acc[ai][bj][m][1];
;                         float o[8];
;                         o[0] = v0[0] * c4[0] - v0[1] * s4[0]; o[1] = v0[1] * c4[0] + v0[0] * s4[0];
;                         o[2] = v0[2] * c4[1] - v0[3] * s4[1]; o[3] = v0[3] * c4[1] + v0[2] * s4[1];
;                         o[4] = v1[0] * c4[2] - v1[1] * s4[2]; o[5] = v1[1] * c4[2] + v1[0] * s4[2];
;                         o[6] = v1[2] * c4[3] - v1[3] * s4[3]; o[7] = v1[3] * c4[3] + v1[2] * s4[3];
;                         if (!isq) {
; #pragma unroll
;                             for (int e = 0; e < 8; ++e) ks[bj][e] += o[e]; }
;                         u32x4 w; w.x = cvt_pk_bf16(o[0] * sc, o[1] * sc); w.y = cvt_pk_bf16(o[2] * sc, o[3] * sc); w.z = cvt_pk_bf16(o[4] * sc, o[5] * sc); w.w = cvt_pk_bf16(o[6] * sc, o[7] * sc);
;                         *(u32x4*)(base + (unsigned)(row * 512 + bj * HALF) * 2u) = w;
.LBB0_1144:
	v_mul_f32_e32 v80, v167, v85
	v_mul_f32_e32 v82, v167, v90
	v_cvt_pk_bf16_f32 v90, v80, v82
	v_mul_f32_e32 v80, v167, v95
	v_mul_f32_e32 v82, v167, v92
	v_cvt_pk_bf16_f32 v91, v80, v82
	v_mul_f32_e32 v80, v167, v81
	v_mul_f32_e32 v81, v167, v86
	v_cvt_pk_bf16_f32 v92, v80, v81
	v_mul_f32_e32 v80, v167, v83
	v_mul_f32_e32 v81, v167, v96
	v_add_u32_e32 v96, 48, v191
	v_cvt_pk_bf16_f32 v93, v80, v81
	v_lshlrev_b32_e32 v80, 7, v96
	v_and_or_b32 v144, v80, s78, v182
	v_lshl_add_u64 v[80:81], s[54:55], 0, v[144:145]
	flat_load_dwordx4 v[80:83], v[80:81]
	v_lshl_add_u64 v[84:85], s[52:53], 0, v[144:145]
	flat_load_dwordx4 v[84:87], v[84:85]
	s_and_b64 vcc, exec, s[8:9]
	flat_store_dwordx4 v[88:89], v[90:93] offset:256 sc1
	s_waitcnt vmcnt(0) lgkmcnt(0)
	v_pk_mul_f32 v[88:89], v[76:77], v[80:81] op_sel_hi:[1,0]
	v_pk_mul_f32 v[92:93], v[78:79], v[80:81] op_sel:[0,1]
	v_pk_mul_f32 v[98:99], v[72:73], v[82:83] op_sel_hi:[1,0]
	v_mov_b32_e32 v100, v83
	v_mov_b32_e32 v102, v87
	v_pk_fma_f32 v[90:91], v[76:77], v[84:85], v[88:89] op_sel:[0,0,1] op_sel_hi:[1,0,0]
	v_pk_fma_f32 v[94:95], v[76:77], v[84:85], v[88:89] op_sel:[0,0,1] op_sel_hi:[1,0,0] neg_lo:[1,0,0] neg_hi:[1,0,0]
	v_pk_fma_f32 v[88:89], v[78:79], v[84:85], v[92:93] op_sel:[0,1,1] op_sel_hi:[1,1,0]
	v_pk_fma_f32 v[92:93], v[78:79], v[84:85], v[92:93] op_sel:[0,1,1] op_sel_hi:[1,1,0] neg_lo:[1,0,0] neg_hi:[1,0,0]
	v_pk_fma_f32 v[76:77], v[72:73], v[86:87], v[98:99] op_sel:[0,0,1] op_sel_hi:[1,0,0]
	v_pk_fma_f32 v[78:79], v[72:73], v[86:87], v[98:99] op_sel:[0,0,1] op_sel_hi:[1,0,0] neg_lo:[1,0,0] neg_hi:[1,0,0]
	v_pk_mul_f32 v[98:99], v[74:75], v[100:101] op_sel_hi:[1,0]
	s_nop 0
	v_pk_fma_f32 v[72:73], v[74:75], v[102:103], v[98:99] op_sel:[0,0,1] op_sel_hi:[1,0,0]
	v_pk_fma_f32 v[74:75], v[74:75], v[102:103], v[98:99] op_sel:[0,0,1] op_sel_hi:[1,0,0] neg_lo:[1,0,0] neg_hi:[1,0,0]
	s_cbranch_vccnz .LBB0_1146
	v_mov_b32_e32 v73, v75
	v_mov_b32_e32 v77, v79
	v_mov_b32_e32 v89, v93
	v_mov_b32_e32 v91, v95
	v_pk_add_f32 v[156:157], v[156:157], v[90:91]
	v_pk_add_f32 v[154:155], v[154:155], v[88:89]
	v_pk_add_f32 v[122:123], v[122:123], v[76:77]
	v_pk_add_f32 v[120:121], v[120:121], v[72:73]

; __device__ __forceinline__ unsigned cvt_pk_bf16(float lo, float hi) { unsigned r; asm volatile("v_cvt_pk_bf16_f32 %0, %1, %2" : "=v"(r) : "v"(lo), "v"(hi)); return r; }
;     __device__ __forceinline__ void operator()(const f32x4 (&acc)[2][2][4][2], const Unit& u, int wr, int wc, int fr, int fq) const {
;     ...
;                 for (int m = 0; m < 4; ++m) {
;                     const int row = row0 + ai * HALF + m * 16, pos = row & 4095;
;                     const unsigned ro = (unsigned)(pos * 32 + i0) * 4u; const f32x4 c4 = *(const f32x4*)(cs + ro), s4 = *(const f32x4*)(sn + ro);
; #pragma unroll
;                     for (int bj = 0; bj < 2; ++bj) {
;                         const f32x4 v0 = acc[ai][bj][m][0], v1 = acc[ai][bj][m][1];
;                         float o[8];
;                         o[0] = v0[0] * c4[0] - v0[1] * s4[0]; o[1] = v0[1] * c4[0] + v0[0] * s4[0];
;                         o[2] = v0[2] * c4[1] - v0[3] * s4[1]; o[3] = v0[3] * c4[1] + v0[2] * s4[1];
;                         o[4] = v1[0] * c4[2] - v1[1] * s4[2]; o[5] = v1[1] * c4[2] + v1[0] * s4[2];
;                         o[6] = v1[2] * c4[3] - v1[3] * s4[3]; o[7] = v1[3] * c4[3] + v1[2] * s4[3];
;                         if (!isq) {
; #pragma unroll
;                             for (int e = 0; e < 8; ++e) ks[bj][e] += o[e]; }
;                         u32x4 w; w.x = cvt_pk_bf16(o[0] * sc, o[1] * sc); w.y = cvt_pk_bf16(o[2] * sc, o[3] * sc); w.z = cvt_pk_bf16(o[4] * sc, o[5] * sc); w.w = cvt_pk_bf16(o[6] * sc, o[7] * sc);
;                         *(u32x4*)(base + (unsigned)(row * 512 + bj * HALF) * 2u) = w;
.LBB0_1148:
	v_mul_f32_e32 v64, v167, v69
	v_mul_f32_e32 v66, v167, v74
	v_cvt_pk_bf16_f32 v74, v64, v66
	v_mul_f32_e32 v64, v167, v79
	v_mul_f32_e32 v66, v167, v76
	v_cvt_pk_bf16_f32 v75, v64, v66
	v_mul_f32_e32 v64, v167, v65
	v_mul_f32_e32 v65, v167, v70
	v_cvt_pk_bf16_f32 v76, v64, v65
	v_mul_f32_e32 v64, v167, v67
	v_mul_f32_e32 v65, v167, v80
	v_add_u32_e32 v80, 0x80, v191
	v_cvt_pk_bf16_f32 v77, v64, v65
	v_lshlrev_b32_e32 v64, 7, v80
	v_and_or_b32 v144, v64, s78, v182
	v_lshl_add_u64 v[64:65], s[54:55], 0, v[144:145]
	flat_load_dwordx4 v[64:67], v[64:65]
	v_lshl_add_u64 v[68:69], s[52:53], 0, v[144:145]
	flat_load_dwordx4 v[68:71], v[68:69]
	s_and_b64 vcc, exec, s[8:9]
	flat_store_dwordx4 v[72:73], v[74:77] offset:256 sc1
	s_waitcnt vmcnt(0) lgkmcnt(0)
	v_pk_mul_f32 v[72:73], v[60:61], v[64:65] op_sel_hi:[1,0]
	v_pk_mul_f32 v[76:77], v[62:63], v[64:65] op_sel:[0,1]
	v_pk_mul_f32 v[82:83], v[56:57], v[66:67] op_sel_hi:[1,0]
	v_mov_b32_e32 v84, v67
	v_mov_b32_e32 v86, v71
	v_pk_fma_f32 v[74:75], v[60:61], v[68:69], v[72:73] op_sel:[0,0,1] op_sel_hi:[1,0,0]
	v_pk_fma_f32 v[78:79], v[60:61], v[68:69], v[72:73] op_sel:[0,0,1] op_sel_hi:[1,0,0] neg_lo:[1,0,0] neg_hi:[1,0,0]
	v_pk_fma_f32 v[72:73], v[62:63], v[68:69], v[76:77] op_sel:[0,1,1] op_sel_hi:[1,1,0]
	v_pk_fma_f32 v[76:77], v[62:63], v[68:69], v[76:77] op_sel:[0,1,1] op_sel_hi:[1,1,0] neg_lo:[1,0,0] neg_hi:[1,0,0]
	v_pk_fma_f32 v[60:61], v[56:57], v[70:71], v[82:83] op_sel:[0,0,1] op_sel_hi:[1,0,0]
	v_pk_fma_f32 v[62:63], v[56:57], v[70:71], v[82:83] op_sel:[0,0,1] op_sel_hi:[1,0,0] neg_lo:[1,0,0] neg_hi:[1,0,0]
	v_pk_mul_f32 v[82:83], v[58:59], v[84:85] op_sel_hi:[1,0]
	s_nop 0
	v_pk_fma_f32 v[56:57], v[58:59], v[86:87], v[82:83] op_sel:[0,0,1] op_sel_hi:[1,0,0]
	v_pk_fma_f32 v[58:59], v[58:59], v[86:87], v[82:83] op_sel:[0,0,1] op_sel_hi:[1,0,0] neg_lo:[1,0,0] neg_hi:[1,0,0]
	s_cbranch_vccnz .LBB0_1150
	v_mov_b32_e32 v57, v59
	v_mov_b32_e32 v61, v63
	v_mov_b32_e32 v73, v77
	v_mov_b32_e32 v75, v79
	v_pk_add_f32 v[156:157], v[156:157], v[74:75]
	v_pk_add_f32 v[154:155], v[154:155], v[72:73]
	v_pk_add_f32 v[122:123], v[122:123], v[60:61]
	v_pk_add_f32 v[120:121], v[120:121], v[56:57]

; __device__ __forceinline__ unsigned cvt_pk_bf16(float lo, float hi) { unsigned r; asm volatile("v_cvt_pk_bf16_f32 %0, %1, %2" : "=v"(r) : "v"(lo), "v"(hi)); return r; }
;     __device__ __forceinline__ void operator()(const f32x4 (&acc)[2][2][4][2], const Unit& u, int wr, int wc, int fr, int fq) const {
;     ...
;                 for (int m = 0; m < 4; ++m) {
;                     const int row = row0 + ai * HALF + m * 16, pos = row & 4095;
;                     const unsigned ro = (unsigned)(pos * 32 + i0) * 4u; const f32x4 c4 = *(const f32x4*)(cs + ro), s4 = *(const f32x4*)(sn + ro);
; #pragma unroll
;                     for (int bj = 0; bj < 2; ++bj) {
;                         const f32x4 v0 = acc[ai][bj][m][0], v1 = acc[ai][bj][m][1];
;                         float o[8];
;                         o[0] = v0[0] * c4[0] - v0[1] * s4[0]; o[1] = v0[1] * c4[0] + v0[0] * s4[0];
;                         o[2] = v0[2] * c4[1] - v0[3] * s4[1]; o[3] = v0[3] * c4[1] + v0[2] * s4[1];
;                         o[4] = v1[0] * c4[2] - v1[1] * s4[2]; o[5] = v1[1] * c4[2] + v1[0] * s4[2];
;                         o[6] = v1[2] * c4[3] - v1[3] * s4[3]; o[7] = v1[3] * c4[3] + v1[2] * s4[3];
;                         if (!isq) {
; #pragma unroll
;                             for (int e = 0; e < 8; ++e) ks[bj][e] += o[e]; }
;                         u32x4 w; w.x = cvt_pk_bf16(o[0] * sc, o[1] * sc); w.y = cvt_pk_bf16(o[2] * sc, o[3] * sc); w.z = cvt_pk_bf16(o[4] * sc, o[5] * sc); w.w = cvt_pk_bf16(o[6] * sc, o[7] * sc);
;                         *(u32x4*)(base + (unsigned)(row * 512 + bj * HALF) * 2u) = w;
.LBB0_1152:
	v_mul_f32_e32 v48, v167, v53
	v_mul_f32_e32 v50, v167, v58
	v_cvt_pk_bf16_f32 v58, v48, v50
	v_mul_f32_e32 v48, v167, v63
	v_mul_f32_e32 v50, v167, v60
	v_cvt_pk_bf16_f32 v59, v48, v50
	v_mul_f32_e32 v48, v167, v49
	v_mul_f32_e32 v49, v167, v54
	v_cvt_pk_bf16_f32 v60, v48, v49
	v_mul_f32_e32 v48, v167, v51
	v_mul_f32_e32 v49, v167, v64
	v_add_u32_e32 v64, 0x90, v191
	v_cvt_pk_bf16_f32 v61, v48, v49
	v_lshlrev_b32_e32 v48, 7, v64
	v_and_or_b32 v144, v48, s78, v182
	v_lshl_add_u64 v[48:49], s[54:55], 0, v[144:145]
	flat_load_dwordx4 v[48:51], v[48:49]
	v_lshl_add_u64 v[52:53], s[52:53], 0, v[144:145]
	flat_load_dwordx4 v[52:55], v[52:53]
	s_and_b64 vcc, exec, s[8:9]
	flat_store_dwordx4 v[56:57], v[58:61] offset:256 sc1
	s_waitcnt vmcnt(0) lgkmcnt(0)
	v_pk_mul_f32 v[56:57], v[44:45], v[48:49] op_sel_hi:[1,0]
	v_pk_mul_f32 v[60:61], v[46:47], v[48:49] op_sel:[0,1]
	v_pk_mul_f32 v[66:67], v[40:41], v[50:51] op_sel_hi:[1,0]
	v_mov_b32_e32 v68, v51
	v_mov_b32_e32 v70, v55
	v_pk_fma_f32 v[58:59], v[44:45], v[52:53], v[56:57] op_sel:[0,0,1] op_sel_hi:[1,0,0]
	v_pk_fma_f32 v[62:63], v[44:45], v[52:53], v[56:57] op_sel:[0,0,1] op_sel_hi:[1,0,0] neg_lo:[1,0,0] neg_hi:[1,0,0]
	v_pk_fma_f32 v[56:57], v[46:47], v[52:53], v[60:61] op_sel:[0,1,1] op_sel_hi:[1,1,0]
	v_pk_fma_f32 v[60:61], v[46:47], v[52:53], v[60:61] op_sel:[0,1,1] op_sel_hi:[1,1,0] neg_lo:[1,0,0] neg_hi:[1,0,0]
	v_pk_fma_f32 v[44:45], v[40:41], v[54:55], v[66:67] op_sel:[0,0,1] op_sel_hi:[1,0,0]
	v_pk_fma_f32 v[46:47], v[40:41], v[54:55], v[66:67] op_sel:[0,0,1] op_sel_hi:[1,0,0] neg_lo:[1,0,0] neg_hi:[1,0,0]
	v_pk_mul_f32 v[66:67], v[42:43], v[68:69] op_sel_hi:[1,0]
	s_nop 0
	v_pk_fma_f32 v[40:41], v[42:43], v[70:71], v[66:67] op_sel:[0,0,1] op_sel_hi:[1,0,0]
	v_pk_fma_f32 v[42:43], v[42:43], v[70:71], v[66:67] op_sel:[0,0,1] op_sel_hi:[1,0,0] neg_lo:[1,0,0] neg_hi:[1,0,0]
	s_cbranch_vccnz .LBB0_1154
	v_mov_b32_e32 v41, v43
	v_mov_b32_e32 v45, v47
	v_mov_b32_e32 v57, v61
	v_mov_b32_e32 v59, v63
	v_pk_add_f32 v[156:157], v[156:157], v[58:59]
	v_pk_add_f32 v[154:155], v[154:155], v[56:57]
	v_pk_add_f32 v[122:123], v[122:123], v[44:45]
	v_pk_add_f32 v[120:121], v[120:121], v[40:41]

; __device__ __forceinline__ unsigned cvt_pk_bf16(float lo, float hi) { unsigned r; asm volatile("v_cvt_pk_bf16_f32 %0, %1, %2" : "=v"(r) : "v"(lo), "v"(hi)); return r; }
;     __device__ __forceinline__ void operator()(const f32x4 (&acc)[2][2][4][2], const Unit& u, int wr, int wc, int fr, int fq) const {
;     ...
;                 for (int m = 0; m < 4; ++m) {
;                     const int row = row0 + ai * HALF + m * 16, pos = row & 4095;
;                     const unsigned ro = (unsigned)(pos * 32 + i0) * 4u; const f32x4 c4 = *(const f32x4*)(cs + ro), s4 = *(const f32x4*)(sn + ro);
; #pragma unroll
;                     for (int bj = 0; bj < 2; ++bj) {
;                         const f32x4 v0 = acc[ai][bj][m][0], v1 = acc[ai][bj][m][1];
;                         float o[8];
;                         o[0] = v0[0] * c4[0] - v0[1] * s4[0]; o[1] = v0[1] * c4[0] + v0[0] * s4[0];
;                         o[2] = v0[2] * c4[1] - v0[3] * s4[1]; o[3] = v0[3] * c4[1] + v0[2] * s4[1];
;                         o[4] = v1[0] * c4[2] - v1[1] * s4[2]; o[5] = v1[1] * c4[2] + v1[0] * s4[2];
;                         o[6] = v1[2] * c4[3] - v1[3] * s4[3]; o[7] = v1[3] * c4[3] + v1[2] * s4[3];
;                         if (!isq) {
; #pragma unroll
;                             for (int e = 0; e < 8; ++e) ks[bj][e] += o[e]; }
;                         u32x4 w; w.x = cvt_pk_bf16(o[0] * sc, o[1] * sc); w.y = cvt_pk_bf16(o[2] * sc, o[3] * sc); w.z = cvt_pk_bf16(o[4] * sc, o[5] * sc); w.w = cvt_pk_bf16(o[6] * sc, o[7] * sc);
;                         *(u32x4*)(base + (unsigned)(row * 512 + bj * HALF) * 2u) = w;
.LBB0_1156:
	v_mul_f32_e32 v32, v167, v37
	v_mul_f32_e32 v34, v167, v42
	v_cvt_pk_bf16_f32 v42, v32, v34
	v_mul_f32_e32 v32, v167, v47
	v_mul_f32_e32 v34, v167, v44
	v_cvt_pk_bf16_f32 v43, v32, v34
	v_mul_f32_e32 v32, v167, v33
	v_mul_f32_e32 v33, v167, v38
	v_cvt_pk_bf16_f32 v44, v32, v33
	v_mul_f32_e32 v32, v167, v35
	v_mul_f32_e32 v33, v167, v48
	v_add_u32_e32 v48, 0xa0, v191
	v_cvt_pk_bf16_f32 v45, v32, v33
	v_lshlrev_b32_e32 v32, 7, v48
	v_and_or_b32 v144, v32, s78, v182
	v_lshl_add_u64 v[32:33], s[54:55], 0, v[144:145]
	flat_load_dwordx4 v[32:35], v[32:33]
	v_lshl_add_u64 v[36:37], s[52:53], 0, v[144:145]
	flat_load_dwordx4 v[36:39], v[36:37]
	s_and_b64 vcc, exec, s[8:9]
	flat_store_dwordx4 v[40:41], v[42:45] offset:256 sc1
	s_waitcnt vmcnt(0) lgkmcnt(0)
	v_pk_mul_f32 v[40:41], v[28:29], v[32:33] op_sel_hi:[1,0]
	v_pk_mul_f32 v[44:45], v[30:31], v[32:33] op_sel:[0,1]
	v_pk_mul_f32 v[50:51], v[24:25], v[34:35] op_sel_hi:[1,0]
	v_mov_b32_e32 v52, v35
	v_mov_b32_e32 v54, v39
	v_pk_fma_f32 v[42:43], v[28:29], v[36:37], v[40:41] op_sel:[0,0,1] op_sel_hi:[1,0,0]
	v_pk_fma_f32 v[46:47], v[28:29], v[36:37], v[40:41] op_sel:[0,0,1] op_sel_hi:[1,0,0] neg_lo:[1,0,0] neg_hi:[1,0,0]
	v_pk_fma_f32 v[40:41], v[30:31], v[36:37], v[44:45] op_sel:[0,1,1] op_sel_hi:[1,1,0]
	v_pk_fma_f32 v[44:45], v[30:31], v[36:37], v[44:45] op_sel:[0,1,1] op_sel_hi:[1,1,0] neg_lo:[1,0,0] neg_hi:[1,0,0]
	v_pk_fma_f32 v[28:29], v[24:25], v[38:39], v[50:51] op_sel:[0,0,1] op_sel_hi:[1,0,0]
	v_pk_fma_f32 v[30:31], v[24:25], v[38:39], v[50:51] op_sel:[0,0,1] op_sel_hi:[1,0,0] neg_lo:[1,0,0] neg_hi:[1,0,0]
	v_pk_mul_f32 v[50:51], v[26:27], v[52:53] op_sel_hi:[1,0]
	s_nop 0
	v_pk_fma_f32 v[24:25], v[26:27], v[54:55], v[50:51] op_sel:[0,0,1] op_sel_hi:[1,0,0]
	v_pk_fma_f32 v[26:27], v[26:27], v[54:55], v[50:51] op_sel:[0,0,1] op_sel_hi:[1,0,0] neg_lo:[1,0,0] neg_hi:[1,0,0]
	s_cbranch_vccnz .LBB0_1158
	v_mov_b32_e32 v25, v27
	v_mov_b32_e32 v29, v31
	v_mov_b32_e32 v41, v45
	v_mov_b32_e32 v43, v47
	v_pk_add_f32 v[156:157], v[156:157], v[42:43]
	v_pk_add_f32 v[154:155], v[154:155], v[40:41]
	v_pk_add_f32 v[122:123], v[122:123], v[28:29]
	v_pk_add_f32 v[120:121], v[120:121], v[24:25]

; __device__ __forceinline__ unsigned cvt_pk_bf16(float lo, float hi) { unsigned r; asm volatile("v_cvt_pk_bf16_f32 %0, %1, %2" : "=v"(r) : "v"(lo), "v"(hi)); return r; }
;     __device__ __forceinline__ void operator()(const f32x4 (&acc)[2][2][4][2], const Unit& u, int wr, int wc, int fr, int fq) const {
;     ...
;                 for (int m = 0; m < 4; ++m) {
;                     const int row = row0 + ai * HALF + m * 16, pos = row & 4095;
;                     const unsigned ro = (unsigned)(pos * 32 + i0) * 4u; const f32x4 c4 = *(const f32x4*)(cs + ro), s4 = *(const f32x4*)(sn + ro);
; #pragma unroll
;                     for (int bj = 0; bj < 2; ++bj) {
;                         const f32x4 v0 = acc[ai][bj][m][0], v1 = acc[ai][bj][m][1];
;                         float o[8];
;                         o[0] = v0[0] * c4[0] - v0[1] * s4[0]; o[1] = v0[1] * c4[0] + v0[0] * s4[0];
;                         o[2] = v0[2] * c4[1] - v0[3] * s4[1]; o[3] = v0[3] * c4[1] + v0[2] * s4[1];
;                         o[4] = v1[0] * c4[2] - v1[1] * s4[2]; o[5] = v1[1] * c4[2] + v1[0] * s4[2];
;                         o[6] = v1[2] * c4[3] - v1[3] * s4[3]; o[7] = v1[3] * c4[3] + v1[2] * s4[3];
;                         if (!isq) {
; #pragma unroll
;                             for (int e = 0; e < 8; ++e) ks[bj][e] += o[e]; }
;                         u32x4 w; w.x = cvt_pk_bf16(o[0] * sc, o[1] * sc); w.y = cvt_pk_bf16(o[2] * sc, o[3] * sc); w.z = cvt_pk_bf16(o[4] * sc, o[5] * sc); w.w = cvt_pk_bf16(o[6] * sc, o[7] * sc);
;                         *(u32x4*)(base + (unsigned)(row * 512 + bj * HALF) * 2u) = w;
.LBB0_1160:
	v_mul_f32_e32 v16, v167, v21
	v_mul_f32_e32 v18, v167, v26
	v_cvt_pk_bf16_f32 v26, v16, v18
	v_mul_f32_e32 v16, v167, v31
	v_mul_f32_e32 v18, v167, v28
	v_cvt_pk_bf16_f32 v27, v16, v18
	v_mul_f32_e32 v16, v167, v17
	v_mul_f32_e32 v17, v167, v22
	v_cvt_pk_bf16_f32 v28, v16, v17
	v_mul_f32_e32 v16, v167, v19
	v_mul_f32_e32 v17, v167, v32
	v_add_u32_e32 v32, 0xb0, v191
	v_cvt_pk_bf16_f32 v29, v16, v17
	v_lshlrev_b32_e32 v16, 7, v32
	v_and_or_b32 v144, v16, s78, v182
	v_lshl_add_u64 v[16:17], s[54:55], 0, v[144:145]
	flat_load_dwordx4 v[16:19], v[16:17]
	v_lshl_add_u64 v[20:21], s[52:53], 0, v[144:145]
	flat_load_dwordx4 v[20:23], v[20:21]
	s_and_b64 vcc, exec, s[8:9]
	flat_store_dwordx4 v[24:25], v[26:29] offset:256 sc1
	s_waitcnt vmcnt(0) lgkmcnt(0)
	v_pk_mul_f32 v[24:25], v[12:13], v[16:17] op_sel_hi:[1,0]
	v_pk_mul_f32 v[28:29], v[14:15], v[16:17] op_sel:[0,1]
	v_pk_mul_f32 v[34:35], v[8:9], v[18:19] op_sel_hi:[1,0]
	v_mov_b32_e32 v36, v19
	v_mov_b32_e32 v38, v23
	v_pk_fma_f32 v[26:27], v[12:13], v[20:21], v[24:25] op_sel:[0,0,1] op_sel_hi:[1,0,0]
	v_pk_fma_f32 v[30:31], v[12:13], v[20:21], v[24:25] op_sel:[0,0,1] op_sel_hi:[1,0,0] neg_lo:[1,0,0] neg_hi:[1,0,0]
	v_pk_fma_f32 v[24:25], v[14:15], v[20:21], v[28:29] op_sel:[0,1,1] op_sel_hi:[1,1,0]
	v_pk_fma_f32 v[28:29], v[14:15], v[20:21], v[28:29] op_sel:[0,1,1] op_sel_hi:[1,1,0] neg_lo:[1,0,0] neg_hi:[1,0,0]
	v_pk_fma_f32 v[12:13], v[8:9], v[22:23], v[34:35] op_sel:[0,0,1] op_sel_hi:[1,0,0]
	v_pk_fma_f32 v[14:15], v[8:9], v[22:23], v[34:35] op_sel:[0,0,1] op_sel_hi:[1,0,0] neg_lo:[1,0,0] neg_hi:[1,0,0]
	v_pk_mul_f32 v[34:35], v[10:11], v[36:37] op_sel_hi:[1,0]
	s_nop 0
	v_pk_fma_f32 v[8:9], v[10:11], v[38:39], v[34:35] op_sel:[0,0,1] op_sel_hi:[1,0,0]
	v_pk_fma_f32 v[10:11], v[10:11], v[38:39], v[34:35] op_sel:[0,0,1] op_sel_hi:[1,0,0] neg_lo:[1,0,0] neg_hi:[1,0,0]
	s_cbranch_vccnz .LBB0_1162
	v_mov_b32_e32 v9, v11
	v_mov_b32_e32 v13, v15
	v_mov_b32_e32 v25, v29
	v_mov_b32_e32 v27, v31
	v_pk_add_f32 v[156:157], v[156:157], v[26:27]
	v_pk_add_f32 v[154:155], v[154:155], v[24:25]
	v_pk_add_f32 v[122:123], v[122:123], v[12:13]
	v_pk_add_f32 v[120:121], v[120:121], v[8:9]

;     __device__ __forceinline__ void operator()(const f32x4 (&acc)[2][2][4][2], const Unit& u, int wr, int wc, int fr, int fq) const {
;     ...
;                         *(u32x4*)(base + (unsigned)(row * 512 + bj * HALF) * 2u) = w;
;                     }
;                 }
;             if (!isq) {
; #pragma unroll
;                 for (int bj = 0; bj < 2; ++bj)
; #pragma unroll
;                     for (int e = 0; e < 8; ++e) { float s = ks[bj][e]; s += __shfl_xor(s, 1); s += __shfl_xor(s, 2); s += __shfl_xor(s, 4); s += __shfl_xor(s, 8); ks[bj][e] = s; }
;                 if (fr == 0 && do_km) {
;                     const int b = u.pm >> 4, nb = u.pm & 15;
; #pragma unroll
;                     for (int bj = 0; bj < 2; ++bj) { const int h = (pn & 1) * 4 + 2 * bj + (wc >> 1); float* kp = (float*)(wb + OFF_KMEAN + (unsigned)(layer * 32768 + ((b * 8 + h) * 16 + nb) * 64 + 32 * (wc & 1) + 8 * fq) * 4u);
; #pragma unroll
;                         for (int e = 0; e < 8; ++e) unsafeAtomicAdd(kp + e, ks[bj][e] * (1.0f / 256.0f)); }
;                 }
.LBB0_1164:
	v_mul_f32_e32 v0, v167, v5
	v_mul_f32_e32 v2, v167, v10
	v_cvt_pk_bf16_f32 v4, v0, v2
	v_mul_f32_e32 v0, v167, v15
	v_mul_f32_e32 v2, v167, v12
	v_cvt_pk_bf16_f32 v5, v0, v2
	v_mul_f32_e32 v0, v167, v1
	v_mul_f32_e32 v1, v167, v6
	s_and_b64 vcc, exec, s[50:51]
	v_cvt_pk_bf16_f32 v6, v0, v1
	v_mul_f32_e32 v0, v167, v3
	v_mul_f32_e32 v1, v167, v16
	v_cvt_pk_bf16_f32 v7, v0, v1
	flat_store_dwordx4 v[8:9], v[4:7] offset:256 sc1
	s_cbranch_vccz .LBB0_1168
	ds_bpermute_b32 v1, v173, v156
	ds_bpermute_b32 v2, v173, v155
	ds_bpermute_b32 v5, v173, v154
	ds_bpermute_b32 v8, v173, v123
	ds_bpermute_b32 v11, v173, v122
	s_waitcnt lgkmcnt(0)
	v_add_f32_e32 v1, v156, v1
	ds_bpermute_b32 v4, v174, v1
	v_add_f32_e32 v6, v155, v2
	v_add_f32_e32 v8, v123, v8
	ds_bpermute_b32 v10, v174, v8
	ds_bpermute_b32 v18, v173, v130
	s_waitcnt lgkmcnt(0)
	v_add_f32_e32 v1, v1, v4
	v_add_f32_e32 v4, v154, v5
	ds_bpermute_b32 v5, v174, v6
	ds_bpermute_b32 v7, v174, v4
	v_add_f32_e32 v8, v8, v10
	v_add_f32_e32 v11, v122, v11
	ds_bpermute_b32 v10, v175, v8
	s_waitcnt lgkmcnt(0)
	v_add_f32_e32 v5, v6, v5
	v_add_f32_e32 v7, v4, v7
	ds_bpermute_b32 v6, v175, v5
	ds_bpermute_b32 v9, v175, v7
	ds_bpermute_b32 v12, v174, v11
	v_add_f32_e32 v18, v130, v18
	ds_bpermute_b32 v20, v174, v18
	s_waitcnt lgkmcnt(0)
	v_add_f32_e32 v4, v5, v6
	v_add_f32_e32 v6, v7, v9
	ds_bpermute_b32 v9, v173, v121
	ds_bpermute_b32 v21, v173, v129
	v_add_f32_e32 v8, v8, v10
	v_add_f32_e32 v10, v11, v12
	ds_bpermute_b32 v15, v173, v131
	s_waitcnt lgkmcnt(0)
	v_add_f32_e32 v13, v121, v9
	ds_bpermute_b32 v14, v174, v13
	v_add_f32_e32 v18, v18, v20
	v_add_f32_e32 v20, v129, v21
	v_add_f32_e32 v15, v131, v15
	ds_bpermute_b32 v21, v174, v20
	s_waitcnt lgkmcnt(0)
	v_add_f32_e32 v12, v13, v14
	ds_bpermute_b32 v14, v173, v120
	ds_bpermute_b32 v22, v173, v128
	ds_bpermute_b32 v17, v174, v15
	v_add_f32_e32 v20, v20, v21
	ds_bpermute_b32 v0, v173, v157
	s_waitcnt lgkmcnt(0)
	v_add_f32_e32 v14, v120, v14
	ds_bpermute_b32 v16, v174, v14
	v_add_f32_e32 v21, v128, v22
	v_add_f32_e32 v17, v15, v17
	ds_bpermute_b32 v22, v174, v21
	ds_bpermute_b32 v19, v175, v17
	s_waitcnt lgkmcnt(0)
	v_add_f32_e32 v14, v14, v16
	ds_bpermute_b32 v16, v175, v14
	ds_bpermute_b32 v27, v173, v125
	v_add_f32_e32 v22, v21, v22
	ds_bpermute_b32 v26, v175, v22
	ds_bpermute_b32 v28, v173, v124
	s_waitcnt lgkmcnt(0)
	v_add_f32_e32 v14, v14, v16
	v_add_f32_e32 v16, v17, v19
	ds_bpermute_b32 v19, v175, v18
	v_add_f32_e32 v22, v22, v26
	ds_bpermute_b32 v26, v173, v126
	v_add_f32_e32 v0, v157, v0
	v_add_f32_e32 v27, v125, v27
	s_waitcnt lgkmcnt(0)
	v_add_f32_e32 v18, v18, v19
	ds_bpermute_b32 v19, v173, v127
	v_add_f32_e32 v26, v126, v26
	v_add_f32_e32 v28, v124, v28
	ds_bpermute_b32 v3, v174, v0
	ds_bpermute_b32 v29, v174, v26
	s_waitcnt lgkmcnt(0)
	v_add_f32_e32 v24, v127, v19
	ds_bpermute_b32 v25, v174, v24
	ds_bpermute_b32 v30, v174, v27
	ds_bpermute_b32 v31, v174, v28
	v_add_f32_e32 v0, v0, v3
	v_add_f32_e32 v26, v26, v29
	s_waitcnt lgkmcnt(0)
	v_add_f32_e32 v24, v24, v25
	v_add_f32_e32 v30, v27, v30
	v_add_f32_e32 v31, v28, v31
	ds_bpermute_b32 v2, v175, v0
	ds_bpermute_b32 v3, v175, v1
	ds_bpermute_b32 v11, v175, v10
	ds_bpermute_b32 v13, v175, v12
	ds_bpermute_b32 v23, v175, v20
	ds_bpermute_b32 v25, v175, v24
	ds_bpermute_b32 v29, v175, v26
	ds_bpermute_b32 v32, v175, v30
	ds_bpermute_b32 v33, v175, v31
	s_waitcnt lgkmcnt(0)
	v_add_f32_e32 v0, v0, v2
	v_add_f32_e32 v2, v1, v3
	v_add_f32_e32 v10, v10, v11
	v_add_f32_e32 v12, v12, v13
	v_add_f32_e32 v20, v20, v23
	v_add_f32_e32 v24, v24, v25
	v_add_f32_e32 v26, v26, v29
	v_add_f32_e32 v28, v30, v32
	v_add_f32_e32 v30, v31, v33
	ds_bpermute_b32 v1, v176, v0
	ds_bpermute_b32 v3, v176, v2
	ds_bpermute_b32 v5, v176, v4
	ds_bpermute_b32 v7, v176, v6
	ds_bpermute_b32 v9, v176, v8
	ds_bpermute_b32 v11, v176, v10
	ds_bpermute_b32 v13, v176, v12
	ds_bpermute_b32 v15, v176, v14
	ds_bpermute_b32 v17, v176, v16
	ds_bpermute_b32 v19, v176, v18
	ds_bpermute_b32 v21, v176, v20
	ds_bpermute_b32 v23, v176, v22
	ds_bpermute_b32 v25, v176, v24
	ds_bpermute_b32 v27, v176, v26
	ds_bpermute_b32 v29, v176, v28
	ds_bpermute_b32 v31, v176, v30
	s_and_saveexec_b64 s[8:9], s[4:5]
	s_cbranch_execz .LBB0_1167
	s_lshl_b32 s27, s27, 2
	s_or_b32 s27, s27, s73
	s_add_u32 s34, s46, 0x80000
	s_addc_u32 s35, s47, 0
	s_lshr_b32 s29, s14, 1
	s_and_b32 s29, s29, 0x3ffff8
	s_lshl_b32 s14, s14, 6
	s_or_b32 s27, s27, s29
	s_and_b32 s14, s14, 0x3c0
	s_or_b32 s14, s14, s74
	s_lshl_b32 s27, s27, 10
	s_or_b32 s29, s14, s27
	s_waitcnt lgkmcnt(0)
	v_add_f32_e32 v2, v2, v3
	v_add_f32_e32 v3, v0, v1
	v_or_b32_e32 v0, s29, v179
	v_lshl_add_u32 v144, v0, 2, v189
	v_lshl_add_u64 v[0:1], s[34:35], 0, v[144:145]
	v_mul_f32_e32 v3, 0x3b800000, v3
	v_add_f32_e32 v4, v4, v5
	flat_atomic_add_f32 v[0:1], v3
	v_mul_f32_e32 v2, 0x3b800000, v2
	v_add_f32_e32 v6, v6, v7
	flat_atomic_add_f32 v[0:1], v2 offset:4
	v_mul_f32_e32 v2, 0x3b800000, v4
	v_add_f32_e32 v8, v8, v9
	flat_atomic_add_f32 v[0:1], v2 offset:8
	v_mul_f32_e32 v2, 0x3b800000, v6
	v_add_f32_e32 v10, v10, v11
	flat_atomic_add_f32 v[0:1], v2 offset:12
	v_mul_f32_e32 v2, 0x3b800000, v8
	v_add_f32_e32 v12, v12, v13
	flat_atomic_add_f32 v[0:1], v2 offset:16
	v_mul_f32_e32 v2, 0x3b800000, v10
	v_add_f32_e32 v14, v14, v15
	flat_atomic_add_f32 v[0:1], v2 offset:20
	v_mul_f32_e32 v2, 0x3b800000, v12
	flat_atomic_add_f32 v[0:1], v2 offset:24
	v_mul_f32_e32 v2, 0x3b800000, v14
	flat_atomic_add_f32 v[0:1], v2 offset:28
	v_or_b32_e32 v0, s14, v179
	v_or_b32_e32 v0, s27, v0
	v_add_f32_e32 v16, v16, v17
	v_lshl_add_u32 v144, v0, 2, v190
	v_add_f32_e32 v18, v18, v19
	v_lshl_add_u64 v[0:1], s[34:35], 0, v[144:145]
	v_mul_f32_e32 v2, 0x3b800000, v16
	v_add_f32_e32 v20, v20, v21
	flat_atomic_add_f32 v[0:1], v2
	v_mul_f32_e32 v2, 0x3b800000, v18
	v_add_f32_e32 v22, v22, v23
	flat_atomic_add_f32 v[0:1], v2 offset:4
	v_mul_f32_e32 v2, 0x3b800000, v20
	v_add_f32_e32 v24, v24, v25
	flat_atomic_add_f32 v[0:1], v2 offset:8
	v_mul_f32_e32 v2, 0x3b800000, v22
	v_add_f32_e32 v26, v26, v27
	flat_atomic_add_f32 v[0:1], v2 offset:12
	v_mul_f32_e32 v2, 0x3b800000, v24
	v_add_f32_e32 v28, v28, v29
	flat_atomic_add_f32 v[0:1], v2 offset:16
	v_mul_f32_e32 v2, 0x3b800000, v26
	v_add_f32_e32 v30, v30, v31
	flat_atomic_add_f32 v[0:1], v2 offset:20
	v_mul_f32_e32 v2, 0x3b800000, v28
	flat_atomic_add_f32 v[0:1], v2 offset:24
	v_mul_f32_e32 v2, 0x3b800000, v30
	flat_atomic_add_f32 v[0:1], v2 offset:28

; #define GAS __attribute__((address_space(1)))
; #define LAS __attribute__((address_space(3)))
; __device__ __forceinline__ void p0_vslice_item(LAS unsigned char* lds, int wave, int tid, const float* vt_l, unsigned char* VS_l, float* vsc_l, int item) {
;     ...
; #pragma unroll 1
;     for (int p = tid; p < 4096; p += 512) { const int cs = p >> 5, k = p & 31;
;         const mk_u32x2 a = *(const LAS mk_u32x2*)(lds + (2 * k) * 1032 + cs * 8), b = *(const LAS mk_u32x2*)(lds + (2 * k + 1) * 1032 + cs * 8);
;         *(GAS v4u*)(VS_l + ((size_t)cs * 16384 + e0 + 2 * k) * 8) = (v4u){a.x, a.y, b.x, b.y}; }
.LBB0_1186:
	v_ashrrev_i32_e32 v16, 5, v5
	v_and_b32_e32 v9, 62, v4
	v_add_u32_e32 v12, 0x200, v5
	v_mul_u32_u24_e32 v13, 0x408, v9
	v_lshlrev_b32_e32 v14, 3, v16
	v_cmp_lt_i32_e32 vcc, s26, v5
	v_mov_b32_e32 v5, v12
	v_add3_u32 v12, 0, v13, v14
	v_ashrrev_i32_e32 v17, 31, v16
	ds_read2_b64 v[12:15], v12 offset1:129
	v_lshlrev_b64 v[16:17], 14, v[16:17]
	v_or_b32_e32 v16, s8, v16
	v_or_b32_e32 v16, v16, v9
	v_add_u32_e32 v4, 0x400, v4
	s_or_b64 s[18:19], vcc, s[18:19]
	v_lshl_add_u64 v[16:17], v[16:17], 3, s[16:17]
	s_waitcnt lgkmcnt(0)
	global_store_dwordx4 v[16:17], v[12:15], off sc1
	s_andn2_b64 exec, exec, s[18:19]
	s_cbranch_execnz .LBB0_1186
	s_branch .LBB0_1179

; #define GAS __attribute__((address_space(1)))
; #define LAS __attribute__((address_space(3)))
; __device__ __forceinline__ unsigned pk2(float lo, float hi) { return f2bf(lo) | (f2bf(hi) << 16); }
; __device__ __forceinline__ void conv_phase(LAS unsigned char* lds, int tile, int tid, const bf16* __restrict__ U, const float* __restrict__ cw, const float* __restrict__ cb, ...
;     ...
;         for (int q = 0; q < 4; ++q) {
;             const int tk = wave * 4 + q;
;             const f32x4 a0 = *(const LAS f32x4*)(obuf + tk * CH + lane * 8), a1 = *(const LAS f32x4*)(obuf + tk * CH + lane * 8 + 4);
;             float v[8] = {a0.x, a0.y, a0.z, a0.w, a1.x, a1.y, a1.z, a1.w};
;             float s = 0.f;
; #pragma unroll
;             for (int e = 0; e < 8; ++e) s += v[e];
; #pragma unroll
;             for (int o = 1; o < 64; o <<= 1) s += __shfl_xor(s, o);
;             const float mean = s * (1.0f / CH); float sq = 0.f;
; #pragma unroll
;             for (int e = 0; e < 8; ++e) { v[e] -= mean; sq += v[e] * v[e]; }
; #pragma unroll
;             for (int o = 1; o < 64; o <<= 1) sq += __shfl_xor(sq, o);
;             const float rstd = 1.0f / sqrtf(sq * (1.0f / CH) + 1e-5f);
;             const f32x4 g0 = *(const GAS f32x4*)(cg + lane * 8), g1 = *(const GAS f32x4*)(cg + lane * 8 + 4), b0 = *(const GAS f32x4*)(cbeta + lane * 8), b1 = *(const GAS f32x4*)(cbeta + lane * 8 + 4);
;             const float gg[8] = {g0.x, g0.y, g0.z, g0.w, g1.x, g1.y, g1.z, g1.w}, bb[8] = {b0.x, b0.y, b0.z, b0.w, b1.x, b1.y, b1.z, b1.w};
;             float y[8];
; #pragma unroll
;             for (int e = 0; e < 8; ++e) { const float z = v[e] * rstd * gg[e] + bb[e]; y[e] = z * __builtin_amdgcn_rcpf(1.0f + __builtin_amdgcn_exp2f(-1.4426950408889634f * z)); }
;             v4u o; o.x = pk2(y[0], y[1]); o.y = pk2(y[2], y[3]); o.z = pk2(y[4], y[5]); o.w = pk2(y[6], y[7]);
;             *(GAS v4u*)(MIX + (size_t)(t0 + tk) * 1024 + 512 + lane * 8) = o;
;         }
.LBB0_1370:
	v_add_u32_e32 v16, s12, v67
	ds_read_b128 v[70:73], v16
	ds_read_b128 v[74:77], v16 offset:16
	s_addk_i32 s12, 0x800
	s_cmpk_eq_i32 s12, 0x2000
	s_waitcnt lgkmcnt(1)
	v_add_f32_e32 v80, 0, v70
	v_mov_b32_e32 v16, v70
	v_add_f32_e32 v70, v71, v80
	v_add_f32_e32 v70, v72, v70
	v_add_f32_e32 v70, v73, v70
	s_waitcnt lgkmcnt(0)
	v_add_f32_e32 v70, v74, v70
	v_add_f32_e32 v70, v75, v70
	v_add_f32_e32 v70, v76, v70
	v_add_f32_e32 v70, v77, v70
	v_mov_b32_e32 v17, v72
	v_mov_b32_e32 v72, v71
	v_mov_b32_e32 v78, v74
	v_mov_b32_e32 v79, v76
	v_mov_b32_e32 v76, v75
	s_nop 1
	v_add_f32_dpp v70, v70, v70 row_shr:1 row_mask:0xf bank_mask:0xf
	s_nop 1
	v_add_f32_dpp v70, v70, v70 row_shr:2 row_mask:0xf bank_mask:0xf
	s_nop 1
	v_add_f32_dpp v70, v70, v70 row_shr:4 row_mask:0xf bank_mask:0xf
	s_nop 1
	v_add_f32_dpp v70, v70, v70 row_shr:8 row_mask:0xf bank_mask:0xf
	s_nop 1
	v_add_f32_dpp v70, v70, v70 row_bcast:15 row_mask:0xa bank_mask:0xf
	s_nop 1
	v_add_f32_dpp v70, v70, v70 row_bcast:31 row_mask:0xc bank_mask:0xf
	s_nop 1
	v_readlane_b32 s98, v70, 63
	s_nop 1
	v_mov_b32_e32 v70, s98
	v_mul_f32_e32 v70, 0x3b000000, v70
	v_pk_add_f32 v[16:17], v[16:17], v[70:71] op_sel_hi:[1,0] neg_lo:[0,1] neg_hi:[0,1]
	v_pk_add_f32 v[72:73], v[72:73], v[70:71] op_sel_hi:[1,0] neg_lo:[0,1] neg_hi:[0,1]
	v_pk_add_f32 v[74:75], v[78:79], v[70:71] op_sel_hi:[1,0] neg_lo:[0,1] neg_hi:[0,1]
	v_pk_add_f32 v[70:71], v[76:77], v[70:71] op_sel_hi:[1,0] neg_lo:[0,1] neg_hi:[0,1]
	v_pk_mul_f32 v[76:77], v[16:17], v[16:17]
	v_pk_mul_f32 v[78:79], v[72:73], v[72:73]
	v_mov_b32_e32 v80, v71
	v_add_f32_e32 v76, v76, v78
	v_add_f32_e32 v76, v77, v76
	v_add_f32_e32 v76, v79, v76
	v_mov_b32_e32 v81, v75
	v_fmac_f32_e32 v76, v74, v74
	v_pk_mul_f32 v[80:81], v[80:81], v[80:81]
	v_fmac_f32_e32 v76, v70, v70
	v_add_f32_e32 v76, v81, v76
	v_add_f32_e32 v76, v80, v76
	s_nop 1
	v_add_f32_dpp v76, v76, v76 row_shr:1 row_mask:0xf bank_mask:0xf
	s_nop 1
	v_add_f32_dpp v76, v76, v76 row_shr:2 row_mask:0xf bank_mask:0xf
	s_nop 1
	v_add_f32_dpp v76, v76, v76 row_shr:4 row_mask:0xf bank_mask:0xf
	s_nop 1
	v_add_f32_dpp v76, v76, v76 row_shr:8 row_mask:0xf bank_mask:0xf
	s_nop 1
	v_add_f32_dpp v76, v76, v76 row_bcast:15 row_mask:0xa bank_mask:0xf
	s_nop 1
	v_add_f32_dpp v76, v76, v76 row_bcast:31 row_mask:0xc bank_mask:0xf
	s_nop 1
	v_readlane_b32 s98, v76, 63
	s_nop 1
	v_mov_b32_e32 v76, s98
	v_fmamk_f32 v76, v76, 0x3b000000, v68
	v_mul_f32_e32 v77, 0x4f800000, v76
	v_cmp_gt_f32_e32 vcc, s18, v76
	s_nop 1
	v_cndmask_b32_e32 v76, v76, v77, vcc
	v_sqrt_f32_e32 v77, v76
	s_nop 0
	v_add_u32_e32 v78, -1, v77
	v_add_u32_e32 v79, 1, v77
	v_fma_f32 v80, -v78, v77, v76
	v_fma_f32 v81, -v79, v77, v76
	v_cmp_ge_f32_e64 s[6:7], 0, v80
	s_nop 1
	v_cndmask_b32_e64 v77, v77, v78, s[6:7]
	v_cmp_lt_f32_e64 s[6:7], 0, v81
	s_nop 1
	v_cndmask_b32_e64 v77, v77, v79, s[6:7]
	v_mul_f32_e32 v78, 0x37800000, v77
	v_cndmask_b32_e32 v77, v77, v78, vcc
	v_cmp_class_f32_e32 vcc, v76, v69
	s_nop 1
	v_cndmask_b32_e32 v76, v77, v76, vcc
	v_div_scale_f32 v77, s[6:7], v76, v76, 1.0
	v_rcp_f32_e32 v79, v77
	v_div_scale_f32 v78, vcc, 1.0, v76, 1.0
	v_fma_f32 v80, -v77, v79, 1.0
	v_fmac_f32_e32 v79, v80, v79
	v_mul_f32_e32 v80, v78, v79
	v_fma_f32 v81, -v77, v80, v78
	v_fmac_f32_e32 v80, v81, v79
	v_fma_f32 v77, -v77, v80, v78
	v_div_fmas_f32 v77, v77, v79, v80
	v_div_fixup_f32 v76, v77, v76, 1.0
	v_pk_mul_f32 v[16:17], v[16:17], v[76:77] op_sel_hi:[1,0]
	v_pk_mul_f32 v[72:73], v[72:73], v[76:77] op_sel_hi:[1,0]
	v_pk_mul_f32 v[74:75], v[74:75], v[76:77] op_sel_hi:[1,0]
	v_pk_mul_f32 v[70:71], v[70:71], v[76:77] op_sel_hi:[1,0]
	v_pk_fma_f32 v[16:17], v[0:1], v[16:17], v[4:5]
	v_pk_fma_f32 v[72:73], v[24:25], v[72:73], v[22:23]
	v_pk_fma_f32 v[74:75], v[8:9], v[74:75], v[12:13]
	v_pk_fma_f32 v[70:71], v[6:7], v[70:71], v[2:3]
	v_mul_f32_e32 v76, 0xbfb8aa3b, v16
	v_mul_f32_e32 v77, 0xbfb8aa3b, v72
	v_mul_f32_e32 v78, 0xbfb8aa3b, v17
	v_mul_f32_e32 v79, 0xbfb8aa3b, v73
	v_mul_f32_e32 v80, 0xbfb8aa3b, v74
	v_mul_f32_e32 v81, 0xbfb8aa3b, v70
	v_mul_f32_e32 v82, 0xbfb8aa3b, v75
	v_mul_f32_e32 v83, 0xbfb8aa3b, v71
	v_exp_f32_e32 v76, v76
	v_exp_f32_e32 v77, v77
	v_exp_f32_e32 v78, v78
	v_exp_f32_e32 v79, v79
	v_exp_f32_e32 v80, v80
	v_exp_f32_e32 v81, v81
	v_exp_f32_e32 v82, v82
	v_exp_f32_e32 v83, v83
	v_add_f32_e32 v76, 1.0, v76
	v_add_f32_e32 v77, 1.0, v77
	v_add_f32_e32 v84, 1.0, v78
	v_add_f32_e32 v79, 1.0, v79
	v_add_f32_e32 v80, 1.0, v80
	v_add_f32_e32 v81, 1.0, v81
	v_add_f32_e32 v85, 1.0, v82
	v_add_f32_e32 v83, 1.0, v83
	v_rcp_f32_e32 v76, v76
	v_rcp_f32_e32 v78, v77
	v_rcp_f32_e32 v77, v84
	v_rcp_f32_e32 v79, v79
	v_rcp_f32_e32 v80, v80
	v_rcp_f32_e32 v82, v81
	v_rcp_f32_e32 v81, v85
	v_rcp_f32_e32 v83, v83
	v_pk_mul_f32 v[16:17], v[16:17], v[76:77]
	v_pk_mul_f32 v[72:73], v[72:73], v[78:79]
	v_pk_mul_f32 v[74:75], v[74:75], v[80:81]
	v_pk_mul_f32 v[70:71], v[70:71], v[82:83]
	v_bfe_u32 v78, v73, 16, 1
	v_bfe_u32 v79, v72, 16, 1
	v_bfe_u32 v80, v16, 16, 1
	v_bfe_u32 v81, v17, 16, 1
	v_bfe_u32 v82, v74, 16, 1
	v_bfe_u32 v83, v75, 16, 1
	v_bfe_u32 v76, v71, 16, 1
	v_bfe_u32 v77, v70, 16, 1
	v_add3_u32 v79, v72, v79, s19
	v_add3_u32 v78, v73, v78, s19
	v_add3_u32 v72, v75, v83, s19
	v_add3_u32 v73, v74, v82, s19
	v_add3_u32 v17, v17, v81, s19
	v_add3_u32 v16, v16, v80, s19
	v_add3_u32 v70, v70, v77, s19
	v_add3_u32 v71, v71, v76, s19
	v_lshrrev_b32_e32 v16, 16, v16
	v_lshrrev_b32_e32 v17, 16, v17
	v_lshrrev_b32_e32 v74, 16, v73
	v_lshrrev_b32_e32 v72, 16, v72
	v_and_or_b32 v73, v71, s20, v72
	v_and_or_b32 v72, v70, s20, v74
	v_and_or_b32 v71, v78, s20, v17
	v_and_or_b32 v70, v79, s20, v16
	global_store_dwordx4 v[14:15], v[70:73], off sc1
	v_lshl_add_u64 v[14:15], v[14:15], 0, s[8:9]
	s_cbranch_scc0 .LBB0_1370
; __device__ __forceinline__ int mk_lane() { int l_ = (int)__builtin_amdgcn_mbcnt_hi(~0u, __builtin_amdgcn_mbcnt_lo(~0u, 0u)); asm volatile("" : "+v"(l_)); return l_; }
; #define BOTH(k) (IN(k) && IN((k) + 1))
; __device__ __forceinline__ void xcd_barrier(const XcdBarrier& b, int wave_id, int pair = -1) {
;     asm volatile("s_waitcnt vmcnt(0)" ::: "memory");
;     __syncthreads();
;     if (wave_id == 0 && mk_lane() == 0) {
;         unsigned* bar = b.bar;
;         __builtin_amdgcn_s_waitcnt(0);
;         unsigned nloc = b.st[0], nx = b.st[1];
;         if (nloc == 0u) { xcd_barrier_complete(bar, b.x, nloc, nx); b.st[0] = nloc; b.st[1] = nx; }
; template <int K> __device__ __forceinline__ void run_phase(Frame& F, const XcdBarrier& bar, int lo, int hi, unsigned char* lds) {
;     ...
;         if (BOTH(k)) {
;             constexpr bool LOCAL_SEAM = MK_LOCALBAR && (sub == 2 || (sub == 6 && l == 0));
;             bool local = false;
;             if (LOCAL_SEAM) local = __hip_atomic_load((unsigned*)(F.ctl + CW_LBAR + 24 * 64), __ATOMIC_RELAXED, __HIP_MEMORY_SCOPE_AGENT) == 0u;
;             constexpr bool PAIR_SEAM = MK_LOCALBAR && (sub == 0 || sub == 1);
;             bool pairok = false;
;             if (PAIR_SEAM) pairok = __hip_atomic_load((unsigned*)(F.ctl + CW_LBAR + 24 * 64), __ATOMIC_RELAXED, __HIP_MEMORY_SCOPE_AGENT) == 0u;
;             if (local) xcd_local_barrier((unsigned*)(F.ctl + CW_LBAR + ((sub == 2 ? l : 2) * 8 + (bx & 7)) * 64), (unsigned)(G >> 3), (unsigned*)(F.ctl + CW_BAR) + XB_TMO, F.wave);
;             else xcd_barrier(bar, F.wave, pairok ? ((bx & 7) >> 1) : -1);
	s_mov_b32 s21, 32
	s_mov_b64 s[6:7], 0
	s_and_b64 vcc, exec, s[10:11]
	s_cbranch_vccz .LBB0_1364
	s_cmp_lt_i32 s41, 11
	s_barrier
	s_cbranch_scc1 .LBB0_1429
	v_mov_b32_e32 v0, 0x31000
	global_load_dword v0, v0, s[30:31] offset:2048 sc1
	s_waitcnt vmcnt(0)
	s_andn2_b64 vcc, exec, s[38:39]
	s_barrier
	s_cbranch_vccnz .LBB0_1428
	s_nop 0
	v_cmp_eq_u32_e32 vcc, 0, v194
	s_and_saveexec_b64 s[6:7], vcc
	s_cbranch_execz .LBB0_1427
	s_add_i32 s4, 0, 0x27f60
	v_mov_b32_e32 v1, s4
	s_waitcnt vmcnt(0) expcnt(0) lgkmcnt(0)
	ds_read_b32 v3, v1
	s_add_i32 s4, 0, 0x27f64
	v_mov_b32_e32 v1, s4
	ds_read_b32 v1, v1
	s_waitcnt lgkmcnt(1)
	v_cmp_ne_u32_e32 vcc, 0, v3
	s_cbranch_vccnz .LBB0_1391
	v_readlane_b32 s4, v248, 0
	v_readlane_b32 s5, v248, 1
	s_load_dwordx2 s[10:11], s[4:5], 0x4
	s_add_u32 s4, s30, 0x4200
	s_addc_u32 s5, s31, 0
	s_add_u32 s8, s30, 0x4400
	s_addc_u32 s9, s31, 0
	s_waitcnt lgkmcnt(0)
	s_mul_i32 s58, s10, s60
	s_add_u32 s10, s30, 0x4500
	s_mul_i32 s58, s58, s11
	s_addc_u32 s11, s31, 0
	s_add_u32 s12, s30, 0x4600
	s_addc_u32 s13, s31, 0
	s_add_u32 s14, s30, 0x4700
	s_addc_u32 s15, s31, 0
	s_add_u32 s16, s30, 0x4800
	s_addc_u32 s17, s31, 0
	s_add_u32 s18, s30, 0x4900
	s_addc_u32 s19, s31, 0
	s_add_u32 s20, s30, 0x4a00
	s_addc_u32 s21, s31, 0
	s_add_u32 s22, s30, 0x4b00
	s_addc_u32 s23, s31, 0
	s_add_u32 s24, s30, 0x4c00
	s_addc_u32 s25, s31, 0
	s_add_u32 s26, s30, 0x4d00
	s_addc_u32 s27, s31, 0
	s_add_u32 s28, s30, 0x4e00
	s_addc_u32 s29, s31, 0
	s_add_u32 s42, s30, 0x4f00
	s_addc_u32 s43, s31, 0
	s_add_u32 s44, s30, 0x5000
	s_addc_u32 s45, s31, 0
	s_add_u32 s46, s30, 0x5100
	s_addc_u32 s47, s31, 0
	s_add_u32 s48, s30, 0x5200
	s_addc_u32 s49, s31, 0
	s_add_u32 s50, s30, 0x5300
	s_addc_u32 s51, s31, 0
	s_mov_b32 s59, 1
	v_mov_b32_e32 v17, 0
	s_branch .LBB0_1378
